# GEMM: first two K-loop vmcnt waits of a tile that follows an epilogue relaxed to 8+stores (the epilogue stores are younger than the loads these waits protect), flag in s100; on top of c4
# baseline (speedup 1.0000x reference)
.LBB0_395:
	v_mov_b32_e32 v133, v161
	v_lshl_add_u64 v[6:7], s[30:31], 0, v[132:133]
	v_mov_b32_e32 v129, v161
	v_readlane_b32 s20, v253, 59
	v_lshl_add_u64 v[8:9], s[30:31], 0, v[128:129]
	v_mov_b32_e32 v135, v161
	v_readlane_b32 s21, v253, 60
	s_add_i32 m0, s43, 0x18000
	v_lshl_add_u64 v[6:7], v[6:7], 0, s[54:55]
	v_lshl_add_u64 v[10:11], s[20:21], 0, v[134:135]
	v_mov_b32_e32 v131, v161
	s_and_b32 s12, s10, 3
	s_lshl_b32 s13, s9, 6
	s_mov_b32 s100, 0
	s_waitcnt vmcnt(2)
	s_barrier
	global_load_lds_dwordx4 v[6:7], off
	v_lshl_add_u64 v[6:7], v[8:9], 0, s[54:55]
	s_add_i32 m0, s43, 0x1a000
	s_add_i32 s57, s43, 0x8000
	s_add_i32 s58, s43, 0xa000
	v_lshl_add_u64 v[12:13], s[20:21], 0, v[130:131]
	global_load_lds_dwordx4 v[6:7], off
	v_lshl_add_u64 v[6:7], v[10:11], 0, s[54:55]
	s_mov_b32 m0, s57
	s_add_u32 s10, s30, 0x20080
	global_load_lds_dwordx4 v[6:7], off
	v_lshl_add_u64 v[6:7], v[12:13], 0, s[54:55]
	s_mov_b32 m0, s58
	s_addc_u32 s11, s31, 0
	global_load_lds_dwordx4 v[6:7], off
	s_add_i32 m0, s43, 0x1c000
	v_lshl_add_u64 v[6:7], s[10:11], 0, v[132:133]
	global_load_lds_dwordx4 v[6:7], off
	v_lshl_add_u64 v[6:7], s[10:11], 0, v[128:129]
	s_add_i32 m0, s43, 0x1e000
	s_cmpk_lt_u32 s8, 0x100
	global_load_lds_dwordx4 v[6:7], off
	s_cselect_b64 s[10:11], -1, 0
	s_lshl_b32 s8, s9, 13
	v_and_b32_e32 v5, 7, v0
	v_bfe_u32 v16, v0, 1, 3
	s_lshl_b32 s9, s12, 11
	s_add_i32 s8, s8, 0
	v_and_b32_e32 v14, 15, v0
	v_bitop3_b32 v16, v3, v16, 3 bitop3:0x6c
	s_add_i32 s8, s8, s9
	v_bfe_u32 v6, v0, 3, 3
	v_bitop3_b32 v3, v3, v5, 3 bitop3:0x6c
	v_or_b32_e32 v15, s13, v14
	v_lshlrev_b32_e32 v16, 4, v16
	v_lshlrev_b32_e32 v18, 7, v14
	s_add_i32 s8, s8, 0x20000
	v_cmp_gt_u32_e32 vcc, 8, v14
	v_lshlrev_b32_e32 v8, 7, v6
	v_lshlrev_b32_e32 v3, 4, v3
	v_and_b32_e32 v0, 4, v0
	v_lshlrev_b32_e32 v15, 7, v15
	s_waitcnt vmcnt(6)
	v_add3_u32 v141, s8, v18, v16
	v_cndmask_b32_e64 v7, v224, 64, vcc
	v_add3_u32 v142, s8, v8, v3
	v_cmp_eq_u32_e32 vcc, 0, v0
	s_lshl_b32 s8, s12, 6
	v_or_b32_e32 v17, v15, v16
	v_lshl_or_b32 v19, s12, 12, v18
	v_cndmask_b32_e64 v3, v224, 64, vcc
	v_lshlrev_b32_e32 v0, 3, v5
	v_bitop3_b32 v5, v15, 64, v16 bitop3:0x36
	s_lshl_b32 s80, s8, 1
	v_readlane_b32 s8, v253, 57
	v_or_b32_e32 v140, v19, v16
	s_mov_b32 s59, 0
	v_or_b32_e32 v143, s13, v6
	v_bitop3_b32 v144, v19, 64, v16 bitop3:0x36
	v_add_u32_e32 v136, v4, v1
	v_mov_b32_e32 v137, v161
	v_add_u32_e32 v138, v2, v1
	v_mov_b32_e32 v139, v161
	v_add_u32_e32 v145, 0, v17
	v_add_u32_e32 v146, 0, v5
	v_lshlrev_b32_e32 v160, 1, v0
	v_add_u32_e32 v147, v141, v7
	v_add_u32_e32 v148, v142, v3
	v_readlane_b32 s70, v254, 47
	s_mov_b32 s71, s8
	s_barrier
	v_readlane_b32 s9, v253, 58
	s_branch .LBB0_398

.LBB0_401:
	s_add_u32 s30, s20, 0xfff80080
	s_addc_u32 s31, s21, -1
	s_add_i32 s65, 0, 0x10000
	s_cmp_eq_u32 s84, 28
	v_add_u32_e32 v149, s65, v140
	v_add_u32_e32 v154, s65, v144
	s_cselect_b32 s35, s15, s31
	s_cselect_b32 s34, s72, s30
	ds_read_b128 v[150:153], v149
	ds_read_b128 v[154:157], v154
	v_add_u32_e32 v149, s1, v140
	s_cselect_b32 s31, s13, s77
	s_cselect_b32 s30, s73, s76
	s_add_i32 s90, 0, 0x14000
	v_add_u32_e32 v158, s1, v144
	ds_read_b128 v[166:169], v149
	ds_read_b128 v[170:173], v158
	v_add_u32_e32 v149, s90, v140
	v_add_u32_e32 v158, s90, v144
	ds_read_b128 v[174:177], v149
	ds_read_b128 v[178:181], v158
	v_add_u32_e32 v149, s86, v140
	v_add_u32_e32 v158, s86, v144
	ds_read_b128 v[182:185], v149
	ds_read_b128 v[186:189], v158
	v_lshl_add_u64 v[158:159], s[20:21], 0, v[136:137]
	s_add_i32 m0, s43, 0xc000
	ds_read_b128 v[190:193], v145
	ds_read_b128 v[194:197], v145 offset:2048
	ds_read_b128 v[198:201], v146
	ds_read_b128 v[202:205], v146 offset:2048
	ds_read_b128 v[206:209], v145 offset:4096
	ds_read_b128 v[210:213], v145 offset:6144
	ds_read_b128 v[214:217], v146 offset:4096
	ds_read_b128 v[226:229], v146 offset:6144
	global_load_lds_dwordx4 v[158:159], off
	v_lshl_add_u64 v[158:159], s[20:21], 0, v[138:139]
	s_add_i32 m0, s43, 0xe000
	s_nop 0
	global_load_lds_dwordx4 v[158:159], off
	s_waitcnt vmcnt(24)
	s_cmp_lg_u32 s100, 0
	s_cbranch_scc1 .Lgrx_1
	s_waitcnt vmcnt(8)
.Lgrx_1:
	s_waitcnt lgkmcnt(0)
	s_barrier
	s_setprio 1
	s_waitcnt lgkmcnt(0)
	v_mfma_f32_16x16x32_bf16 v[124:127], v[150:153], v[190:193], v[124:127]
	v_mfma_f32_16x16x32_bf16 v[120:123], v[166:169], v[190:193], v[120:123]
	v_mfma_f32_16x16x32_bf16 v[116:119], v[150:153], v[194:197], v[116:119]
	v_mfma_f32_16x16x32_bf16 v[112:115], v[166:169], v[194:197], v[112:115]
	v_mfma_f32_16x16x32_bf16 v[100:103], v[150:153], v[206:209], v[100:103]
	v_mfma_f32_16x16x32_bf16 v[96:99], v[166:169], v[206:209], v[96:99]
	v_mfma_f32_16x16x32_bf16 v[84:87], v[150:153], v[210:213], v[84:87]
	v_mfma_f32_16x16x32_bf16 v[76:79], v[166:169], v[210:213], v[76:79]
	v_mfma_f32_16x16x32_bf16 v[124:127], v[154:157], v[198:201], v[124:127]
	v_mfma_f32_16x16x32_bf16 v[120:123], v[170:173], v[198:201], v[120:123]
	v_mfma_f32_16x16x32_bf16 v[116:119], v[154:157], v[202:205], v[116:119]
	v_mfma_f32_16x16x32_bf16 v[112:115], v[170:173], v[202:205], v[112:115]
	v_mfma_f32_16x16x32_bf16 v[100:103], v[154:157], v[214:217], v[100:103]
	v_mfma_f32_16x16x32_bf16 v[96:99], v[170:173], v[214:217], v[96:99]
	v_mfma_f32_16x16x32_bf16 v[84:87], v[154:157], v[226:229], v[84:87]
	v_mfma_f32_16x16x32_bf16 v[76:79], v[170:173], v[226:229], v[76:79]
	s_setprio 0
	s_setprio 1
	v_mfma_f32_16x16x32_bf16 v[108:111], v[174:177], v[190:193], v[108:111]
	v_mfma_f32_16x16x32_bf16 v[104:107], v[182:185], v[190:193], v[104:107]
	v_mfma_f32_16x16x32_bf16 v[92:95], v[174:177], v[194:197], v[92:95]
	v_mfma_f32_16x16x32_bf16 v[88:91], v[182:185], v[194:197], v[88:91]
	v_mfma_f32_16x16x32_bf16 v[80:83], v[174:177], v[206:209], v[80:83]
	v_mfma_f32_16x16x32_bf16 v[72:75], v[182:185], v[206:209], v[72:75]
	v_mfma_f32_16x16x32_bf16 v[68:71], v[174:177], v[210:213], v[68:71]
	v_mfma_f32_16x16x32_bf16 v[64:67], v[182:185], v[210:213], v[64:67]
	v_mfma_f32_16x16x32_bf16 v[108:111], v[178:181], v[198:201], v[108:111]
	v_mfma_f32_16x16x32_bf16 v[104:107], v[186:189], v[198:201], v[104:107]
	v_mfma_f32_16x16x32_bf16 v[92:95], v[178:181], v[202:205], v[92:95]
	v_mfma_f32_16x16x32_bf16 v[88:91], v[186:189], v[202:205], v[88:91]
	v_mfma_f32_16x16x32_bf16 v[80:83], v[178:181], v[214:217], v[80:83]
	v_mfma_f32_16x16x32_bf16 v[72:75], v[186:189], v[214:217], v[72:75]
	v_mfma_f32_16x16x32_bf16 v[68:71], v[178:181], v[226:229], v[68:71]
	v_mfma_f32_16x16x32_bf16 v[64:67], v[186:189], v[226:229], v[64:67]
	s_setprio 0
	s_barrier
	s_add_i32 s65, s65, s41
	v_lshl_add_u64 v[158:159], s[30:31], 0, v[132:133]
	s_mov_b32 m0, s65
	ds_read_b128 v[190:193], v145 offset:16384
	ds_read_b128 v[194:197], v145 offset:18432
	ds_read_b128 v[198:201], v146 offset:16384
	ds_read_b128 v[202:205], v146 offset:18432
	ds_read_b128 v[206:209], v145 offset:20480
	ds_read_b128 v[210:213], v145 offset:22528
	ds_read_b128 v[214:217], v146 offset:20480
	ds_read_b128 v[226:229], v146 offset:22528
	global_load_lds_dwordx4 v[158:159], off
	s_add_i32 m0, s65, 0x2000
	s_add_u32 s88, s30, 0x20000
	v_lshl_add_u64 v[218:219], s[30:31], 0, v[128:129]
	s_addc_u32 s89, s31, 0
	s_add_i32 s65, s90, s41
	global_load_lds_dwordx4 v[218:219], off
	v_lshl_add_u64 v[230:231], s[88:89], 0, v[132:133]
	s_mov_b32 m0, s65
	v_lshl_add_u64 v[232:233], s[34:35], 0, v[130:131]
	global_load_lds_dwordx4 v[230:231], off
	v_lshl_add_u64 v[230:231], s[88:89], 0, v[128:129]
	s_add_i32 m0, s65, 0x2000
	s_nop 0
	global_load_lds_dwordx4 v[230:231], off
	v_lshl_add_u64 v[230:231], s[34:35], 0, v[134:135]
	s_mov_b32 m0, s43
	s_nop 0
	global_load_lds_dwordx4 v[230:231], off
	s_mov_b32 m0, s46
	s_nop 0
	global_load_lds_dwordx4 v[232:233], off
	s_waitcnt vmcnt(24)
	s_cmp_lg_u32 s100, 0
	s_cbranch_scc1 .Lgrx_2
	s_waitcnt vmcnt(8)
.Lgrx_2:
	s_mov_b32 s100, 0
	s_waitcnt lgkmcnt(0)
	s_barrier
	s_setprio 1
	s_waitcnt lgkmcnt(0)
	v_mfma_f32_16x16x32_bf16 v[60:63], v[150:153], v[190:193], v[60:63]
	v_mfma_f32_16x16x32_bf16 v[56:59], v[166:169], v[190:193], v[56:59]
	v_mfma_f32_16x16x32_bf16 v[52:55], v[150:153], v[194:197], v[52:55]
	v_mfma_f32_16x16x32_bf16 v[44:47], v[166:169], v[194:197], v[44:47]
	v_mfma_f32_16x16x32_bf16 v[36:39], v[150:153], v[206:209], v[36:39]
	v_mfma_f32_16x16x32_bf16 v[28:31], v[166:169], v[206:209], v[28:31]
	v_mfma_f32_16x16x32_bf16 v[20:23], v[150:153], v[210:213], v[20:23]
	v_mfma_f32_16x16x32_bf16 v[12:15], v[166:169], v[210:213], v[12:15]
	v_mfma_f32_16x16x32_bf16 v[60:63], v[154:157], v[198:201], v[60:63]
	v_mfma_f32_16x16x32_bf16 v[56:59], v[170:173], v[198:201], v[56:59]
	v_mfma_f32_16x16x32_bf16 v[52:55], v[154:157], v[202:205], v[52:55]
	v_mfma_f32_16x16x32_bf16 v[44:47], v[170:173], v[202:205], v[44:47]
	v_mfma_f32_16x16x32_bf16 v[36:39], v[154:157], v[214:217], v[36:39]
	v_mfma_f32_16x16x32_bf16 v[28:31], v[170:173], v[214:217], v[28:31]
	v_mfma_f32_16x16x32_bf16 v[20:23], v[154:157], v[226:229], v[20:23]
	v_mfma_f32_16x16x32_bf16 v[12:15], v[170:173], v[226:229], v[12:15]
	s_setprio 0
	s_setprio 1
	v_mfma_f32_16x16x32_bf16 v[48:51], v[174:177], v[190:193], v[48:51]
	v_mfma_f32_16x16x32_bf16 v[40:43], v[182:185], v[190:193], v[40:43]
	v_mfma_f32_16x16x32_bf16 v[32:35], v[174:177], v[194:197], v[32:35]
	v_mfma_f32_16x16x32_bf16 v[24:27], v[182:185], v[194:197], v[24:27]
	v_mfma_f32_16x16x32_bf16 v[16:19], v[174:177], v[206:209], v[16:19]
	v_mfma_f32_16x16x32_bf16 v[8:11], v[182:185], v[206:209], v[8:11]
	v_mfma_f32_16x16x32_bf16 v[4:7], v[174:177], v[210:213], v[4:7]
	v_mfma_f32_16x16x32_bf16 v[0:3], v[182:185], v[210:213], v[0:3]
	v_mfma_f32_16x16x32_bf16 v[48:51], v[178:181], v[198:201], v[48:51]
	v_mfma_f32_16x16x32_bf16 v[40:43], v[186:189], v[198:201], v[40:43]
	v_mfma_f32_16x16x32_bf16 v[32:35], v[178:181], v[202:205], v[32:35]
	v_mfma_f32_16x16x32_bf16 v[24:27], v[186:189], v[202:205], v[24:27]
	v_mfma_f32_16x16x32_bf16 v[16:19], v[178:181], v[214:217], v[16:19]
	v_mfma_f32_16x16x32_bf16 v[8:11], v[186:189], v[214:217], v[8:11]
	v_mfma_f32_16x16x32_bf16 v[4:7], v[178:181], v[226:229], v[4:7]
	v_mfma_f32_16x16x32_bf16 v[0:3], v[186:189], v[226:229], v[0:3]
	s_setprio 0
	s_barrier
	s_add_i32 s65, 0, 0x18000
	v_add_u32_e32 v149, s65, v140
	v_add_u32_e32 v154, s65, v144
	ds_read_b128 v[150:153], v149
	ds_read_b128 v[154:157], v154
	v_add_u32_e32 v149, s87, v140
	s_add_i32 s88, 0, 0x1c000
	v_add_u32_e32 v162, s87, v144
	ds_read_b128 v[166:169], v149
	ds_read_b128 v[170:173], v162
	v_add_u32_e32 v149, s88, v140
	v_add_u32_e32 v162, s88, v144
	ds_read_b128 v[174:177], v149
	ds_read_b128 v[178:181], v162
	v_add_u32_e32 v149, s2, v140
	v_add_u32_e32 v162, s2, v144
	ds_read_b128 v[182:185], v149
	ds_read_b128 v[186:189], v162
	s_add_u32 s34, s34, 0x80000
	s_addc_u32 s35, s35, 0
	s_mov_b32 m0, s47
	v_lshl_add_u64 v[234:235], s[34:35], 0, v[134:135]
	ds_read_b128 v[190:193], v145 offset:32768
	ds_read_b128 v[194:197], v145 offset:34816
	ds_read_b128 v[198:201], v146 offset:32768
	ds_read_b128 v[202:205], v146 offset:34816
	ds_read_b128 v[206:209], v145 offset:36864
	ds_read_b128 v[210:213], v145 offset:38912
	ds_read_b128 v[214:217], v146 offset:36864
	ds_read_b128 v[226:229], v146 offset:38912
	global_load_lds_dwordx4 v[234:235], off
	v_lshl_add_u64 v[234:235], s[34:35], 0, v[130:131]
	s_mov_b32 m0, s56
	s_nop 0
	global_load_lds_dwordx4 v[234:235], off
	s_waitcnt vmcnt(8)
	s_waitcnt lgkmcnt(0)
	s_barrier
	s_setprio 1
	s_waitcnt lgkmcnt(0)
	v_mfma_f32_16x16x32_bf16 v[124:127], v[150:153], v[190:193], v[124:127]
	v_mfma_f32_16x16x32_bf16 v[120:123], v[166:169], v[190:193], v[120:123]
	v_mfma_f32_16x16x32_bf16 v[116:119], v[150:153], v[194:197], v[116:119]
	v_mfma_f32_16x16x32_bf16 v[112:115], v[166:169], v[194:197], v[112:115]
	v_mfma_f32_16x16x32_bf16 v[100:103], v[150:153], v[206:209], v[100:103]
	v_mfma_f32_16x16x32_bf16 v[96:99], v[166:169], v[206:209], v[96:99]
	v_mfma_f32_16x16x32_bf16 v[84:87], v[150:153], v[210:213], v[84:87]
	v_mfma_f32_16x16x32_bf16 v[76:79], v[166:169], v[210:213], v[76:79]
	v_mfma_f32_16x16x32_bf16 v[124:127], v[154:157], v[198:201], v[124:127]
	v_mfma_f32_16x16x32_bf16 v[120:123], v[170:173], v[198:201], v[120:123]
	v_mfma_f32_16x16x32_bf16 v[116:119], v[154:157], v[202:205], v[116:119]
	v_mfma_f32_16x16x32_bf16 v[112:115], v[170:173], v[202:205], v[112:115]
	v_mfma_f32_16x16x32_bf16 v[100:103], v[154:157], v[214:217], v[100:103]
	v_mfma_f32_16x16x32_bf16 v[96:99], v[170:173], v[214:217], v[96:99]
	v_mfma_f32_16x16x32_bf16 v[84:87], v[154:157], v[226:229], v[84:87]
	v_mfma_f32_16x16x32_bf16 v[76:79], v[170:173], v[226:229], v[76:79]
	s_setprio 0
	s_setprio 1
	v_mfma_f32_16x16x32_bf16 v[108:111], v[174:177], v[190:193], v[108:111]
	v_mfma_f32_16x16x32_bf16 v[104:107], v[182:185], v[190:193], v[104:107]
	v_mfma_f32_16x16x32_bf16 v[92:95], v[174:177], v[194:197], v[92:95]
	v_mfma_f32_16x16x32_bf16 v[88:91], v[182:185], v[194:197], v[88:91]
	v_mfma_f32_16x16x32_bf16 v[80:83], v[174:177], v[206:209], v[80:83]
	v_mfma_f32_16x16x32_bf16 v[72:75], v[182:185], v[206:209], v[72:75]
	v_mfma_f32_16x16x32_bf16 v[68:71], v[174:177], v[210:213], v[68:71]
	v_mfma_f32_16x16x32_bf16 v[64:67], v[182:185], v[210:213], v[64:67]
	v_mfma_f32_16x16x32_bf16 v[108:111], v[178:181], v[198:201], v[108:111]
	v_mfma_f32_16x16x32_bf16 v[104:107], v[186:189], v[198:201], v[104:107]
	v_mfma_f32_16x16x32_bf16 v[92:95], v[178:181], v[202:205], v[92:95]
	v_mfma_f32_16x16x32_bf16 v[88:91], v[186:189], v[202:205], v[88:91]
	v_mfma_f32_16x16x32_bf16 v[80:83], v[178:181], v[214:217], v[80:83]
	v_mfma_f32_16x16x32_bf16 v[72:75], v[186:189], v[214:217], v[72:75]
	v_mfma_f32_16x16x32_bf16 v[68:71], v[178:181], v[226:229], v[68:71]
	v_mfma_f32_16x16x32_bf16 v[64:67], v[186:189], v[226:229], v[64:67]
	s_setprio 0
	s_barrier
	s_add_i32 s34, s65, s41
	v_lshl_add_u64 v[158:159], v[158:159], 0, s[54:55]
	s_mov_b32 m0, s34
	ds_read_b128 v[190:193], v145 offset:49152
	ds_read_b128 v[194:197], v145 offset:51200
	ds_read_b128 v[198:201], v146 offset:49152
	ds_read_b128 v[202:205], v146 offset:51200
	ds_read_b128 v[206:209], v145 offset:53248
	ds_read_b128 v[210:213], v145 offset:55296
	ds_read_b128 v[214:217], v146 offset:53248
	ds_read_b128 v[226:229], v146 offset:55296
	global_load_lds_dwordx4 v[158:159], off
	s_add_i32 m0, s34, 0x2000
	s_add_u32 s30, s30, 0x20080
	v_lshl_add_u64 v[158:159], v[218:219], 0, s[54:55]
	s_addc_u32 s31, s31, 0
	s_add_i32 s34, s88, s41
	global_load_lds_dwordx4 v[158:159], off
	v_lshl_add_u64 v[158:159], s[30:31], 0, v[132:133]
	s_mov_b32 m0, s34
	s_nop 0
	global_load_lds_dwordx4 v[158:159], off
	v_lshl_add_u64 v[158:159], s[30:31], 0, v[128:129]
	s_add_i32 m0, s34, 0x2000
	s_nop 0
	global_load_lds_dwordx4 v[158:159], off
	v_lshl_add_u64 v[158:159], v[230:231], 0, s[54:55]
	s_mov_b32 m0, s57
	s_nop 0
	global_load_lds_dwordx4 v[158:159], off
	v_lshl_add_u64 v[158:159], v[232:233], 0, s[54:55]
	s_mov_b32 m0, s58
	s_nop 0
	global_load_lds_dwordx4 v[158:159], off
	s_waitcnt vmcnt(8)
	s_waitcnt lgkmcnt(0)
	s_barrier
	s_setprio 1
	s_waitcnt lgkmcnt(0)
	v_mfma_f32_16x16x32_bf16 v[60:63], v[150:153], v[190:193], v[60:63]
	v_mfma_f32_16x16x32_bf16 v[56:59], v[166:169], v[190:193], v[56:59]
	v_mfma_f32_16x16x32_bf16 v[52:55], v[150:153], v[194:197], v[52:55]
	v_mfma_f32_16x16x32_bf16 v[44:47], v[166:169], v[194:197], v[44:47]
	v_mfma_f32_16x16x32_bf16 v[36:39], v[150:153], v[206:209], v[36:39]
	v_mfma_f32_16x16x32_bf16 v[28:31], v[166:169], v[206:209], v[28:31]
	v_mfma_f32_16x16x32_bf16 v[20:23], v[150:153], v[210:213], v[20:23]
	v_mfma_f32_16x16x32_bf16 v[12:15], v[166:169], v[210:213], v[12:15]
	v_mfma_f32_16x16x32_bf16 v[60:63], v[154:157], v[198:201], v[60:63]
	v_mfma_f32_16x16x32_bf16 v[56:59], v[170:173], v[198:201], v[56:59]
	v_mfma_f32_16x16x32_bf16 v[52:55], v[154:157], v[202:205], v[52:55]
	v_mfma_f32_16x16x32_bf16 v[44:47], v[170:173], v[202:205], v[44:47]
	v_mfma_f32_16x16x32_bf16 v[36:39], v[154:157], v[214:217], v[36:39]
	v_mfma_f32_16x16x32_bf16 v[28:31], v[170:173], v[214:217], v[28:31]
	v_mfma_f32_16x16x32_bf16 v[20:23], v[154:157], v[226:229], v[20:23]
	v_mfma_f32_16x16x32_bf16 v[12:15], v[170:173], v[226:229], v[12:15]
	s_setprio 0
	s_setprio 1
	v_mfma_f32_16x16x32_bf16 v[48:51], v[174:177], v[190:193], v[48:51]
	v_mfma_f32_16x16x32_bf16 v[40:43], v[182:185], v[190:193], v[40:43]
	v_mfma_f32_16x16x32_bf16 v[32:35], v[174:177], v[194:197], v[32:35]
	v_mfma_f32_16x16x32_bf16 v[24:27], v[182:185], v[194:197], v[24:27]
	v_mfma_f32_16x16x32_bf16 v[16:19], v[174:177], v[206:209], v[16:19]
	v_mfma_f32_16x16x32_bf16 v[8:11], v[182:185], v[206:209], v[8:11]
	v_mfma_f32_16x16x32_bf16 v[4:7], v[174:177], v[210:213], v[4:7]
	v_mfma_f32_16x16x32_bf16 v[0:3], v[182:185], v[210:213], v[0:3]
	v_mfma_f32_16x16x32_bf16 v[48:51], v[178:181], v[198:201], v[48:51]
	v_mfma_f32_16x16x32_bf16 v[40:43], v[186:189], v[198:201], v[40:43]
	v_mfma_f32_16x16x32_bf16 v[32:35], v[178:181], v[202:205], v[32:35]
	v_mfma_f32_16x16x32_bf16 v[24:27], v[186:189], v[202:205], v[24:27]
	v_mfma_f32_16x16x32_bf16 v[16:19], v[178:181], v[214:217], v[16:19]
	v_mfma_f32_16x16x32_bf16 v[8:11], v[186:189], v[214:217], v[8:11]
	v_mfma_f32_16x16x32_bf16 v[4:7], v[178:181], v[226:229], v[4:7]
	v_mfma_f32_16x16x32_bf16 v[0:3], v[186:189], v[226:229], v[0:3]
	s_setprio 0
	s_barrier
	s_add_i32 s84, s84, 2
	s_add_u32 s20, s20, 0x100
	s_addc_u32 s21, s21, 0
	s_add_u32 s76, s76, 0x100
	s_addc_u32 s77, s77, 0
	s_cmp_gt_u32 s84, 29
	s_cbranch_scc0 .LBB0_401
	s_mov_b32 s100, 1
	s_and_b64 vcc, exec, s[10:11]
	s_cbranch_vccz .LBB0_404
	s_barrier

.LBB0_495:
	v_mov_b32_e32 v133, v161
	v_lshl_add_u64 v[6:7], s[34:35], 0, v[132:133]
	v_mov_b32_e32 v129, v161
	v_readlane_b32 s30, v254, 1
	v_lshl_add_u64 v[8:9], s[34:35], 0, v[128:129]
	v_mov_b32_e32 v135, v161
	v_readlane_b32 s31, v254, 2
	s_add_i32 m0, s47, 0x18000
	v_lshl_add_u64 v[6:7], v[6:7], 0, s[54:55]
	v_lshl_add_u64 v[10:11], s[30:31], 0, v[134:135]
	v_mov_b32_e32 v131, v161
	s_and_b32 s14, s12, 3
	s_lshl_b32 s15, s9, 6
	s_mov_b32 s100, 0
	s_waitcnt vmcnt(2)
	s_barrier
	global_load_lds_dwordx4 v[6:7], off
	v_lshl_add_u64 v[6:7], v[8:9], 0, s[54:55]
	s_add_i32 m0, s47, 0x1a000
	s_add_i32 s59, s47, 0x8000
	s_add_i32 s70, s47, 0xa000
	v_lshl_add_u64 v[12:13], s[30:31], 0, v[130:131]
	global_load_lds_dwordx4 v[6:7], off
	v_lshl_add_u64 v[6:7], v[10:11], 0, s[54:55]
	s_mov_b32 m0, s59
	s_add_u32 s12, s34, 0x20080
	global_load_lds_dwordx4 v[6:7], off
	v_lshl_add_u64 v[6:7], v[12:13], 0, s[54:55]
	s_mov_b32 m0, s70
	s_addc_u32 s13, s35, 0
	global_load_lds_dwordx4 v[6:7], off
	s_add_i32 m0, s47, 0x1c000
	v_lshl_add_u64 v[6:7], s[12:13], 0, v[132:133]
	global_load_lds_dwordx4 v[6:7], off
	v_lshl_add_u64 v[6:7], s[12:13], 0, v[128:129]
	s_add_i32 m0, s47, 0x1e000
	s_cmpk_lt_u32 s8, 0x100
	global_load_lds_dwordx4 v[6:7], off
	s_cselect_b64 s[12:13], -1, 0
	s_lshl_b32 s8, s9, 13
	v_and_b32_e32 v5, 7, v0
	v_bfe_u32 v16, v0, 1, 3
	s_lshl_b32 s9, s14, 11
	s_add_i32 s8, s8, 0
	v_and_b32_e32 v14, 15, v0
	v_bitop3_b32 v16, v3, v16, 3 bitop3:0x6c
	s_add_i32 s8, s8, s9
	v_bfe_u32 v6, v0, 3, 3
	v_bitop3_b32 v3, v3, v5, 3 bitop3:0x6c
	v_or_b32_e32 v15, s15, v14
	v_lshlrev_b32_e32 v16, 4, v16
	v_lshlrev_b32_e32 v18, 7, v14
	s_add_i32 s8, s8, 0x20000
	v_cmp_gt_u32_e32 vcc, 8, v14
	v_lshlrev_b32_e32 v8, 7, v6
	v_lshlrev_b32_e32 v3, 4, v3
	v_and_b32_e32 v0, 4, v0
	v_lshlrev_b32_e32 v15, 7, v15
	s_waitcnt vmcnt(6)
	v_add3_u32 v141, s8, v18, v16
	v_cndmask_b32_e64 v7, v224, 64, vcc
	v_add3_u32 v142, s8, v8, v3
	v_cmp_eq_u32_e32 vcc, 0, v0
	s_lshl_b32 s8, s14, 6
	v_or_b32_e32 v17, v15, v16
	v_lshl_or_b32 v19, s14, 12, v18
	v_cndmask_b32_e64 v3, v224, 64, vcc
	v_lshlrev_b32_e32 v0, 3, v5
	v_bitop3_b32 v5, v15, 64, v16 bitop3:0x36
	s_lshl_b32 s80, s8, 1
	v_readlane_b32 s8, v254, 31
	v_or_b32_e32 v140, v19, v16
	s_mov_b32 s71, 0
	v_or_b32_e32 v143, s15, v6
	v_bitop3_b32 v144, v19, 64, v16 bitop3:0x36
	v_add_u32_e32 v136, v4, v1
	v_mov_b32_e32 v137, v161
	v_add_u32_e32 v138, v2, v1
	v_mov_b32_e32 v139, v161
	v_add_u32_e32 v145, 0, v17
	v_add_u32_e32 v146, 0, v5
	v_lshlrev_b32_e32 v160, 1, v0
	v_add_u32_e32 v147, v141, v7
	v_add_u32_e32 v148, v142, v3
	v_readlane_b32 s72, v254, 48
	s_mov_b32 s73, s8
	s_barrier
	v_readlane_b32 s9, v254, 32
	s_branch .LBB0_498

.LBB0_501:
	s_add_u32 s34, s30, 0xfff80080
	s_addc_u32 s35, s31, -1
	s_add_i32 s65, 0, 0x10000
	s_cmp_eq_u32 s89, 28
	v_add_u32_e32 v149, s65, v140
	v_add_u32_e32 v154, s65, v144
	s_cselect_b32 s37, s17, s35
	s_cselect_b32 s36, s76, s34
	ds_read_b128 v[150:153], v149
	ds_read_b128 v[154:157], v154
	v_add_u32_e32 v149, s1, v140
	s_cselect_b32 s35, s15, s88
	s_cselect_b32 s34, s77, s84
	s_add_i32 s94, 0, 0x14000
	v_add_u32_e32 v158, s1, v144
	ds_read_b128 v[166:169], v149
	ds_read_b128 v[170:173], v158
	v_add_u32_e32 v149, s94, v140
	v_add_u32_e32 v158, s94, v144
	ds_read_b128 v[174:177], v149
	ds_read_b128 v[178:181], v158
	v_add_u32_e32 v149, s86, v140
	v_add_u32_e32 v158, s86, v144
	ds_read_b128 v[182:185], v149
	ds_read_b128 v[186:189], v158
	v_lshl_add_u64 v[158:159], s[30:31], 0, v[136:137]
	s_add_i32 m0, s47, 0xc000
	ds_read_b128 v[190:193], v145
	ds_read_b128 v[194:197], v145 offset:2048
	ds_read_b128 v[198:201], v146
	ds_read_b128 v[202:205], v146 offset:2048
	ds_read_b128 v[206:209], v145 offset:4096
	ds_read_b128 v[210:213], v145 offset:6144
	ds_read_b128 v[214:217], v146 offset:4096
	ds_read_b128 v[226:229], v146 offset:6144
	global_load_lds_dwordx4 v[158:159], off
	v_lshl_add_u64 v[158:159], s[30:31], 0, v[138:139]
	s_add_i32 m0, s47, 0xe000
	s_nop 0
	global_load_lds_dwordx4 v[158:159], off
	s_waitcnt vmcnt(24)
	s_cmp_lg_u32 s100, 0
	s_cbranch_scc1 .Lgrx_3
	s_waitcnt vmcnt(8)
.Lgrx_3:
	s_waitcnt lgkmcnt(0)
	s_barrier
	s_setprio 1
	s_waitcnt lgkmcnt(0)
	v_mfma_f32_16x16x32_bf16 v[124:127], v[150:153], v[190:193], v[124:127]
	v_mfma_f32_16x16x32_bf16 v[120:123], v[166:169], v[190:193], v[120:123]
	v_mfma_f32_16x16x32_bf16 v[116:119], v[150:153], v[194:197], v[116:119]
	v_mfma_f32_16x16x32_bf16 v[112:115], v[166:169], v[194:197], v[112:115]
	v_mfma_f32_16x16x32_bf16 v[100:103], v[150:153], v[206:209], v[100:103]
	v_mfma_f32_16x16x32_bf16 v[96:99], v[166:169], v[206:209], v[96:99]
	v_mfma_f32_16x16x32_bf16 v[84:87], v[150:153], v[210:213], v[84:87]
	v_mfma_f32_16x16x32_bf16 v[76:79], v[166:169], v[210:213], v[76:79]
	v_mfma_f32_16x16x32_bf16 v[124:127], v[154:157], v[198:201], v[124:127]
	v_mfma_f32_16x16x32_bf16 v[120:123], v[170:173], v[198:201], v[120:123]
	v_mfma_f32_16x16x32_bf16 v[116:119], v[154:157], v[202:205], v[116:119]
	v_mfma_f32_16x16x32_bf16 v[112:115], v[170:173], v[202:205], v[112:115]
	v_mfma_f32_16x16x32_bf16 v[100:103], v[154:157], v[214:217], v[100:103]
	v_mfma_f32_16x16x32_bf16 v[96:99], v[170:173], v[214:217], v[96:99]
	v_mfma_f32_16x16x32_bf16 v[84:87], v[154:157], v[226:229], v[84:87]
	v_mfma_f32_16x16x32_bf16 v[76:79], v[170:173], v[226:229], v[76:79]
	s_setprio 0
	s_setprio 1
	v_mfma_f32_16x16x32_bf16 v[108:111], v[174:177], v[190:193], v[108:111]
	v_mfma_f32_16x16x32_bf16 v[104:107], v[182:185], v[190:193], v[104:107]
	v_mfma_f32_16x16x32_bf16 v[92:95], v[174:177], v[194:197], v[92:95]
	v_mfma_f32_16x16x32_bf16 v[88:91], v[182:185], v[194:197], v[88:91]
	v_mfma_f32_16x16x32_bf16 v[80:83], v[174:177], v[206:209], v[80:83]
	v_mfma_f32_16x16x32_bf16 v[72:75], v[182:185], v[206:209], v[72:75]
	v_mfma_f32_16x16x32_bf16 v[68:71], v[174:177], v[210:213], v[68:71]
	v_mfma_f32_16x16x32_bf16 v[64:67], v[182:185], v[210:213], v[64:67]
	v_mfma_f32_16x16x32_bf16 v[108:111], v[178:181], v[198:201], v[108:111]
	v_mfma_f32_16x16x32_bf16 v[104:107], v[186:189], v[198:201], v[104:107]
	v_mfma_f32_16x16x32_bf16 v[92:95], v[178:181], v[202:205], v[92:95]
	v_mfma_f32_16x16x32_bf16 v[88:91], v[186:189], v[202:205], v[88:91]
	v_mfma_f32_16x16x32_bf16 v[80:83], v[178:181], v[214:217], v[80:83]
	v_mfma_f32_16x16x32_bf16 v[72:75], v[186:189], v[214:217], v[72:75]
	v_mfma_f32_16x16x32_bf16 v[68:71], v[178:181], v[226:229], v[68:71]
	v_mfma_f32_16x16x32_bf16 v[64:67], v[186:189], v[226:229], v[64:67]
	s_setprio 0
	s_barrier
	s_add_i32 s65, s65, s46
	v_lshl_add_u64 v[158:159], s[34:35], 0, v[132:133]
	s_mov_b32 m0, s65
	ds_read_b128 v[190:193], v145 offset:16384
	ds_read_b128 v[194:197], v145 offset:18432
	ds_read_b128 v[198:201], v146 offset:16384
	ds_read_b128 v[202:205], v146 offset:18432
	ds_read_b128 v[206:209], v145 offset:20480
	ds_read_b128 v[210:213], v145 offset:22528
	ds_read_b128 v[214:217], v146 offset:20480
	ds_read_b128 v[226:229], v146 offset:22528
	global_load_lds_dwordx4 v[158:159], off
	s_add_i32 m0, s65, 0x2000
	s_add_u32 s90, s34, 0x20000
	v_lshl_add_u64 v[218:219], s[34:35], 0, v[128:129]
	s_addc_u32 s91, s35, 0
	s_add_i32 s65, s94, s46
	global_load_lds_dwordx4 v[218:219], off
	v_lshl_add_u64 v[230:231], s[90:91], 0, v[132:133]
	s_mov_b32 m0, s65
	v_lshl_add_u64 v[232:233], s[36:37], 0, v[130:131]
	global_load_lds_dwordx4 v[230:231], off
	v_lshl_add_u64 v[230:231], s[90:91], 0, v[128:129]
	s_add_i32 m0, s65, 0x2000
	s_nop 0
	global_load_lds_dwordx4 v[230:231], off
	v_lshl_add_u64 v[230:231], s[36:37], 0, v[134:135]
	s_mov_b32 m0, s47
	s_nop 0
	global_load_lds_dwordx4 v[230:231], off
	s_mov_b32 m0, s56
	s_nop 0
	global_load_lds_dwordx4 v[232:233], off
	s_waitcnt vmcnt(24)
	s_cmp_lg_u32 s100, 0
	s_cbranch_scc1 .Lgrx_4
	s_waitcnt vmcnt(8)
.Lgrx_4:
	s_mov_b32 s100, 0
	s_waitcnt lgkmcnt(0)
	s_barrier
	s_setprio 1
	s_waitcnt lgkmcnt(0)
	v_mfma_f32_16x16x32_bf16 v[60:63], v[150:153], v[190:193], v[60:63]
	v_mfma_f32_16x16x32_bf16 v[56:59], v[166:169], v[190:193], v[56:59]
	v_mfma_f32_16x16x32_bf16 v[52:55], v[150:153], v[194:197], v[52:55]
	v_mfma_f32_16x16x32_bf16 v[44:47], v[166:169], v[194:197], v[44:47]
	v_mfma_f32_16x16x32_bf16 v[36:39], v[150:153], v[206:209], v[36:39]
	v_mfma_f32_16x16x32_bf16 v[28:31], v[166:169], v[206:209], v[28:31]
	v_mfma_f32_16x16x32_bf16 v[20:23], v[150:153], v[210:213], v[20:23]
	v_mfma_f32_16x16x32_bf16 v[12:15], v[166:169], v[210:213], v[12:15]
	v_mfma_f32_16x16x32_bf16 v[60:63], v[154:157], v[198:201], v[60:63]
	v_mfma_f32_16x16x32_bf16 v[56:59], v[170:173], v[198:201], v[56:59]
	v_mfma_f32_16x16x32_bf16 v[52:55], v[154:157], v[202:205], v[52:55]
	v_mfma_f32_16x16x32_bf16 v[44:47], v[170:173], v[202:205], v[44:47]
	v_mfma_f32_16x16x32_bf16 v[36:39], v[154:157], v[214:217], v[36:39]
	v_mfma_f32_16x16x32_bf16 v[28:31], v[170:173], v[214:217], v[28:31]
	v_mfma_f32_16x16x32_bf16 v[20:23], v[154:157], v[226:229], v[20:23]
	v_mfma_f32_16x16x32_bf16 v[12:15], v[170:173], v[226:229], v[12:15]
	s_setprio 0
	s_setprio 1
	v_mfma_f32_16x16x32_bf16 v[48:51], v[174:177], v[190:193], v[48:51]
	v_mfma_f32_16x16x32_bf16 v[40:43], v[182:185], v[190:193], v[40:43]
	v_mfma_f32_16x16x32_bf16 v[32:35], v[174:177], v[194:197], v[32:35]
	v_mfma_f32_16x16x32_bf16 v[24:27], v[182:185], v[194:197], v[24:27]
	v_mfma_f32_16x16x32_bf16 v[16:19], v[174:177], v[206:209], v[16:19]
	v_mfma_f32_16x16x32_bf16 v[8:11], v[182:185], v[206:209], v[8:11]
	v_mfma_f32_16x16x32_bf16 v[4:7], v[174:177], v[210:213], v[4:7]
	v_mfma_f32_16x16x32_bf16 v[0:3], v[182:185], v[210:213], v[0:3]
	v_mfma_f32_16x16x32_bf16 v[48:51], v[178:181], v[198:201], v[48:51]
	v_mfma_f32_16x16x32_bf16 v[40:43], v[186:189], v[198:201], v[40:43]
	v_mfma_f32_16x16x32_bf16 v[32:35], v[178:181], v[202:205], v[32:35]
	v_mfma_f32_16x16x32_bf16 v[24:27], v[186:189], v[202:205], v[24:27]
	v_mfma_f32_16x16x32_bf16 v[16:19], v[178:181], v[214:217], v[16:19]
	v_mfma_f32_16x16x32_bf16 v[8:11], v[186:189], v[214:217], v[8:11]
	v_mfma_f32_16x16x32_bf16 v[4:7], v[178:181], v[226:229], v[4:7]
	v_mfma_f32_16x16x32_bf16 v[0:3], v[186:189], v[226:229], v[0:3]
	s_setprio 0
	s_barrier
	s_add_i32 s65, 0, 0x18000
	v_add_u32_e32 v149, s65, v140
	v_add_u32_e32 v154, s65, v144
	ds_read_b128 v[150:153], v149
	ds_read_b128 v[154:157], v154
	v_add_u32_e32 v149, s87, v140
	s_add_i32 s90, 0, 0x1c000
	v_add_u32_e32 v162, s87, v144
	ds_read_b128 v[166:169], v149
	ds_read_b128 v[170:173], v162
	v_add_u32_e32 v149, s90, v140
	v_add_u32_e32 v162, s90, v144
	ds_read_b128 v[174:177], v149
	ds_read_b128 v[178:181], v162
	v_add_u32_e32 v149, s2, v140
	v_add_u32_e32 v162, s2, v144
	ds_read_b128 v[182:185], v149
	ds_read_b128 v[186:189], v162
	s_add_u32 s36, s36, 0x80000
	s_addc_u32 s37, s37, 0
	s_mov_b32 m0, s57
	v_lshl_add_u64 v[234:235], s[36:37], 0, v[134:135]
	ds_read_b128 v[190:193], v145 offset:32768
	ds_read_b128 v[194:197], v145 offset:34816
	ds_read_b128 v[198:201], v146 offset:32768
	ds_read_b128 v[202:205], v146 offset:34816
	ds_read_b128 v[206:209], v145 offset:36864
	ds_read_b128 v[210:213], v145 offset:38912
	ds_read_b128 v[214:217], v146 offset:36864
	ds_read_b128 v[226:229], v146 offset:38912
	global_load_lds_dwordx4 v[234:235], off
	v_lshl_add_u64 v[234:235], s[36:37], 0, v[130:131]
	s_mov_b32 m0, s58
	s_nop 0
	global_load_lds_dwordx4 v[234:235], off
	s_waitcnt vmcnt(8)
	s_waitcnt lgkmcnt(0)
	s_barrier
	s_setprio 1
	s_waitcnt lgkmcnt(0)
	v_mfma_f32_16x16x32_bf16 v[124:127], v[150:153], v[190:193], v[124:127]
	v_mfma_f32_16x16x32_bf16 v[120:123], v[166:169], v[190:193], v[120:123]
	v_mfma_f32_16x16x32_bf16 v[116:119], v[150:153], v[194:197], v[116:119]
	v_mfma_f32_16x16x32_bf16 v[112:115], v[166:169], v[194:197], v[112:115]
	v_mfma_f32_16x16x32_bf16 v[100:103], v[150:153], v[206:209], v[100:103]
	v_mfma_f32_16x16x32_bf16 v[96:99], v[166:169], v[206:209], v[96:99]
	v_mfma_f32_16x16x32_bf16 v[84:87], v[150:153], v[210:213], v[84:87]
	v_mfma_f32_16x16x32_bf16 v[76:79], v[166:169], v[210:213], v[76:79]
	v_mfma_f32_16x16x32_bf16 v[124:127], v[154:157], v[198:201], v[124:127]
	v_mfma_f32_16x16x32_bf16 v[120:123], v[170:173], v[198:201], v[120:123]
	v_mfma_f32_16x16x32_bf16 v[116:119], v[154:157], v[202:205], v[116:119]
	v_mfma_f32_16x16x32_bf16 v[112:115], v[170:173], v[202:205], v[112:115]
	v_mfma_f32_16x16x32_bf16 v[100:103], v[154:157], v[214:217], v[100:103]
	v_mfma_f32_16x16x32_bf16 v[96:99], v[170:173], v[214:217], v[96:99]
	v_mfma_f32_16x16x32_bf16 v[84:87], v[154:157], v[226:229], v[84:87]
	v_mfma_f32_16x16x32_bf16 v[76:79], v[170:173], v[226:229], v[76:79]
	s_setprio 0
	s_setprio 1
	v_mfma_f32_16x16x32_bf16 v[108:111], v[174:177], v[190:193], v[108:111]
	v_mfma_f32_16x16x32_bf16 v[104:107], v[182:185], v[190:193], v[104:107]
	v_mfma_f32_16x16x32_bf16 v[92:95], v[174:177], v[194:197], v[92:95]
	v_mfma_f32_16x16x32_bf16 v[88:91], v[182:185], v[194:197], v[88:91]
	v_mfma_f32_16x16x32_bf16 v[80:83], v[174:177], v[206:209], v[80:83]
	v_mfma_f32_16x16x32_bf16 v[72:75], v[182:185], v[206:209], v[72:75]
	v_mfma_f32_16x16x32_bf16 v[68:71], v[174:177], v[210:213], v[68:71]
	v_mfma_f32_16x16x32_bf16 v[64:67], v[182:185], v[210:213], v[64:67]
	v_mfma_f32_16x16x32_bf16 v[108:111], v[178:181], v[198:201], v[108:111]
	v_mfma_f32_16x16x32_bf16 v[104:107], v[186:189], v[198:201], v[104:107]
	v_mfma_f32_16x16x32_bf16 v[92:95], v[178:181], v[202:205], v[92:95]
	v_mfma_f32_16x16x32_bf16 v[88:91], v[186:189], v[202:205], v[88:91]
	v_mfma_f32_16x16x32_bf16 v[80:83], v[178:181], v[214:217], v[80:83]
	v_mfma_f32_16x16x32_bf16 v[72:75], v[186:189], v[214:217], v[72:75]
	v_mfma_f32_16x16x32_bf16 v[68:71], v[178:181], v[226:229], v[68:71]
	v_mfma_f32_16x16x32_bf16 v[64:67], v[186:189], v[226:229], v[64:67]
	s_setprio 0
	s_barrier
	s_add_i32 s36, s65, s46
	v_lshl_add_u64 v[158:159], v[158:159], 0, s[54:55]
	s_mov_b32 m0, s36
	ds_read_b128 v[190:193], v145 offset:49152
	ds_read_b128 v[194:197], v145 offset:51200
	ds_read_b128 v[198:201], v146 offset:49152
	ds_read_b128 v[202:205], v146 offset:51200
	ds_read_b128 v[206:209], v145 offset:53248
	ds_read_b128 v[210:213], v145 offset:55296
	ds_read_b128 v[214:217], v146 offset:53248
	ds_read_b128 v[226:229], v146 offset:55296
	global_load_lds_dwordx4 v[158:159], off
	s_add_i32 m0, s36, 0x2000
	s_add_u32 s34, s34, 0x20080
	v_lshl_add_u64 v[158:159], v[218:219], 0, s[54:55]
	s_addc_u32 s35, s35, 0
	s_add_i32 s36, s90, s46
	global_load_lds_dwordx4 v[158:159], off
	v_lshl_add_u64 v[158:159], s[34:35], 0, v[132:133]
	s_mov_b32 m0, s36
	s_nop 0
	global_load_lds_dwordx4 v[158:159], off
	v_lshl_add_u64 v[158:159], s[34:35], 0, v[128:129]
	s_add_i32 m0, s36, 0x2000
	s_nop 0
	global_load_lds_dwordx4 v[158:159], off
	v_lshl_add_u64 v[158:159], v[230:231], 0, s[54:55]
	s_mov_b32 m0, s59
	s_nop 0
	global_load_lds_dwordx4 v[158:159], off
	v_lshl_add_u64 v[158:159], v[232:233], 0, s[54:55]
	s_mov_b32 m0, s70
	s_nop 0
	global_load_lds_dwordx4 v[158:159], off
	s_waitcnt vmcnt(8)
	s_waitcnt lgkmcnt(0)
	s_barrier
	s_setprio 1
	s_waitcnt lgkmcnt(0)
	v_mfma_f32_16x16x32_bf16 v[60:63], v[150:153], v[190:193], v[60:63]
	v_mfma_f32_16x16x32_bf16 v[56:59], v[166:169], v[190:193], v[56:59]
	v_mfma_f32_16x16x32_bf16 v[52:55], v[150:153], v[194:197], v[52:55]
	v_mfma_f32_16x16x32_bf16 v[44:47], v[166:169], v[194:197], v[44:47]
	v_mfma_f32_16x16x32_bf16 v[36:39], v[150:153], v[206:209], v[36:39]
	v_mfma_f32_16x16x32_bf16 v[28:31], v[166:169], v[206:209], v[28:31]
	v_mfma_f32_16x16x32_bf16 v[20:23], v[150:153], v[210:213], v[20:23]
	v_mfma_f32_16x16x32_bf16 v[12:15], v[166:169], v[210:213], v[12:15]
	v_mfma_f32_16x16x32_bf16 v[60:63], v[154:157], v[198:201], v[60:63]
	v_mfma_f32_16x16x32_bf16 v[56:59], v[170:173], v[198:201], v[56:59]
	v_mfma_f32_16x16x32_bf16 v[52:55], v[154:157], v[202:205], v[52:55]
	v_mfma_f32_16x16x32_bf16 v[44:47], v[170:173], v[202:205], v[44:47]
	v_mfma_f32_16x16x32_bf16 v[36:39], v[154:157], v[214:217], v[36:39]
	v_mfma_f32_16x16x32_bf16 v[28:31], v[170:173], v[214:217], v[28:31]
	v_mfma_f32_16x16x32_bf16 v[20:23], v[154:157], v[226:229], v[20:23]
	v_mfma_f32_16x16x32_bf16 v[12:15], v[170:173], v[226:229], v[12:15]
	s_setprio 0
	s_setprio 1
	v_mfma_f32_16x16x32_bf16 v[48:51], v[174:177], v[190:193], v[48:51]
	v_mfma_f32_16x16x32_bf16 v[40:43], v[182:185], v[190:193], v[40:43]
	v_mfma_f32_16x16x32_bf16 v[32:35], v[174:177], v[194:197], v[32:35]
	v_mfma_f32_16x16x32_bf16 v[24:27], v[182:185], v[194:197], v[24:27]
	v_mfma_f32_16x16x32_bf16 v[16:19], v[174:177], v[206:209], v[16:19]
	v_mfma_f32_16x16x32_bf16 v[8:11], v[182:185], v[206:209], v[8:11]
	v_mfma_f32_16x16x32_bf16 v[4:7], v[174:177], v[210:213], v[4:7]
	v_mfma_f32_16x16x32_bf16 v[0:3], v[182:185], v[210:213], v[0:3]
	v_mfma_f32_16x16x32_bf16 v[48:51], v[178:181], v[198:201], v[48:51]
	v_mfma_f32_16x16x32_bf16 v[40:43], v[186:189], v[198:201], v[40:43]
	v_mfma_f32_16x16x32_bf16 v[32:35], v[178:181], v[202:205], v[32:35]
	v_mfma_f32_16x16x32_bf16 v[24:27], v[186:189], v[202:205], v[24:27]
	v_mfma_f32_16x16x32_bf16 v[16:19], v[178:181], v[214:217], v[16:19]
	v_mfma_f32_16x16x32_bf16 v[8:11], v[186:189], v[214:217], v[8:11]
	v_mfma_f32_16x16x32_bf16 v[4:7], v[178:181], v[226:229], v[4:7]
	v_mfma_f32_16x16x32_bf16 v[0:3], v[186:189], v[226:229], v[0:3]
	s_setprio 0
	s_barrier
	s_add_i32 s89, s89, 2
	s_add_u32 s30, s30, 0x100
	s_addc_u32 s31, s31, 0
	s_add_u32 s84, s84, 0x100
	s_addc_u32 s88, s88, 0
	s_cmp_gt_u32 s89, 29
	s_cbranch_scc0 .LBB0_501
	s_mov_b32 s100, 1
	s_and_b64 vcc, exec, s[12:13]
	s_cbranch_vccz .LBB0_504
	s_barrier

.LBB0_547:
	v_mov_b32_e32 v131, v161
	v_lshl_add_u64 v[4:5], s[20:21], 0, v[130:131]
	v_mov_b32_e32 v129, v161
	v_readlane_b32 s18, v253, 42
	v_lshl_add_u64 v[6:7], s[20:21], 0, v[128:129]
	v_readlane_b32 s19, v253, 43
	s_and_b32 s10, s8, 3
	s_add_i32 m0, s37, 0x18000
	v_lshl_add_u64 v[4:5], v[4:5], 0, s[54:55]
	v_lshl_add_u64 v[8:9], s[18:19], 0, v[130:131]
	s_lshl_b32 s11, s7, 6
	s_lshl_b32 s12, s10, 5
	s_mov_b32 s100, 0
	s_waitcnt vmcnt(2)
	s_barrier
	global_load_lds_dwordx4 v[4:5], off
	v_lshl_add_u64 v[4:5], v[6:7], 0, s[54:55]
	s_add_i32 m0, s37, 0x1a000
	s_add_i32 s47, s37, 0x8000
	s_add_i32 s56, s37, 0xa000
	v_lshl_add_u64 v[10:11], s[18:19], 0, v[128:129]
	global_load_lds_dwordx4 v[4:5], off
	v_lshl_add_u64 v[4:5], v[8:9], 0, s[54:55]
	s_mov_b32 m0, s47
	s_add_u32 s8, s20, 0x80080
	global_load_lds_dwordx4 v[4:5], off
	v_lshl_add_u64 v[4:5], v[10:11], 0, s[54:55]
	s_mov_b32 m0, s56
	s_addc_u32 s9, s21, 0
	global_load_lds_dwordx4 v[4:5], off
	s_add_i32 m0, s37, 0x1c000
	v_lshl_add_u64 v[4:5], s[8:9], 0, v[130:131]
	global_load_lds_dwordx4 v[4:5], off
	v_lshl_add_u64 v[4:5], s[8:9], 0, v[128:129]
	s_add_i32 m0, s37, 0x1e000
	s_cmpk_lt_u32 s6, 0x100
	global_load_lds_dwordx4 v[4:5], off
	s_cselect_b64 s[8:9], -1, 0
	s_lshl_b32 s6, s7, 13
	v_lshrrev_b32_e32 v4, 4, v0
	v_bfe_u32 v7, v0, 1, 3
	s_lshl_b32 s7, s10, 11
	s_add_i32 s6, s6, 0
	v_and_b32_e32 v5, 15, v0
	v_bitop3_b32 v7, v4, v7, 3 bitop3:0x6c
	s_add_i32 s6, s6, s7
	v_and_b32_e32 v11, 7, v0
	v_or_b32_e32 v6, s11, v5
	v_lshlrev_b32_e32 v7, 4, v7
	s_add_i32 s6, s6, 0x20000
	v_bfe_u32 v10, v0, 3, 3
	v_lshlrev_b32_e32 v12, 7, v5
	v_cmp_gt_u32_e32 vcc, 8, v5
	v_bitop3_b32 v4, v4, v11, 3 bitop3:0x6c
	v_and_b32_e32 v0, 4, v0
	v_lshlrev_b32_e32 v6, 7, v6
	v_or_b32_e32 v9, s12, v5
	s_waitcnt vmcnt(6)
	v_add3_u32 v137, s6, v12, v7
	v_cndmask_b32_e64 v5, v224, 64, vcc
	v_lshlrev_b32_e32 v12, 7, v10
	v_lshlrev_b32_e32 v4, 4, v4
	v_cmp_eq_u32_e32 vcc, 0, v0
	v_or_b32_e32 v8, v6, v7
	v_lshlrev_b32_e32 v9, 7, v9
	v_add3_u32 v138, s6, v12, v4
	v_cndmask_b32_e64 v4, v224, 64, vcc
	v_lshlrev_b32_e32 v0, 2, v11
	v_bitop3_b32 v6, v6, 64, v7 bitop3:0x36
	v_readlane_b32 s6, v253, 40
	v_or_b32_e32 v136, v9, v7
	s_mov_b32 s57, 0
	v_or_b32_e32 v139, s11, v10
	v_bitop3_b32 v140, v9, 64, v7 bitop3:0x36
	v_add_u32_e32 v132, v2, v3
	v_mov_b32_e32 v133, v161
	v_add_u32_e32 v134, v1, v3
	v_mov_b32_e32 v135, v161
	v_add_u32_e32 v141, 0, v8
	v_add_u32_e32 v142, 0, v6
	s_lshl_b32 s80, s12, 2
	v_lshlrev_b32_e32 v160, 2, v0
	v_add_u32_e32 v143, v137, v5
	v_add_u32_e32 v144, v138, v4
	v_readlane_b32 s58, v253, 37
	s_mov_b32 s59, s6
	s_barrier
	v_readlane_b32 s7, v253, 41
	s_branch .LBB0_550

.LBB0_557:
	s_add_u32 s20, s18, 0xfff80080
	s_addc_u32 s21, s19, -1
	s_add_i32 s65, 0, 0x10000
	s_cmp_eq_u32 s76, 28
	v_add_u32_e32 v145, s65, v136
	v_add_u32_e32 v150, s65, v140
	s_cselect_b32 s31, s13, s21
	s_cselect_b32 s30, s70, s20
	ds_read_b128 v[146:149], v145
	ds_read_b128 v[150:153], v150
	v_add_u32_e32 v145, s1, v136
	s_cselect_b32 s21, s11, s73
	s_cselect_b32 s20, s71, s72
	s_add_i32 s77, 0, 0x14000
	v_add_u32_e32 v158, s1, v140
	ds_read_b128 v[154:157], v145
	ds_read_b128 v[166:169], v158
	v_add_u32_e32 v145, s77, v136
	v_add_u32_e32 v158, s77, v140
	ds_read_b128 v[170:173], v145
	ds_read_b128 v[174:177], v158
	v_add_u32_e32 v145, s86, v136
	v_add_u32_e32 v158, s86, v140
	ds_read_b128 v[178:181], v145
	ds_read_b128 v[182:185], v158
	v_lshl_add_u64 v[158:159], s[18:19], 0, v[132:133]
	s_add_i32 m0, s37, 0xc000
	ds_read_b128 v[186:189], v141
	ds_read_b128 v[190:193], v141 offset:2048
	ds_read_b128 v[194:197], v142
	ds_read_b128 v[198:201], v142 offset:2048
	ds_read_b128 v[202:205], v141 offset:4096
	ds_read_b128 v[206:209], v141 offset:6144
	ds_read_b128 v[210:213], v142 offset:4096
	ds_read_b128 v[214:217], v142 offset:6144
	global_load_lds_dwordx4 v[158:159], off
	v_lshl_add_u64 v[158:159], s[18:19], 0, v[134:135]
	s_add_i32 m0, s37, 0xe000
	s_nop 0
	global_load_lds_dwordx4 v[158:159], off
	s_waitcnt vmcnt(40)
	s_cmp_lg_u32 s100, 0
	s_cbranch_scc1 .Lgrx_5
	s_waitcnt vmcnt(8)
.Lgrx_5:
	s_waitcnt lgkmcnt(0)
	s_barrier
	s_setprio 1
	s_waitcnt lgkmcnt(0)
	v_mfma_f32_16x16x32_bf16 v[124:127], v[146:149], v[186:189], v[124:127]
	v_mfma_f32_16x16x32_bf16 v[120:123], v[154:157], v[186:189], v[120:123]
	v_mfma_f32_16x16x32_bf16 v[116:119], v[146:149], v[190:193], v[116:119]
	v_mfma_f32_16x16x32_bf16 v[112:115], v[154:157], v[190:193], v[112:115]
	v_mfma_f32_16x16x32_bf16 v[100:103], v[146:149], v[202:205], v[100:103]
	v_mfma_f32_16x16x32_bf16 v[96:99], v[154:157], v[202:205], v[96:99]
	v_mfma_f32_16x16x32_bf16 v[84:87], v[146:149], v[206:209], v[84:87]
	v_mfma_f32_16x16x32_bf16 v[80:83], v[154:157], v[206:209], v[80:83]
	v_mfma_f32_16x16x32_bf16 v[124:127], v[150:153], v[194:197], v[124:127]
	v_mfma_f32_16x16x32_bf16 v[120:123], v[166:169], v[194:197], v[120:123]
	v_mfma_f32_16x16x32_bf16 v[116:119], v[150:153], v[198:201], v[116:119]
	v_mfma_f32_16x16x32_bf16 v[112:115], v[166:169], v[198:201], v[112:115]
	v_mfma_f32_16x16x32_bf16 v[100:103], v[150:153], v[210:213], v[100:103]
	v_mfma_f32_16x16x32_bf16 v[96:99], v[166:169], v[210:213], v[96:99]
	v_mfma_f32_16x16x32_bf16 v[84:87], v[150:153], v[214:217], v[84:87]
	v_mfma_f32_16x16x32_bf16 v[80:83], v[166:169], v[214:217], v[80:83]
	s_setprio 0
	s_setprio 1
	v_mfma_f32_16x16x32_bf16 v[108:111], v[170:173], v[186:189], v[108:111]
	v_mfma_f32_16x16x32_bf16 v[104:107], v[178:181], v[186:189], v[104:107]
	v_mfma_f32_16x16x32_bf16 v[92:95], v[170:173], v[190:193], v[92:95]
	v_mfma_f32_16x16x32_bf16 v[88:91], v[178:181], v[190:193], v[88:91]
	v_mfma_f32_16x16x32_bf16 v[76:79], v[170:173], v[202:205], v[76:79]
	v_mfma_f32_16x16x32_bf16 v[72:75], v[178:181], v[202:205], v[72:75]
	v_mfma_f32_16x16x32_bf16 v[68:71], v[170:173], v[206:209], v[68:71]
	v_mfma_f32_16x16x32_bf16 v[64:67], v[178:181], v[206:209], v[64:67]
	v_mfma_f32_16x16x32_bf16 v[108:111], v[174:177], v[194:197], v[108:111]
	v_mfma_f32_16x16x32_bf16 v[104:107], v[182:185], v[194:197], v[104:107]
	v_mfma_f32_16x16x32_bf16 v[92:95], v[174:177], v[198:201], v[92:95]
	v_mfma_f32_16x16x32_bf16 v[88:91], v[182:185], v[198:201], v[88:91]
	v_mfma_f32_16x16x32_bf16 v[76:79], v[174:177], v[210:213], v[76:79]
	v_mfma_f32_16x16x32_bf16 v[72:75], v[182:185], v[210:213], v[72:75]
	v_mfma_f32_16x16x32_bf16 v[68:71], v[174:177], v[214:217], v[68:71]
	v_mfma_f32_16x16x32_bf16 v[64:67], v[182:185], v[214:217], v[64:67]
	s_setprio 0
	s_barrier
	s_add_i32 s65, s65, s36
	v_lshl_add_u64 v[158:159], s[20:21], 0, v[130:131]
	s_mov_b32 m0, s65
	ds_read_b128 v[186:189], v141 offset:16384
	ds_read_b128 v[190:193], v141 offset:18432
	ds_read_b128 v[194:197], v142 offset:16384
	ds_read_b128 v[198:201], v142 offset:18432
	ds_read_b128 v[202:205], v141 offset:20480
	ds_read_b128 v[206:209], v141 offset:22528
	ds_read_b128 v[210:213], v142 offset:20480
	ds_read_b128 v[214:217], v142 offset:22528
	global_load_lds_dwordx4 v[158:159], off
	s_add_i32 m0, s65, 0x2000
	s_add_u32 s88, s20, 0x80000
	v_lshl_add_u64 v[218:219], s[20:21], 0, v[128:129]
	s_addc_u32 s89, s21, 0
	s_add_i32 s65, s77, s36
	global_load_lds_dwordx4 v[218:219], off
	v_lshl_add_u64 v[226:227], s[88:89], 0, v[130:131]
	s_mov_b32 m0, s65
	v_lshl_add_u64 v[228:229], s[30:31], 0, v[128:129]
	global_load_lds_dwordx4 v[226:227], off
	v_lshl_add_u64 v[226:227], s[88:89], 0, v[128:129]
	s_add_i32 m0, s65, 0x2000
	s_nop 0
	global_load_lds_dwordx4 v[226:227], off
	v_lshl_add_u64 v[226:227], s[30:31], 0, v[130:131]
	s_mov_b32 m0, s37
	s_nop 0
	global_load_lds_dwordx4 v[226:227], off
	s_mov_b32 m0, s41
	s_nop 0
	global_load_lds_dwordx4 v[228:229], off
	s_waitcnt vmcnt(40)
	s_cmp_lg_u32 s100, 0
	s_cbranch_scc1 .Lgrx_6
	s_waitcnt vmcnt(8)
.Lgrx_6:
	s_mov_b32 s100, 0
	s_waitcnt lgkmcnt(0)
	s_barrier
	s_setprio 1
	s_waitcnt lgkmcnt(0)
	v_mfma_f32_16x16x32_bf16 v[60:63], v[146:149], v[186:189], v[60:63]
	v_mfma_f32_16x16x32_bf16 v[56:59], v[154:157], v[186:189], v[56:59]
	v_mfma_f32_16x16x32_bf16 v[52:55], v[146:149], v[190:193], v[52:55]
	v_mfma_f32_16x16x32_bf16 v[48:51], v[154:157], v[190:193], v[48:51]
	v_mfma_f32_16x16x32_bf16 v[36:39], v[146:149], v[202:205], v[36:39]
	v_mfma_f32_16x16x32_bf16 v[32:35], v[154:157], v[202:205], v[32:35]
	v_mfma_f32_16x16x32_bf16 v[20:23], v[146:149], v[206:209], v[20:23]
	v_mfma_f32_16x16x32_bf16 v[16:19], v[154:157], v[206:209], v[16:19]
	v_mfma_f32_16x16x32_bf16 v[60:63], v[150:153], v[194:197], v[60:63]
	v_mfma_f32_16x16x32_bf16 v[56:59], v[166:169], v[194:197], v[56:59]
	v_mfma_f32_16x16x32_bf16 v[52:55], v[150:153], v[198:201], v[52:55]
	v_mfma_f32_16x16x32_bf16 v[48:51], v[166:169], v[198:201], v[48:51]
	v_mfma_f32_16x16x32_bf16 v[36:39], v[150:153], v[210:213], v[36:39]
	v_mfma_f32_16x16x32_bf16 v[32:35], v[166:169], v[210:213], v[32:35]
	v_mfma_f32_16x16x32_bf16 v[20:23], v[150:153], v[214:217], v[20:23]
	v_mfma_f32_16x16x32_bf16 v[16:19], v[166:169], v[214:217], v[16:19]
	s_setprio 0
	s_setprio 1
	v_mfma_f32_16x16x32_bf16 v[44:47], v[170:173], v[186:189], v[44:47]
	v_mfma_f32_16x16x32_bf16 v[40:43], v[178:181], v[186:189], v[40:43]
	v_mfma_f32_16x16x32_bf16 v[28:31], v[170:173], v[190:193], v[28:31]
	v_mfma_f32_16x16x32_bf16 v[24:27], v[178:181], v[190:193], v[24:27]
	v_mfma_f32_16x16x32_bf16 v[12:15], v[170:173], v[202:205], v[12:15]
	v_mfma_f32_16x16x32_bf16 v[8:11], v[178:181], v[202:205], v[8:11]
	v_mfma_f32_16x16x32_bf16 v[4:7], v[170:173], v[206:209], v[4:7]
	v_mfma_f32_16x16x32_bf16 v[0:3], v[178:181], v[206:209], v[0:3]
	v_mfma_f32_16x16x32_bf16 v[44:47], v[174:177], v[194:197], v[44:47]
	v_mfma_f32_16x16x32_bf16 v[40:43], v[182:185], v[194:197], v[40:43]
	v_mfma_f32_16x16x32_bf16 v[28:31], v[174:177], v[198:201], v[28:31]
	v_mfma_f32_16x16x32_bf16 v[24:27], v[182:185], v[198:201], v[24:27]
	v_mfma_f32_16x16x32_bf16 v[12:15], v[174:177], v[210:213], v[12:15]
	v_mfma_f32_16x16x32_bf16 v[8:11], v[182:185], v[210:213], v[8:11]
	v_mfma_f32_16x16x32_bf16 v[4:7], v[174:177], v[214:217], v[4:7]
	v_mfma_f32_16x16x32_bf16 v[0:3], v[182:185], v[214:217], v[0:3]
	s_setprio 0
	s_barrier
	s_add_i32 s65, 0, 0x18000
	v_add_u32_e32 v145, s65, v136
	v_add_u32_e32 v150, s65, v140
	ds_read_b128 v[146:149], v145
	ds_read_b128 v[150:153], v150
	v_add_u32_e32 v145, s87, v136
	s_add_i32 s77, 0, 0x1c000
	v_add_u32_e32 v162, s87, v140
	ds_read_b128 v[154:157], v145
	ds_read_b128 v[166:169], v162
	v_add_u32_e32 v145, s77, v136
	v_add_u32_e32 v162, s77, v140
	ds_read_b128 v[170:173], v145
	ds_read_b128 v[174:177], v162
	v_add_u32_e32 v145, s2, v136
	v_add_u32_e32 v162, s2, v140
	ds_read_b128 v[178:181], v145
	ds_read_b128 v[182:185], v162
	s_add_u32 s30, s30, 0x80000
	s_addc_u32 s31, s31, 0
	s_mov_b32 m0, s43
	v_lshl_add_u64 v[230:231], s[30:31], 0, v[130:131]
	ds_read_b128 v[186:189], v141 offset:32768
	ds_read_b128 v[190:193], v141 offset:34816
	ds_read_b128 v[194:197], v142 offset:32768
	ds_read_b128 v[198:201], v142 offset:34816
	ds_read_b128 v[202:205], v141 offset:36864
	ds_read_b128 v[206:209], v141 offset:38912
	ds_read_b128 v[210:213], v142 offset:36864
	ds_read_b128 v[214:217], v142 offset:38912
	global_load_lds_dwordx4 v[230:231], off
	v_lshl_add_u64 v[230:231], s[30:31], 0, v[128:129]
	s_mov_b32 m0, s46
	s_nop 0
	global_load_lds_dwordx4 v[230:231], off
	s_waitcnt vmcnt(8)
	s_waitcnt lgkmcnt(0)
	s_barrier
	s_setprio 1
	s_waitcnt lgkmcnt(0)
	v_mfma_f32_16x16x32_bf16 v[124:127], v[146:149], v[186:189], v[124:127]
	v_mfma_f32_16x16x32_bf16 v[120:123], v[154:157], v[186:189], v[120:123]
	v_mfma_f32_16x16x32_bf16 v[116:119], v[146:149], v[190:193], v[116:119]
	v_mfma_f32_16x16x32_bf16 v[112:115], v[154:157], v[190:193], v[112:115]
	v_mfma_f32_16x16x32_bf16 v[100:103], v[146:149], v[202:205], v[100:103]
	v_mfma_f32_16x16x32_bf16 v[96:99], v[154:157], v[202:205], v[96:99]
	v_mfma_f32_16x16x32_bf16 v[84:87], v[146:149], v[206:209], v[84:87]
	v_mfma_f32_16x16x32_bf16 v[80:83], v[154:157], v[206:209], v[80:83]
	v_mfma_f32_16x16x32_bf16 v[124:127], v[150:153], v[194:197], v[124:127]
	v_mfma_f32_16x16x32_bf16 v[120:123], v[166:169], v[194:197], v[120:123]
	v_mfma_f32_16x16x32_bf16 v[116:119], v[150:153], v[198:201], v[116:119]
	v_mfma_f32_16x16x32_bf16 v[112:115], v[166:169], v[198:201], v[112:115]
	v_mfma_f32_16x16x32_bf16 v[100:103], v[150:153], v[210:213], v[100:103]
	v_mfma_f32_16x16x32_bf16 v[96:99], v[166:169], v[210:213], v[96:99]
	v_mfma_f32_16x16x32_bf16 v[84:87], v[150:153], v[214:217], v[84:87]
	v_mfma_f32_16x16x32_bf16 v[80:83], v[166:169], v[214:217], v[80:83]
	s_setprio 0
	s_setprio 1
	v_mfma_f32_16x16x32_bf16 v[108:111], v[170:173], v[186:189], v[108:111]
	v_mfma_f32_16x16x32_bf16 v[104:107], v[178:181], v[186:189], v[104:107]
	v_mfma_f32_16x16x32_bf16 v[92:95], v[170:173], v[190:193], v[92:95]
	v_mfma_f32_16x16x32_bf16 v[88:91], v[178:181], v[190:193], v[88:91]
	v_mfma_f32_16x16x32_bf16 v[76:79], v[170:173], v[202:205], v[76:79]
	v_mfma_f32_16x16x32_bf16 v[72:75], v[178:181], v[202:205], v[72:75]
	v_mfma_f32_16x16x32_bf16 v[68:71], v[170:173], v[206:209], v[68:71]
	v_mfma_f32_16x16x32_bf16 v[64:67], v[178:181], v[206:209], v[64:67]
	v_mfma_f32_16x16x32_bf16 v[108:111], v[174:177], v[194:197], v[108:111]
	v_mfma_f32_16x16x32_bf16 v[104:107], v[182:185], v[194:197], v[104:107]
	v_mfma_f32_16x16x32_bf16 v[92:95], v[174:177], v[198:201], v[92:95]
	v_mfma_f32_16x16x32_bf16 v[88:91], v[182:185], v[198:201], v[88:91]
	v_mfma_f32_16x16x32_bf16 v[76:79], v[174:177], v[210:213], v[76:79]
	v_mfma_f32_16x16x32_bf16 v[72:75], v[182:185], v[210:213], v[72:75]
	v_mfma_f32_16x16x32_bf16 v[68:71], v[174:177], v[214:217], v[68:71]
	v_mfma_f32_16x16x32_bf16 v[64:67], v[182:185], v[214:217], v[64:67]
	s_setprio 0
	s_barrier
	s_add_i32 s30, s65, s36
	v_lshl_add_u64 v[158:159], v[158:159], 0, s[54:55]
	s_mov_b32 m0, s30
	ds_read_b128 v[186:189], v141 offset:49152
	ds_read_b128 v[190:193], v141 offset:51200
	ds_read_b128 v[194:197], v142 offset:49152
	ds_read_b128 v[198:201], v142 offset:51200
	ds_read_b128 v[202:205], v141 offset:53248
	ds_read_b128 v[206:209], v141 offset:55296
	ds_read_b128 v[210:213], v142 offset:53248
	ds_read_b128 v[214:217], v142 offset:55296
	global_load_lds_dwordx4 v[158:159], off
	s_add_i32 m0, s30, 0x2000
	s_add_u32 s20, s20, 0x80080
	v_lshl_add_u64 v[158:159], v[218:219], 0, s[54:55]
	s_addc_u32 s21, s21, 0
	s_add_i32 s30, s77, s36
	global_load_lds_dwordx4 v[158:159], off
	v_lshl_add_u64 v[158:159], s[20:21], 0, v[130:131]
	s_mov_b32 m0, s30
	s_nop 0
	global_load_lds_dwordx4 v[158:159], off
	v_lshl_add_u64 v[158:159], s[20:21], 0, v[128:129]
	s_add_i32 m0, s30, 0x2000
	s_nop 0
	global_load_lds_dwordx4 v[158:159], off
	v_lshl_add_u64 v[158:159], v[226:227], 0, s[54:55]
	s_mov_b32 m0, s47
	s_nop 0
	global_load_lds_dwordx4 v[158:159], off
	v_lshl_add_u64 v[158:159], v[228:229], 0, s[54:55]
	s_mov_b32 m0, s56
	s_nop 0
	global_load_lds_dwordx4 v[158:159], off
	s_waitcnt vmcnt(8)
	s_waitcnt lgkmcnt(0)
	s_barrier
	s_setprio 1
	s_waitcnt lgkmcnt(0)
	v_mfma_f32_16x16x32_bf16 v[60:63], v[146:149], v[186:189], v[60:63]
	v_mfma_f32_16x16x32_bf16 v[56:59], v[154:157], v[186:189], v[56:59]
	v_mfma_f32_16x16x32_bf16 v[52:55], v[146:149], v[190:193], v[52:55]
	v_mfma_f32_16x16x32_bf16 v[48:51], v[154:157], v[190:193], v[48:51]
	v_mfma_f32_16x16x32_bf16 v[36:39], v[146:149], v[202:205], v[36:39]
	v_mfma_f32_16x16x32_bf16 v[32:35], v[154:157], v[202:205], v[32:35]
	v_mfma_f32_16x16x32_bf16 v[20:23], v[146:149], v[206:209], v[20:23]
	v_mfma_f32_16x16x32_bf16 v[16:19], v[154:157], v[206:209], v[16:19]
	v_mfma_f32_16x16x32_bf16 v[60:63], v[150:153], v[194:197], v[60:63]
	v_mfma_f32_16x16x32_bf16 v[56:59], v[166:169], v[194:197], v[56:59]
	v_mfma_f32_16x16x32_bf16 v[52:55], v[150:153], v[198:201], v[52:55]
	v_mfma_f32_16x16x32_bf16 v[48:51], v[166:169], v[198:201], v[48:51]
	v_mfma_f32_16x16x32_bf16 v[36:39], v[150:153], v[210:213], v[36:39]
	v_mfma_f32_16x16x32_bf16 v[32:35], v[166:169], v[210:213], v[32:35]
	v_mfma_f32_16x16x32_bf16 v[20:23], v[150:153], v[214:217], v[20:23]
	v_mfma_f32_16x16x32_bf16 v[16:19], v[166:169], v[214:217], v[16:19]
	s_setprio 0
	s_setprio 1
	v_mfma_f32_16x16x32_bf16 v[44:47], v[170:173], v[186:189], v[44:47]
	v_mfma_f32_16x16x32_bf16 v[40:43], v[178:181], v[186:189], v[40:43]
	v_mfma_f32_16x16x32_bf16 v[28:31], v[170:173], v[190:193], v[28:31]
	v_mfma_f32_16x16x32_bf16 v[24:27], v[178:181], v[190:193], v[24:27]
	v_mfma_f32_16x16x32_bf16 v[12:15], v[170:173], v[202:205], v[12:15]
	v_mfma_f32_16x16x32_bf16 v[8:11], v[178:181], v[202:205], v[8:11]
	v_mfma_f32_16x16x32_bf16 v[4:7], v[170:173], v[206:209], v[4:7]
	v_mfma_f32_16x16x32_bf16 v[0:3], v[178:181], v[206:209], v[0:3]
	v_mfma_f32_16x16x32_bf16 v[44:47], v[174:177], v[194:197], v[44:47]
	v_mfma_f32_16x16x32_bf16 v[40:43], v[182:185], v[194:197], v[40:43]
	v_mfma_f32_16x16x32_bf16 v[28:31], v[174:177], v[198:201], v[28:31]
	v_mfma_f32_16x16x32_bf16 v[24:27], v[182:185], v[198:201], v[24:27]
	v_mfma_f32_16x16x32_bf16 v[12:15], v[174:177], v[210:213], v[12:15]
	v_mfma_f32_16x16x32_bf16 v[8:11], v[182:185], v[210:213], v[8:11]
	v_mfma_f32_16x16x32_bf16 v[4:7], v[174:177], v[214:217], v[4:7]
	v_mfma_f32_16x16x32_bf16 v[0:3], v[182:185], v[214:217], v[0:3]
	s_setprio 0
	s_barrier
	s_add_i32 s76, s76, 2
	s_add_u32 s18, s18, 0x100
	s_addc_u32 s19, s19, 0
	s_add_u32 s72, s72, 0x100
	s_addc_u32 s73, s73, 0
	s_cmp_gt_u32 s76, 29
	s_cbranch_scc0 .LBB0_557
	s_mov_b32 s100, 1
	s_and_b64 vcc, exec, s[8:9]
	s_cbranch_vccz .LBB0_560
	s_barrier

.LBB0_646:
	v_mov_b32_e32 v133, v161
	v_lshl_add_u64 v[6:7], s[20:21], 0, v[132:133]
	v_mov_b32_e32 v129, v161
	v_readlane_b32 s18, v254, 11
	v_lshl_add_u64 v[8:9], s[20:21], 0, v[128:129]
	v_mov_b32_e32 v135, v161
	v_readlane_b32 s19, v254, 12
	s_add_i32 m0, s77, 0x18000
	v_lshl_add_u64 v[6:7], v[6:7], 0, s[54:55]
	v_lshl_add_u64 v[10:11], s[18:19], 0, v[134:135]
	v_mov_b32_e32 v131, v161
	s_and_b32 s10, s8, 3
	s_lshl_b32 s11, s7, 6
	s_mov_b32 s100, 0
	s_waitcnt vmcnt(2)
	s_barrier
	global_load_lds_dwordx4 v[6:7], off
	v_lshl_add_u64 v[6:7], v[8:9], 0, s[54:55]
	s_add_i32 m0, s77, 0x1a000
	s_add_i32 s90, s77, 0x8000
	s_add_i32 s91, s77, 0xa000
	v_lshl_add_u64 v[12:13], s[18:19], 0, v[130:131]
	global_load_lds_dwordx4 v[6:7], off
	v_lshl_add_u64 v[6:7], v[10:11], 0, s[54:55]
	s_mov_b32 m0, s90
	s_add_u32 s8, s20, 0x8080
	global_load_lds_dwordx4 v[6:7], off
	v_lshl_add_u64 v[6:7], v[12:13], 0, s[54:55]
	s_mov_b32 m0, s91
	s_addc_u32 s9, s21, 0
	global_load_lds_dwordx4 v[6:7], off
	s_add_i32 m0, s77, 0x1c000
	v_lshl_add_u64 v[6:7], s[8:9], 0, v[132:133]
	global_load_lds_dwordx4 v[6:7], off
	v_lshl_add_u64 v[6:7], s[8:9], 0, v[128:129]
	s_add_i32 m0, s77, 0x1e000
	s_cmpk_lt_u32 s6, 0x100
	global_load_lds_dwordx4 v[6:7], off
	s_cselect_b64 s[8:9], -1, 0
	s_lshl_b32 s6, s7, 13
	v_and_b32_e32 v5, 7, v0
	v_bfe_u32 v16, v0, 1, 3
	s_lshl_b32 s7, s10, 11
	s_add_i32 s6, s6, 0
	v_and_b32_e32 v14, 15, v0
	v_bitop3_b32 v16, v3, v16, 3 bitop3:0x6c
	s_add_i32 s6, s6, s7
	v_bfe_u32 v6, v0, 3, 3
	v_bitop3_b32 v3, v3, v5, 3 bitop3:0x6c
	v_or_b32_e32 v15, s11, v14
	v_lshlrev_b32_e32 v16, 4, v16
	v_lshlrev_b32_e32 v18, 7, v14
	s_add_i32 s6, s6, 0x20000
	v_cmp_gt_u32_e32 vcc, 8, v14
	v_lshlrev_b32_e32 v8, 7, v6
	v_lshlrev_b32_e32 v3, 4, v3
	v_and_b32_e32 v0, 4, v0
	v_lshlrev_b32_e32 v15, 7, v15
	s_waitcnt vmcnt(6)
	v_add3_u32 v141, s6, v18, v16
	v_cndmask_b32_e64 v7, v224, 64, vcc
	v_add3_u32 v142, s6, v8, v3
	v_cmp_eq_u32_e32 vcc, 0, v0
	s_lshl_b32 s6, s10, 6
	v_or_b32_e32 v17, v15, v16
	v_lshl_or_b32 v19, s10, 12, v18
	v_cndmask_b32_e64 v3, v224, 64, vcc
	v_lshlrev_b32_e32 v0, 3, v5
	v_bitop3_b32 v5, v15, 64, v16 bitop3:0x36
	s_lshl_b32 s80, s6, 1
	v_readlane_b32 s6, v254, 7
	v_or_b32_e32 v140, v19, v16
	s_mov_b32 s94, 0
	v_or_b32_e32 v143, s11, v6
	v_bitop3_b32 v144, v19, 64, v16 bitop3:0x36
	v_add_u32_e32 v136, v4, v1
	v_mov_b32_e32 v137, v161
	v_add_u32_e32 v138, v2, v1
	v_mov_b32_e32 v139, v161
	v_add_u32_e32 v145, 0, v17
	v_add_u32_e32 v146, 0, v5
	v_lshlrev_b32_e32 v160, 1, v0
	v_add_u32_e32 v147, v141, v7
	v_add_u32_e32 v148, v142, v3
	v_readlane_b32 s35, v254, 49
	s_mov_b32 s34, s6
	s_barrier
	v_readlane_b32 s7, v254, 8
	s_branch .LBB0_649

.LBB0_652:
	s_add_u32 s20, s18, 0xfffe0080
	s_addc_u32 s21, s19, -1
	s_add_i32 s57, 0, 0x10000
	s_cmp_eq_u32 s56, 4
	v_add_u32_e32 v149, s57, v140
	v_add_u32_e32 v154, s57, v144
	s_cselect_b32 s31, s13, s21
	s_cselect_b32 s30, s36, s20
	ds_read_b128 v[150:153], v149
	ds_read_b128 v[154:157], v154
	v_add_u32_e32 v149, s1, v140
	s_cselect_b32 s21, s11, s47
	s_cselect_b32 s20, s37, s46
	s_add_i32 s65, 0, 0x14000
	v_add_u32_e32 v158, s1, v144
	ds_read_b128 v[166:169], v149
	ds_read_b128 v[170:173], v158
	v_add_u32_e32 v149, s65, v140
	v_add_u32_e32 v158, s65, v144
	ds_read_b128 v[174:177], v149
	ds_read_b128 v[178:181], v158
	v_add_u32_e32 v149, s86, v140
	v_add_u32_e32 v158, s86, v144
	ds_read_b128 v[182:185], v149
	ds_read_b128 v[186:189], v158
	v_lshl_add_u64 v[158:159], s[18:19], 0, v[136:137]
	s_add_i32 m0, s77, 0xc000
	ds_read_b128 v[190:193], v145
	ds_read_b128 v[194:197], v145 offset:2048
	ds_read_b128 v[198:201], v146
	ds_read_b128 v[202:205], v146 offset:2048
	ds_read_b128 v[206:209], v145 offset:4096
	ds_read_b128 v[210:213], v145 offset:6144
	ds_read_b128 v[214:217], v146 offset:4096
	ds_read_b128 v[226:229], v146 offset:6144
	global_load_lds_dwordx4 v[158:159], off
	v_lshl_add_u64 v[158:159], s[18:19], 0, v[138:139]
	s_add_i32 m0, s77, 0xe000
	s_nop 0
	global_load_lds_dwordx4 v[158:159], off
	s_waitcnt vmcnt(24)
	s_cmp_lg_u32 s100, 0
	s_cbranch_scc1 .Lgrx_7
	s_waitcnt vmcnt(8)
.Lgrx_7:
	s_waitcnt lgkmcnt(0)
	s_barrier
	s_setprio 1
	s_waitcnt lgkmcnt(0)
	v_mfma_f32_16x16x32_bf16 v[124:127], v[150:153], v[190:193], v[124:127]
	v_mfma_f32_16x16x32_bf16 v[120:123], v[166:169], v[190:193], v[120:123]
	v_mfma_f32_16x16x32_bf16 v[116:119], v[150:153], v[194:197], v[116:119]
	v_mfma_f32_16x16x32_bf16 v[112:115], v[166:169], v[194:197], v[112:115]
	v_mfma_f32_16x16x32_bf16 v[100:103], v[150:153], v[206:209], v[100:103]
	v_mfma_f32_16x16x32_bf16 v[96:99], v[166:169], v[206:209], v[96:99]
	v_mfma_f32_16x16x32_bf16 v[84:87], v[150:153], v[210:213], v[84:87]
	v_mfma_f32_16x16x32_bf16 v[80:83], v[166:169], v[210:213], v[80:83]
	v_mfma_f32_16x16x32_bf16 v[124:127], v[154:157], v[198:201], v[124:127]
	v_mfma_f32_16x16x32_bf16 v[120:123], v[170:173], v[198:201], v[120:123]
	v_mfma_f32_16x16x32_bf16 v[116:119], v[154:157], v[202:205], v[116:119]
	v_mfma_f32_16x16x32_bf16 v[112:115], v[170:173], v[202:205], v[112:115]
	v_mfma_f32_16x16x32_bf16 v[100:103], v[154:157], v[214:217], v[100:103]
	v_mfma_f32_16x16x32_bf16 v[96:99], v[170:173], v[214:217], v[96:99]
	v_mfma_f32_16x16x32_bf16 v[84:87], v[154:157], v[226:229], v[84:87]
	v_mfma_f32_16x16x32_bf16 v[80:83], v[170:173], v[226:229], v[80:83]
	s_setprio 0
	s_setprio 1
	v_mfma_f32_16x16x32_bf16 v[108:111], v[174:177], v[190:193], v[108:111]
	v_mfma_f32_16x16x32_bf16 v[104:107], v[182:185], v[190:193], v[104:107]
	v_mfma_f32_16x16x32_bf16 v[92:95], v[174:177], v[194:197], v[92:95]
	v_mfma_f32_16x16x32_bf16 v[88:91], v[182:185], v[194:197], v[88:91]
	v_mfma_f32_16x16x32_bf16 v[76:79], v[174:177], v[206:209], v[76:79]
	v_mfma_f32_16x16x32_bf16 v[72:75], v[182:185], v[206:209], v[72:75]
	v_mfma_f32_16x16x32_bf16 v[68:71], v[174:177], v[210:213], v[68:71]
	v_mfma_f32_16x16x32_bf16 v[64:67], v[182:185], v[210:213], v[64:67]
	v_mfma_f32_16x16x32_bf16 v[108:111], v[178:181], v[198:201], v[108:111]
	v_mfma_f32_16x16x32_bf16 v[104:107], v[186:189], v[198:201], v[104:107]
	v_mfma_f32_16x16x32_bf16 v[92:95], v[178:181], v[202:205], v[92:95]
	v_mfma_f32_16x16x32_bf16 v[88:91], v[186:189], v[202:205], v[88:91]
	v_mfma_f32_16x16x32_bf16 v[76:79], v[178:181], v[214:217], v[76:79]
	v_mfma_f32_16x16x32_bf16 v[72:75], v[186:189], v[214:217], v[72:75]
	v_mfma_f32_16x16x32_bf16 v[68:71], v[178:181], v[226:229], v[68:71]
	v_mfma_f32_16x16x32_bf16 v[64:67], v[186:189], v[226:229], v[64:67]
	s_setprio 0
	s_barrier
	s_add_i32 s57, s57, s76
	v_lshl_add_u64 v[158:159], s[20:21], 0, v[132:133]
	s_mov_b32 m0, s57
	ds_read_b128 v[190:193], v145 offset:16384
	ds_read_b128 v[194:197], v145 offset:18432
	ds_read_b128 v[198:201], v146 offset:16384
	ds_read_b128 v[202:205], v146 offset:18432
	ds_read_b128 v[206:209], v145 offset:20480
	ds_read_b128 v[210:213], v145 offset:22528
	ds_read_b128 v[214:217], v146 offset:20480
	ds_read_b128 v[226:229], v146 offset:22528
	global_load_lds_dwordx4 v[158:159], off
	s_add_i32 m0, s57, 0x2000
	s_add_u32 s58, s20, 0x8000
	v_lshl_add_u64 v[218:219], s[20:21], 0, v[128:129]
	s_addc_u32 s59, s21, 0
	s_add_i32 s57, s65, s76
	global_load_lds_dwordx4 v[218:219], off
	v_lshl_add_u64 v[230:231], s[58:59], 0, v[132:133]
	s_mov_b32 m0, s57
	v_lshl_add_u64 v[232:233], s[30:31], 0, v[130:131]
	global_load_lds_dwordx4 v[230:231], off
	v_lshl_add_u64 v[230:231], s[58:59], 0, v[128:129]
	s_add_i32 m0, s57, 0x2000
	s_nop 0
	global_load_lds_dwordx4 v[230:231], off
	v_lshl_add_u64 v[230:231], s[30:31], 0, v[134:135]
	s_mov_b32 m0, s77
	s_nop 0
	global_load_lds_dwordx4 v[230:231], off
	s_mov_b32 m0, s84
	s_nop 0
	global_load_lds_dwordx4 v[232:233], off
	s_waitcnt vmcnt(24)
	s_cmp_lg_u32 s100, 0
	s_cbranch_scc1 .Lgrx_8
	s_waitcnt vmcnt(8)
.Lgrx_8:
	s_mov_b32 s100, 0
	s_waitcnt lgkmcnt(0)
	s_barrier
	s_setprio 1
	s_waitcnt lgkmcnt(0)
	v_mfma_f32_16x16x32_bf16 v[60:63], v[150:153], v[190:193], v[60:63]
	v_mfma_f32_16x16x32_bf16 v[56:59], v[166:169], v[190:193], v[56:59]
	v_mfma_f32_16x16x32_bf16 v[52:55], v[150:153], v[194:197], v[52:55]
	v_mfma_f32_16x16x32_bf16 v[44:47], v[166:169], v[194:197], v[44:47]
	v_mfma_f32_16x16x32_bf16 v[36:39], v[150:153], v[206:209], v[36:39]
	v_mfma_f32_16x16x32_bf16 v[28:31], v[166:169], v[206:209], v[28:31]
	v_mfma_f32_16x16x32_bf16 v[20:23], v[150:153], v[210:213], v[20:23]
	v_mfma_f32_16x16x32_bf16 v[12:15], v[166:169], v[210:213], v[12:15]
	v_mfma_f32_16x16x32_bf16 v[60:63], v[154:157], v[198:201], v[60:63]
	v_mfma_f32_16x16x32_bf16 v[56:59], v[170:173], v[198:201], v[56:59]
	v_mfma_f32_16x16x32_bf16 v[52:55], v[154:157], v[202:205], v[52:55]
	v_mfma_f32_16x16x32_bf16 v[44:47], v[170:173], v[202:205], v[44:47]
	v_mfma_f32_16x16x32_bf16 v[36:39], v[154:157], v[214:217], v[36:39]
	v_mfma_f32_16x16x32_bf16 v[28:31], v[170:173], v[214:217], v[28:31]
	v_mfma_f32_16x16x32_bf16 v[20:23], v[154:157], v[226:229], v[20:23]
	v_mfma_f32_16x16x32_bf16 v[12:15], v[170:173], v[226:229], v[12:15]
	s_setprio 0
	s_setprio 1
	v_mfma_f32_16x16x32_bf16 v[48:51], v[174:177], v[190:193], v[48:51]
	v_mfma_f32_16x16x32_bf16 v[40:43], v[182:185], v[190:193], v[40:43]
	v_mfma_f32_16x16x32_bf16 v[32:35], v[174:177], v[194:197], v[32:35]
	v_mfma_f32_16x16x32_bf16 v[24:27], v[182:185], v[194:197], v[24:27]
	v_mfma_f32_16x16x32_bf16 v[16:19], v[174:177], v[206:209], v[16:19]
	v_mfma_f32_16x16x32_bf16 v[8:11], v[182:185], v[206:209], v[8:11]
	v_mfma_f32_16x16x32_bf16 v[4:7], v[174:177], v[210:213], v[4:7]
	v_mfma_f32_16x16x32_bf16 v[0:3], v[182:185], v[210:213], v[0:3]
	v_mfma_f32_16x16x32_bf16 v[48:51], v[178:181], v[198:201], v[48:51]
	v_mfma_f32_16x16x32_bf16 v[40:43], v[186:189], v[198:201], v[40:43]
	v_mfma_f32_16x16x32_bf16 v[32:35], v[178:181], v[202:205], v[32:35]
	v_mfma_f32_16x16x32_bf16 v[24:27], v[186:189], v[202:205], v[24:27]
	v_mfma_f32_16x16x32_bf16 v[16:19], v[178:181], v[214:217], v[16:19]
	v_mfma_f32_16x16x32_bf16 v[8:11], v[186:189], v[214:217], v[8:11]
	v_mfma_f32_16x16x32_bf16 v[4:7], v[178:181], v[226:229], v[4:7]
	v_mfma_f32_16x16x32_bf16 v[0:3], v[186:189], v[226:229], v[0:3]
	s_setprio 0
	s_barrier
	s_add_i32 s57, 0, 0x18000
	v_add_u32_e32 v149, s57, v140
	v_add_u32_e32 v154, s57, v144
	ds_read_b128 v[150:153], v149
	ds_read_b128 v[154:157], v154
	v_add_u32_e32 v149, s87, v140
	s_add_i32 s58, 0, 0x1c000
	v_add_u32_e32 v162, s87, v144
	ds_read_b128 v[166:169], v149
	ds_read_b128 v[170:173], v162
	v_add_u32_e32 v149, s58, v140
	v_add_u32_e32 v162, s58, v144
	ds_read_b128 v[174:177], v149
	ds_read_b128 v[178:181], v162
	v_add_u32_e32 v149, s2, v140
	v_add_u32_e32 v162, s2, v144
	ds_read_b128 v[182:185], v149
	ds_read_b128 v[186:189], v162
	s_add_u32 s30, s30, 0x20000
	s_addc_u32 s31, s31, 0
	s_mov_b32 m0, s88
	v_lshl_add_u64 v[234:235], s[30:31], 0, v[134:135]
	ds_read_b128 v[190:193], v145 offset:32768
	ds_read_b128 v[194:197], v145 offset:34816
	ds_read_b128 v[198:201], v146 offset:32768
	ds_read_b128 v[202:205], v146 offset:34816
	ds_read_b128 v[206:209], v145 offset:36864
	ds_read_b128 v[210:213], v145 offset:38912
	ds_read_b128 v[214:217], v146 offset:36864
	ds_read_b128 v[226:229], v146 offset:38912
	global_load_lds_dwordx4 v[234:235], off
	v_lshl_add_u64 v[234:235], s[30:31], 0, v[130:131]
	s_mov_b32 m0, s89
	s_nop 0
	global_load_lds_dwordx4 v[234:235], off
	s_waitcnt vmcnt(8)
	s_waitcnt lgkmcnt(0)
	s_barrier
	s_setprio 1
	s_waitcnt lgkmcnt(0)
	v_mfma_f32_16x16x32_bf16 v[124:127], v[150:153], v[190:193], v[124:127]
	v_mfma_f32_16x16x32_bf16 v[120:123], v[166:169], v[190:193], v[120:123]
	v_mfma_f32_16x16x32_bf16 v[116:119], v[150:153], v[194:197], v[116:119]
	v_mfma_f32_16x16x32_bf16 v[112:115], v[166:169], v[194:197], v[112:115]
	v_mfma_f32_16x16x32_bf16 v[100:103], v[150:153], v[206:209], v[100:103]
	v_mfma_f32_16x16x32_bf16 v[96:99], v[166:169], v[206:209], v[96:99]
	v_mfma_f32_16x16x32_bf16 v[84:87], v[150:153], v[210:213], v[84:87]
	v_mfma_f32_16x16x32_bf16 v[80:83], v[166:169], v[210:213], v[80:83]
	v_mfma_f32_16x16x32_bf16 v[124:127], v[154:157], v[198:201], v[124:127]
	v_mfma_f32_16x16x32_bf16 v[120:123], v[170:173], v[198:201], v[120:123]
	v_mfma_f32_16x16x32_bf16 v[116:119], v[154:157], v[202:205], v[116:119]
	v_mfma_f32_16x16x32_bf16 v[112:115], v[170:173], v[202:205], v[112:115]
	v_mfma_f32_16x16x32_bf16 v[100:103], v[154:157], v[214:217], v[100:103]
	v_mfma_f32_16x16x32_bf16 v[96:99], v[170:173], v[214:217], v[96:99]
	v_mfma_f32_16x16x32_bf16 v[84:87], v[154:157], v[226:229], v[84:87]
	v_mfma_f32_16x16x32_bf16 v[80:83], v[170:173], v[226:229], v[80:83]
	s_setprio 0
	s_setprio 1
	v_mfma_f32_16x16x32_bf16 v[108:111], v[174:177], v[190:193], v[108:111]
	v_mfma_f32_16x16x32_bf16 v[104:107], v[182:185], v[190:193], v[104:107]
	v_mfma_f32_16x16x32_bf16 v[92:95], v[174:177], v[194:197], v[92:95]
	v_mfma_f32_16x16x32_bf16 v[88:91], v[182:185], v[194:197], v[88:91]
	v_mfma_f32_16x16x32_bf16 v[76:79], v[174:177], v[206:209], v[76:79]
	v_mfma_f32_16x16x32_bf16 v[72:75], v[182:185], v[206:209], v[72:75]
	v_mfma_f32_16x16x32_bf16 v[68:71], v[174:177], v[210:213], v[68:71]
	v_mfma_f32_16x16x32_bf16 v[64:67], v[182:185], v[210:213], v[64:67]
	v_mfma_f32_16x16x32_bf16 v[108:111], v[178:181], v[198:201], v[108:111]
	v_mfma_f32_16x16x32_bf16 v[104:107], v[186:189], v[198:201], v[104:107]
	v_mfma_f32_16x16x32_bf16 v[92:95], v[178:181], v[202:205], v[92:95]
	v_mfma_f32_16x16x32_bf16 v[88:91], v[186:189], v[202:205], v[88:91]
	v_mfma_f32_16x16x32_bf16 v[76:79], v[178:181], v[214:217], v[76:79]
	v_mfma_f32_16x16x32_bf16 v[72:75], v[186:189], v[214:217], v[72:75]
	v_mfma_f32_16x16x32_bf16 v[68:71], v[178:181], v[226:229], v[68:71]
	v_mfma_f32_16x16x32_bf16 v[64:67], v[186:189], v[226:229], v[64:67]
	s_setprio 0
	s_barrier
	s_add_i32 s30, s57, s76
	v_lshl_add_u64 v[158:159], v[158:159], 0, s[54:55]
	s_mov_b32 m0, s30
	ds_read_b128 v[190:193], v145 offset:49152
	ds_read_b128 v[194:197], v145 offset:51200
	ds_read_b128 v[198:201], v146 offset:49152
	ds_read_b128 v[202:205], v146 offset:51200
	ds_read_b128 v[206:209], v145 offset:53248
	ds_read_b128 v[210:213], v145 offset:55296
	ds_read_b128 v[214:217], v146 offset:53248
	ds_read_b128 v[226:229], v146 offset:55296
	global_load_lds_dwordx4 v[158:159], off
	s_add_i32 m0, s30, 0x2000
	s_add_u32 s20, s20, 0x8080
	v_lshl_add_u64 v[158:159], v[218:219], 0, s[54:55]
	s_addc_u32 s21, s21, 0
	s_add_i32 s30, s58, s76
	global_load_lds_dwordx4 v[158:159], off
	v_lshl_add_u64 v[158:159], s[20:21], 0, v[132:133]
	s_mov_b32 m0, s30
	s_nop 0
	global_load_lds_dwordx4 v[158:159], off
	v_lshl_add_u64 v[158:159], s[20:21], 0, v[128:129]
	s_add_i32 m0, s30, 0x2000
	s_nop 0
	global_load_lds_dwordx4 v[158:159], off
	v_lshl_add_u64 v[158:159], v[230:231], 0, s[54:55]
	s_mov_b32 m0, s90
	s_nop 0
	global_load_lds_dwordx4 v[158:159], off
	v_lshl_add_u64 v[158:159], v[232:233], 0, s[54:55]
	s_mov_b32 m0, s91
	s_nop 0
	global_load_lds_dwordx4 v[158:159], off
	s_waitcnt vmcnt(8)
	s_waitcnt lgkmcnt(0)
	s_barrier
	s_setprio 1
	s_waitcnt lgkmcnt(0)
	v_mfma_f32_16x16x32_bf16 v[60:63], v[150:153], v[190:193], v[60:63]
	v_mfma_f32_16x16x32_bf16 v[56:59], v[166:169], v[190:193], v[56:59]
	v_mfma_f32_16x16x32_bf16 v[52:55], v[150:153], v[194:197], v[52:55]
	v_mfma_f32_16x16x32_bf16 v[44:47], v[166:169], v[194:197], v[44:47]
	v_mfma_f32_16x16x32_bf16 v[36:39], v[150:153], v[206:209], v[36:39]
	v_mfma_f32_16x16x32_bf16 v[28:31], v[166:169], v[206:209], v[28:31]
	v_mfma_f32_16x16x32_bf16 v[20:23], v[150:153], v[210:213], v[20:23]
	v_mfma_f32_16x16x32_bf16 v[12:15], v[166:169], v[210:213], v[12:15]
	v_mfma_f32_16x16x32_bf16 v[60:63], v[154:157], v[198:201], v[60:63]
	v_mfma_f32_16x16x32_bf16 v[56:59], v[170:173], v[198:201], v[56:59]
	v_mfma_f32_16x16x32_bf16 v[52:55], v[154:157], v[202:205], v[52:55]
	v_mfma_f32_16x16x32_bf16 v[44:47], v[170:173], v[202:205], v[44:47]
	v_mfma_f32_16x16x32_bf16 v[36:39], v[154:157], v[214:217], v[36:39]
	v_mfma_f32_16x16x32_bf16 v[28:31], v[170:173], v[214:217], v[28:31]
	v_mfma_f32_16x16x32_bf16 v[20:23], v[154:157], v[226:229], v[20:23]
	v_mfma_f32_16x16x32_bf16 v[12:15], v[170:173], v[226:229], v[12:15]
	s_setprio 0
	s_setprio 1
	v_mfma_f32_16x16x32_bf16 v[48:51], v[174:177], v[190:193], v[48:51]
	v_mfma_f32_16x16x32_bf16 v[40:43], v[182:185], v[190:193], v[40:43]
	v_mfma_f32_16x16x32_bf16 v[32:35], v[174:177], v[194:197], v[32:35]
	v_mfma_f32_16x16x32_bf16 v[24:27], v[182:185], v[194:197], v[24:27]
	v_mfma_f32_16x16x32_bf16 v[16:19], v[174:177], v[206:209], v[16:19]
	v_mfma_f32_16x16x32_bf16 v[8:11], v[182:185], v[206:209], v[8:11]
	v_mfma_f32_16x16x32_bf16 v[4:7], v[174:177], v[210:213], v[4:7]
	v_mfma_f32_16x16x32_bf16 v[0:3], v[182:185], v[210:213], v[0:3]
	v_mfma_f32_16x16x32_bf16 v[48:51], v[178:181], v[198:201], v[48:51]
	v_mfma_f32_16x16x32_bf16 v[40:43], v[186:189], v[198:201], v[40:43]
	v_mfma_f32_16x16x32_bf16 v[32:35], v[178:181], v[202:205], v[32:35]
	v_mfma_f32_16x16x32_bf16 v[24:27], v[186:189], v[202:205], v[24:27]
	v_mfma_f32_16x16x32_bf16 v[16:19], v[178:181], v[214:217], v[16:19]
	v_mfma_f32_16x16x32_bf16 v[8:11], v[186:189], v[214:217], v[8:11]
	v_mfma_f32_16x16x32_bf16 v[4:7], v[178:181], v[226:229], v[4:7]
	v_mfma_f32_16x16x32_bf16 v[0:3], v[186:189], v[226:229], v[0:3]
	s_setprio 0
	s_barrier
	s_add_i32 s56, s56, 2
	s_add_u32 s18, s18, 0x100
	s_addc_u32 s19, s19, 0
	s_add_u32 s46, s46, 0x100
	s_addc_u32 s47, s47, 0
	s_cmp_gt_u32 s56, 5
	s_cbranch_scc0 .LBB0_652
	s_mov_b32 s100, 1
	s_and_b64 vcc, exec, s[8:9]
	s_cbranch_vccz .LBB0_655
	s_barrier

.LBB0_848:
	v_mov_b32_e32 v133, v161
	v_lshl_add_u64 v[6:7], s[20:21], 0, v[132:133]
	v_mov_b32_e32 v129, v161
	v_readlane_b32 s18, v254, 19
	v_lshl_add_u64 v[8:9], s[20:21], 0, v[128:129]
	v_mov_b32_e32 v135, v161
	v_readlane_b32 s19, v254, 20
	s_add_i32 m0, s37, 0x18000
	v_lshl_add_u64 v[6:7], v[6:7], 0, s[54:55]
	v_lshl_add_u64 v[10:11], s[18:19], 0, v[134:135]
	v_mov_b32_e32 v131, v161
	s_and_b32 s12, s8, 3
	s_lshl_b32 s13, s7, 6
	s_mov_b32 s100, 0
	s_waitcnt vmcnt(2)
	s_barrier
	global_load_lds_dwordx4 v[6:7], off
	v_lshl_add_u64 v[6:7], v[8:9], 0, s[54:55]
	s_add_i32 m0, s37, 0x1a000
	s_add_i32 s47, s37, 0x8000
	s_add_i32 s56, s37, 0xa000
	v_lshl_add_u64 v[12:13], s[18:19], 0, v[130:131]
	global_load_lds_dwordx4 v[6:7], off
	v_lshl_add_u64 v[6:7], v[10:11], 0, s[54:55]
	s_mov_b32 m0, s47
	s_add_u32 s8, s20, 0x8080
	global_load_lds_dwordx4 v[6:7], off
	v_lshl_add_u64 v[6:7], v[12:13], 0, s[54:55]
	s_mov_b32 m0, s56
	s_addc_u32 s9, s21, 0
	global_load_lds_dwordx4 v[6:7], off
	s_add_i32 m0, s37, 0x1c000
	v_lshl_add_u64 v[6:7], s[8:9], 0, v[132:133]
	global_load_lds_dwordx4 v[6:7], off
	v_lshl_add_u64 v[6:7], s[8:9], 0, v[128:129]
	s_add_i32 m0, s37, 0x1e000
	s_cmpk_lt_u32 s6, 0x100
	global_load_lds_dwordx4 v[6:7], off
	s_cselect_b64 s[10:11], -1, 0
	s_lshl_b32 s6, s7, 13
	v_and_b32_e32 v5, 7, v0
	v_bfe_u32 v16, v0, 1, 3
	s_lshl_b32 s7, s12, 11
	s_add_i32 s6, s6, 0
	v_and_b32_e32 v14, 15, v0
	v_bitop3_b32 v16, v3, v16, 3 bitop3:0x6c
	s_add_i32 s6, s6, s7
	v_bfe_u32 v6, v0, 3, 3
	v_bitop3_b32 v3, v3, v5, 3 bitop3:0x6c
	v_or_b32_e32 v15, s13, v14
	v_lshlrev_b32_e32 v16, 4, v16
	v_lshlrev_b32_e32 v18, 7, v14
	s_add_i32 s6, s6, 0x20000
	v_cmp_gt_u32_e32 vcc, 8, v14
	v_lshlrev_b32_e32 v8, 7, v6
	v_lshlrev_b32_e32 v3, 4, v3
	v_and_b32_e32 v0, 4, v0
	v_lshlrev_b32_e32 v15, 7, v15
	s_waitcnt vmcnt(6)
	v_add3_u32 v141, s6, v18, v16
	v_cndmask_b32_e64 v7, v224, 64, vcc
	v_add3_u32 v142, s6, v8, v3
	v_cmp_eq_u32_e32 vcc, 0, v0
	s_lshl_b32 s6, s12, 6
	v_or_b32_e32 v17, v15, v16
	v_lshl_or_b32 v19, s12, 12, v18
	v_cndmask_b32_e64 v3, v224, 64, vcc
	v_lshlrev_b32_e32 v0, 3, v5
	v_bitop3_b32 v5, v15, 64, v16 bitop3:0x36
	s_lshl_b32 s80, s6, 1
	v_readlane_b32 s6, v254, 17
	v_or_b32_e32 v140, v19, v16
	s_mov_b32 s57, 0
	v_or_b32_e32 v143, s13, v6
	v_bitop3_b32 v144, v19, 64, v16 bitop3:0x36
	v_add_u32_e32 v136, v4, v1
	v_mov_b32_e32 v137, v161
	v_add_u32_e32 v138, v2, v1
	v_mov_b32_e32 v139, v161
	v_add_u32_e32 v145, 0, v17
	v_add_u32_e32 v146, 0, v5
	v_lshlrev_b32_e32 v160, 1, v0
	v_add_u32_e32 v147, v141, v7
	v_add_u32_e32 v148, v142, v3
	v_readlane_b32 s58, v254, 50
	s_mov_b32 s59, s6
	s_barrier
	v_readlane_b32 s7, v254, 18
	s_branch .LBB0_851

.LBB0_856:
	s_add_u32 s20, s18, 0xffe00080
	s_addc_u32 s21, s19, -1
	s_add_i32 s65, 0, 0x10000
	s_cmp_eq_u32 s72, 4
	v_add_u32_e32 v149, s65, v140
	v_add_u32_e32 v154, s65, v144
	s_cselect_b32 s31, s9, s21
	s_cselect_b32 s30, s8, s20
	ds_read_b128 v[150:153], v149
	ds_read_b128 v[154:157], v154
	v_add_u32_e32 v149, s1, v140
	s_cselect_b32 s21, s13, s71
	s_cselect_b32 s20, s15, s70
	s_add_i32 s73, 0, 0x14000
	v_add_u32_e32 v158, s1, v144
	ds_read_b128 v[166:169], v149
	ds_read_b128 v[170:173], v158
	v_add_u32_e32 v149, s73, v140
	v_add_u32_e32 v158, s73, v144
	ds_read_b128 v[174:177], v149
	ds_read_b128 v[178:181], v158
	v_add_u32_e32 v149, s86, v140
	v_add_u32_e32 v158, s86, v144
	ds_read_b128 v[182:185], v149
	ds_read_b128 v[186:189], v158
	v_lshl_add_u64 v[158:159], s[18:19], 0, v[136:137]
	s_add_i32 m0, s37, 0xc000
	ds_read_b128 v[190:193], v145
	ds_read_b128 v[194:197], v145 offset:2048
	ds_read_b128 v[198:201], v146
	ds_read_b128 v[202:205], v146 offset:2048
	ds_read_b128 v[206:209], v145 offset:4096
	ds_read_b128 v[210:213], v145 offset:6144
	ds_read_b128 v[214:217], v146 offset:4096
	ds_read_b128 v[226:229], v146 offset:6144
	global_load_lds_dwordx4 v[158:159], off
	v_lshl_add_u64 v[158:159], s[18:19], 0, v[138:139]
	s_add_i32 m0, s37, 0xe000
	s_nop 0
	global_load_lds_dwordx4 v[158:159], off
	s_waitcnt vmcnt(24)
	s_cmp_lg_u32 s100, 0
	s_cbranch_scc1 .Lgrx_9
	s_waitcnt vmcnt(8)
.Lgrx_9:
	s_waitcnt lgkmcnt(0)
	s_barrier
	s_setprio 1
	s_waitcnt lgkmcnt(0)
	v_mfma_f32_16x16x32_bf16 v[124:127], v[150:153], v[190:193], v[124:127]
	v_mfma_f32_16x16x32_bf16 v[120:123], v[166:169], v[190:193], v[120:123]
	v_mfma_f32_16x16x32_bf16 v[116:119], v[150:153], v[194:197], v[116:119]
	v_mfma_f32_16x16x32_bf16 v[112:115], v[166:169], v[194:197], v[112:115]
	v_mfma_f32_16x16x32_bf16 v[100:103], v[150:153], v[206:209], v[100:103]
	v_mfma_f32_16x16x32_bf16 v[96:99], v[166:169], v[206:209], v[96:99]
	v_mfma_f32_16x16x32_bf16 v[84:87], v[150:153], v[210:213], v[84:87]
	v_mfma_f32_16x16x32_bf16 v[76:79], v[166:169], v[210:213], v[76:79]
	v_mfma_f32_16x16x32_bf16 v[124:127], v[154:157], v[198:201], v[124:127]
	v_mfma_f32_16x16x32_bf16 v[120:123], v[170:173], v[198:201], v[120:123]
	v_mfma_f32_16x16x32_bf16 v[116:119], v[154:157], v[202:205], v[116:119]
	v_mfma_f32_16x16x32_bf16 v[112:115], v[170:173], v[202:205], v[112:115]
	v_mfma_f32_16x16x32_bf16 v[100:103], v[154:157], v[214:217], v[100:103]
	v_mfma_f32_16x16x32_bf16 v[96:99], v[170:173], v[214:217], v[96:99]
	v_mfma_f32_16x16x32_bf16 v[84:87], v[154:157], v[226:229], v[84:87]
	v_mfma_f32_16x16x32_bf16 v[76:79], v[170:173], v[226:229], v[76:79]
	s_setprio 0
	s_setprio 1
	v_mfma_f32_16x16x32_bf16 v[108:111], v[174:177], v[190:193], v[108:111]
	v_mfma_f32_16x16x32_bf16 v[104:107], v[182:185], v[190:193], v[104:107]
	v_mfma_f32_16x16x32_bf16 v[92:95], v[174:177], v[194:197], v[92:95]
	v_mfma_f32_16x16x32_bf16 v[88:91], v[182:185], v[194:197], v[88:91]
	v_mfma_f32_16x16x32_bf16 v[80:83], v[174:177], v[206:209], v[80:83]
	v_mfma_f32_16x16x32_bf16 v[72:75], v[182:185], v[206:209], v[72:75]
	v_mfma_f32_16x16x32_bf16 v[68:71], v[174:177], v[210:213], v[68:71]
	v_mfma_f32_16x16x32_bf16 v[64:67], v[182:185], v[210:213], v[64:67]
	v_mfma_f32_16x16x32_bf16 v[108:111], v[178:181], v[198:201], v[108:111]
	v_mfma_f32_16x16x32_bf16 v[104:107], v[186:189], v[198:201], v[104:107]
	v_mfma_f32_16x16x32_bf16 v[92:95], v[178:181], v[202:205], v[92:95]
	v_mfma_f32_16x16x32_bf16 v[88:91], v[186:189], v[202:205], v[88:91]
	v_mfma_f32_16x16x32_bf16 v[80:83], v[178:181], v[214:217], v[80:83]
	v_mfma_f32_16x16x32_bf16 v[72:75], v[186:189], v[214:217], v[72:75]
	v_mfma_f32_16x16x32_bf16 v[68:71], v[178:181], v[226:229], v[68:71]
	v_mfma_f32_16x16x32_bf16 v[64:67], v[186:189], v[226:229], v[64:67]
	s_setprio 0
	s_barrier
	s_add_i32 s65, s65, s36
	v_lshl_add_u64 v[158:159], s[20:21], 0, v[132:133]
	s_mov_b32 m0, s65
	ds_read_b128 v[190:193], v145 offset:16384
	ds_read_b128 v[194:197], v145 offset:18432
	ds_read_b128 v[198:201], v146 offset:16384
	ds_read_b128 v[202:205], v146 offset:18432
	ds_read_b128 v[206:209], v145 offset:20480
	ds_read_b128 v[210:213], v145 offset:22528
	ds_read_b128 v[214:217], v146 offset:20480
	ds_read_b128 v[226:229], v146 offset:22528
	global_load_lds_dwordx4 v[158:159], off
	s_add_i32 m0, s65, 0x2000
	s_add_u32 s76, s20, 0x8000
	v_lshl_add_u64 v[218:219], s[20:21], 0, v[128:129]
	s_addc_u32 s77, s21, 0
	s_add_i32 s65, s73, s36
	global_load_lds_dwordx4 v[218:219], off
	v_lshl_add_u64 v[230:231], s[76:77], 0, v[132:133]
	s_mov_b32 m0, s65
	v_lshl_add_u64 v[232:233], s[30:31], 0, v[130:131]
	global_load_lds_dwordx4 v[230:231], off
	v_lshl_add_u64 v[230:231], s[76:77], 0, v[128:129]
	s_add_i32 m0, s65, 0x2000
	s_nop 0
	global_load_lds_dwordx4 v[230:231], off
	v_lshl_add_u64 v[230:231], s[30:31], 0, v[134:135]
	s_mov_b32 m0, s37
	s_nop 0
	global_load_lds_dwordx4 v[230:231], off
	s_mov_b32 m0, s41
	s_nop 0
	global_load_lds_dwordx4 v[232:233], off
	s_waitcnt vmcnt(24)
	s_cmp_lg_u32 s100, 0
	s_cbranch_scc1 .Lgrx_10
	s_waitcnt vmcnt(8)
.Lgrx_10:
	s_mov_b32 s100, 0
	s_waitcnt lgkmcnt(0)
	s_barrier
	s_setprio 1
	s_waitcnt lgkmcnt(0)
	v_mfma_f32_16x16x32_bf16 v[60:63], v[150:153], v[190:193], v[60:63]
	v_mfma_f32_16x16x32_bf16 v[56:59], v[166:169], v[190:193], v[56:59]
	v_mfma_f32_16x16x32_bf16 v[52:55], v[150:153], v[194:197], v[52:55]
	v_mfma_f32_16x16x32_bf16 v[44:47], v[166:169], v[194:197], v[44:47]
	v_mfma_f32_16x16x32_bf16 v[36:39], v[150:153], v[206:209], v[36:39]
	v_mfma_f32_16x16x32_bf16 v[28:31], v[166:169], v[206:209], v[28:31]
	v_mfma_f32_16x16x32_bf16 v[20:23], v[150:153], v[210:213], v[20:23]
	v_mfma_f32_16x16x32_bf16 v[12:15], v[166:169], v[210:213], v[12:15]
	v_mfma_f32_16x16x32_bf16 v[60:63], v[154:157], v[198:201], v[60:63]
	v_mfma_f32_16x16x32_bf16 v[56:59], v[170:173], v[198:201], v[56:59]
	v_mfma_f32_16x16x32_bf16 v[52:55], v[154:157], v[202:205], v[52:55]
	v_mfma_f32_16x16x32_bf16 v[44:47], v[170:173], v[202:205], v[44:47]
	v_mfma_f32_16x16x32_bf16 v[36:39], v[154:157], v[214:217], v[36:39]
	v_mfma_f32_16x16x32_bf16 v[28:31], v[170:173], v[214:217], v[28:31]
	v_mfma_f32_16x16x32_bf16 v[20:23], v[154:157], v[226:229], v[20:23]
	v_mfma_f32_16x16x32_bf16 v[12:15], v[170:173], v[226:229], v[12:15]
	s_setprio 0
	s_setprio 1
	v_mfma_f32_16x16x32_bf16 v[48:51], v[174:177], v[190:193], v[48:51]
	v_mfma_f32_16x16x32_bf16 v[40:43], v[182:185], v[190:193], v[40:43]
	v_mfma_f32_16x16x32_bf16 v[32:35], v[174:177], v[194:197], v[32:35]
	v_mfma_f32_16x16x32_bf16 v[24:27], v[182:185], v[194:197], v[24:27]
	v_mfma_f32_16x16x32_bf16 v[16:19], v[174:177], v[206:209], v[16:19]
	v_mfma_f32_16x16x32_bf16 v[8:11], v[182:185], v[206:209], v[8:11]
	v_mfma_f32_16x16x32_bf16 v[4:7], v[174:177], v[210:213], v[4:7]
	v_mfma_f32_16x16x32_bf16 v[0:3], v[182:185], v[210:213], v[0:3]
	v_mfma_f32_16x16x32_bf16 v[48:51], v[178:181], v[198:201], v[48:51]
	v_mfma_f32_16x16x32_bf16 v[40:43], v[186:189], v[198:201], v[40:43]
	v_mfma_f32_16x16x32_bf16 v[32:35], v[178:181], v[202:205], v[32:35]
	v_mfma_f32_16x16x32_bf16 v[24:27], v[186:189], v[202:205], v[24:27]
	v_mfma_f32_16x16x32_bf16 v[16:19], v[178:181], v[214:217], v[16:19]
	v_mfma_f32_16x16x32_bf16 v[8:11], v[186:189], v[214:217], v[8:11]
	v_mfma_f32_16x16x32_bf16 v[4:7], v[178:181], v[226:229], v[4:7]
	v_mfma_f32_16x16x32_bf16 v[0:3], v[186:189], v[226:229], v[0:3]
	s_setprio 0
	s_barrier
	s_add_i32 s65, 0, 0x18000
	v_add_u32_e32 v149, s65, v140
	v_add_u32_e32 v154, s65, v144
	ds_read_b128 v[150:153], v149
	ds_read_b128 v[154:157], v154
	v_add_u32_e32 v149, s87, v140
	s_add_i32 s73, 0, 0x1c000
	v_add_u32_e32 v162, s87, v144
	ds_read_b128 v[166:169], v149
	ds_read_b128 v[170:173], v162
	v_add_u32_e32 v149, s73, v140
	v_add_u32_e32 v162, s73, v144
	ds_read_b128 v[174:177], v149
	ds_read_b128 v[178:181], v162
	v_add_u32_e32 v149, s2, v140
	v_add_u32_e32 v162, s2, v144
	ds_read_b128 v[182:185], v149
	ds_read_b128 v[186:189], v162
	s_add_u32 s30, s30, 0x200000
	s_addc_u32 s31, s31, 0
	s_mov_b32 m0, s43
	v_lshl_add_u64 v[234:235], s[30:31], 0, v[134:135]
	ds_read_b128 v[190:193], v145 offset:32768
	ds_read_b128 v[194:197], v145 offset:34816
	ds_read_b128 v[198:201], v146 offset:32768
	ds_read_b128 v[202:205], v146 offset:34816
	ds_read_b128 v[206:209], v145 offset:36864
	ds_read_b128 v[210:213], v145 offset:38912
	ds_read_b128 v[214:217], v146 offset:36864
	ds_read_b128 v[226:229], v146 offset:38912
	global_load_lds_dwordx4 v[234:235], off
	v_lshl_add_u64 v[234:235], s[30:31], 0, v[130:131]
	s_mov_b32 m0, s46
	s_nop 0
	global_load_lds_dwordx4 v[234:235], off
	s_waitcnt vmcnt(8)
	s_waitcnt lgkmcnt(0)
	s_barrier
	s_setprio 1
	s_waitcnt lgkmcnt(0)
	v_mfma_f32_16x16x32_bf16 v[124:127], v[150:153], v[190:193], v[124:127]
	v_mfma_f32_16x16x32_bf16 v[120:123], v[166:169], v[190:193], v[120:123]
	v_mfma_f32_16x16x32_bf16 v[116:119], v[150:153], v[194:197], v[116:119]
	v_mfma_f32_16x16x32_bf16 v[112:115], v[166:169], v[194:197], v[112:115]
	v_mfma_f32_16x16x32_bf16 v[100:103], v[150:153], v[206:209], v[100:103]
	v_mfma_f32_16x16x32_bf16 v[96:99], v[166:169], v[206:209], v[96:99]
	v_mfma_f32_16x16x32_bf16 v[84:87], v[150:153], v[210:213], v[84:87]
	v_mfma_f32_16x16x32_bf16 v[76:79], v[166:169], v[210:213], v[76:79]
	v_mfma_f32_16x16x32_bf16 v[124:127], v[154:157], v[198:201], v[124:127]
	v_mfma_f32_16x16x32_bf16 v[120:123], v[170:173], v[198:201], v[120:123]
	v_mfma_f32_16x16x32_bf16 v[116:119], v[154:157], v[202:205], v[116:119]
	v_mfma_f32_16x16x32_bf16 v[112:115], v[170:173], v[202:205], v[112:115]
	v_mfma_f32_16x16x32_bf16 v[100:103], v[154:157], v[214:217], v[100:103]
	v_mfma_f32_16x16x32_bf16 v[96:99], v[170:173], v[214:217], v[96:99]
	v_mfma_f32_16x16x32_bf16 v[84:87], v[154:157], v[226:229], v[84:87]
	v_mfma_f32_16x16x32_bf16 v[76:79], v[170:173], v[226:229], v[76:79]
	s_setprio 0
	s_setprio 1
	v_mfma_f32_16x16x32_bf16 v[108:111], v[174:177], v[190:193], v[108:111]
	v_mfma_f32_16x16x32_bf16 v[104:107], v[182:185], v[190:193], v[104:107]
	v_mfma_f32_16x16x32_bf16 v[92:95], v[174:177], v[194:197], v[92:95]
	v_mfma_f32_16x16x32_bf16 v[88:91], v[182:185], v[194:197], v[88:91]
	v_mfma_f32_16x16x32_bf16 v[80:83], v[174:177], v[206:209], v[80:83]
	v_mfma_f32_16x16x32_bf16 v[72:75], v[182:185], v[206:209], v[72:75]
	v_mfma_f32_16x16x32_bf16 v[68:71], v[174:177], v[210:213], v[68:71]
	v_mfma_f32_16x16x32_bf16 v[64:67], v[182:185], v[210:213], v[64:67]
	v_mfma_f32_16x16x32_bf16 v[108:111], v[178:181], v[198:201], v[108:111]
	v_mfma_f32_16x16x32_bf16 v[104:107], v[186:189], v[198:201], v[104:107]
	v_mfma_f32_16x16x32_bf16 v[92:95], v[178:181], v[202:205], v[92:95]
	v_mfma_f32_16x16x32_bf16 v[88:91], v[186:189], v[202:205], v[88:91]
	v_mfma_f32_16x16x32_bf16 v[80:83], v[178:181], v[214:217], v[80:83]
	v_mfma_f32_16x16x32_bf16 v[72:75], v[186:189], v[214:217], v[72:75]
	v_mfma_f32_16x16x32_bf16 v[68:71], v[178:181], v[226:229], v[68:71]
	v_mfma_f32_16x16x32_bf16 v[64:67], v[186:189], v[226:229], v[64:67]
	s_setprio 0
	s_barrier
	s_add_i32 s30, s65, s36
	v_lshl_add_u64 v[158:159], v[158:159], 0, s[54:55]
	s_mov_b32 m0, s30
	ds_read_b128 v[190:193], v145 offset:49152
	ds_read_b128 v[194:197], v145 offset:51200
	ds_read_b128 v[198:201], v146 offset:49152
	ds_read_b128 v[202:205], v146 offset:51200
	ds_read_b128 v[206:209], v145 offset:53248
	ds_read_b128 v[210:213], v145 offset:55296
	ds_read_b128 v[214:217], v146 offset:53248
	ds_read_b128 v[226:229], v146 offset:55296
	global_load_lds_dwordx4 v[158:159], off
	s_add_i32 m0, s30, 0x2000
	s_add_u32 s20, s20, 0x8080
	v_lshl_add_u64 v[158:159], v[218:219], 0, s[54:55]
	s_addc_u32 s21, s21, 0
	s_add_i32 s30, s73, s36
	global_load_lds_dwordx4 v[158:159], off
	v_lshl_add_u64 v[158:159], s[20:21], 0, v[132:133]
	s_mov_b32 m0, s30
	s_nop 0
	global_load_lds_dwordx4 v[158:159], off
	v_lshl_add_u64 v[158:159], s[20:21], 0, v[128:129]
	s_add_i32 m0, s30, 0x2000
	s_nop 0
	global_load_lds_dwordx4 v[158:159], off
	v_lshl_add_u64 v[158:159], v[230:231], 0, s[54:55]
	s_mov_b32 m0, s47
	s_nop 0
	global_load_lds_dwordx4 v[158:159], off
	v_lshl_add_u64 v[158:159], v[232:233], 0, s[54:55]
	s_mov_b32 m0, s56
	s_nop 0
	global_load_lds_dwordx4 v[158:159], off
	s_waitcnt vmcnt(8)
	s_waitcnt lgkmcnt(0)
	s_barrier
	s_setprio 1
	s_waitcnt lgkmcnt(0)
	v_mfma_f32_16x16x32_bf16 v[60:63], v[150:153], v[190:193], v[60:63]
	v_mfma_f32_16x16x32_bf16 v[56:59], v[166:169], v[190:193], v[56:59]
	v_mfma_f32_16x16x32_bf16 v[52:55], v[150:153], v[194:197], v[52:55]
	v_mfma_f32_16x16x32_bf16 v[44:47], v[166:169], v[194:197], v[44:47]
	v_mfma_f32_16x16x32_bf16 v[36:39], v[150:153], v[206:209], v[36:39]
	v_mfma_f32_16x16x32_bf16 v[28:31], v[166:169], v[206:209], v[28:31]
	v_mfma_f32_16x16x32_bf16 v[20:23], v[150:153], v[210:213], v[20:23]
	v_mfma_f32_16x16x32_bf16 v[12:15], v[166:169], v[210:213], v[12:15]
	v_mfma_f32_16x16x32_bf16 v[60:63], v[154:157], v[198:201], v[60:63]
	v_mfma_f32_16x16x32_bf16 v[56:59], v[170:173], v[198:201], v[56:59]
	v_mfma_f32_16x16x32_bf16 v[52:55], v[154:157], v[202:205], v[52:55]
	v_mfma_f32_16x16x32_bf16 v[44:47], v[170:173], v[202:205], v[44:47]
	v_mfma_f32_16x16x32_bf16 v[36:39], v[154:157], v[214:217], v[36:39]
	v_mfma_f32_16x16x32_bf16 v[28:31], v[170:173], v[214:217], v[28:31]
	v_mfma_f32_16x16x32_bf16 v[20:23], v[154:157], v[226:229], v[20:23]
	v_mfma_f32_16x16x32_bf16 v[12:15], v[170:173], v[226:229], v[12:15]
	s_setprio 0
	s_setprio 1
	v_mfma_f32_16x16x32_bf16 v[48:51], v[174:177], v[190:193], v[48:51]
	v_mfma_f32_16x16x32_bf16 v[40:43], v[182:185], v[190:193], v[40:43]
	v_mfma_f32_16x16x32_bf16 v[32:35], v[174:177], v[194:197], v[32:35]
	v_mfma_f32_16x16x32_bf16 v[24:27], v[182:185], v[194:197], v[24:27]
	v_mfma_f32_16x16x32_bf16 v[16:19], v[174:177], v[206:209], v[16:19]
	v_mfma_f32_16x16x32_bf16 v[8:11], v[182:185], v[206:209], v[8:11]
	v_mfma_f32_16x16x32_bf16 v[4:7], v[174:177], v[210:213], v[4:7]
	v_mfma_f32_16x16x32_bf16 v[0:3], v[182:185], v[210:213], v[0:3]
	v_mfma_f32_16x16x32_bf16 v[48:51], v[178:181], v[198:201], v[48:51]
	v_mfma_f32_16x16x32_bf16 v[40:43], v[186:189], v[198:201], v[40:43]
	v_mfma_f32_16x16x32_bf16 v[32:35], v[178:181], v[202:205], v[32:35]
	v_mfma_f32_16x16x32_bf16 v[24:27], v[186:189], v[202:205], v[24:27]
	v_mfma_f32_16x16x32_bf16 v[16:19], v[178:181], v[214:217], v[16:19]
	v_mfma_f32_16x16x32_bf16 v[8:11], v[186:189], v[214:217], v[8:11]
	v_mfma_f32_16x16x32_bf16 v[4:7], v[178:181], v[226:229], v[4:7]
	v_mfma_f32_16x16x32_bf16 v[0:3], v[186:189], v[226:229], v[0:3]
	s_setprio 0
	s_barrier
	s_add_i32 s72, s72, 2
	s_add_u32 s18, s18, 0x100
	s_addc_u32 s19, s19, 0
	s_add_u32 s70, s70, 0x100
	s_addc_u32 s71, s71, 0
	s_cmp_gt_u32 s72, 5
	s_cbranch_scc0 .LBB0_856
	s_mov_b32 s100, 1
	s_and_b64 vcc, exec, s[10:11]
	s_cbranch_vccz .LBB0_859
	s_barrier

.LBB0_901:
	v_mov_b32_e32 v133, v161
	v_lshl_add_u64 v[6:7], s[20:21], 0, v[132:133]
	v_mov_b32_e32 v129, v161
	v_readlane_b32 s18, v254, 25
	v_lshl_add_u64 v[8:9], s[20:21], 0, v[128:129]
	v_mov_b32_e32 v135, v161
	v_readlane_b32 s19, v254, 26
	s_add_i32 m0, s37, 0x18000
	v_lshl_add_u64 v[6:7], v[6:7], 0, s[54:55]
	v_lshl_add_u64 v[10:11], s[18:19], 0, v[134:135]
	v_mov_b32_e32 v131, v161
	s_and_b32 s10, s8, 3
	s_lshl_b32 s11, s7, 6
	s_mov_b32 s100, 0
	s_waitcnt vmcnt(2)
	s_barrier
	global_load_lds_dwordx4 v[6:7], off
	v_lshl_add_u64 v[6:7], v[8:9], 0, s[54:55]
	s_add_i32 m0, s37, 0x1a000
	s_add_i32 s47, s37, 0x8000
	s_add_i32 s56, s37, 0xa000
	v_lshl_add_u64 v[12:13], s[18:19], 0, v[130:131]
	global_load_lds_dwordx4 v[6:7], off
	v_lshl_add_u64 v[6:7], v[10:11], 0, s[54:55]
	s_mov_b32 m0, s47
	s_add_u32 s8, s20, 0x40080
	global_load_lds_dwordx4 v[6:7], off
	v_lshl_add_u64 v[6:7], v[12:13], 0, s[54:55]
	s_mov_b32 m0, s56
	s_addc_u32 s9, s21, 0
	global_load_lds_dwordx4 v[6:7], off
	s_add_i32 m0, s37, 0x1c000
	v_lshl_add_u64 v[6:7], s[8:9], 0, v[132:133]
	global_load_lds_dwordx4 v[6:7], off
	v_lshl_add_u64 v[6:7], s[8:9], 0, v[128:129]
	s_add_i32 m0, s37, 0x1e000
	s_cmpk_lt_u32 s6, 0x100
	global_load_lds_dwordx4 v[6:7], off
	s_cselect_b64 s[8:9], -1, 0
	s_lshl_b32 s6, s7, 13
	v_and_b32_e32 v5, 7, v0
	v_bfe_u32 v16, v0, 1, 3
	s_lshl_b32 s7, s10, 11
	s_add_i32 s6, s6, 0
	v_and_b32_e32 v14, 15, v0
	v_bitop3_b32 v16, v3, v16, 3 bitop3:0x6c
	s_add_i32 s6, s6, s7
	v_bfe_u32 v6, v0, 3, 3
	v_bitop3_b32 v3, v3, v5, 3 bitop3:0x6c
	v_or_b32_e32 v15, s11, v14
	v_lshlrev_b32_e32 v16, 4, v16
	v_lshlrev_b32_e32 v18, 7, v14
	s_add_i32 s6, s6, 0x20000
	v_cmp_gt_u32_e32 vcc, 8, v14
	v_lshlrev_b32_e32 v8, 7, v6
	v_lshlrev_b32_e32 v3, 4, v3
	v_and_b32_e32 v0, 4, v0
	v_lshlrev_b32_e32 v15, 7, v15
	s_waitcnt vmcnt(6)
	v_add3_u32 v141, s6, v18, v16
	v_cndmask_b32_e64 v7, v224, 64, vcc
	v_add3_u32 v142, s6, v8, v3
	v_cmp_eq_u32_e32 vcc, 0, v0
	s_lshl_b32 s6, s10, 6
	v_or_b32_e32 v17, v15, v16
	v_lshl_or_b32 v19, s10, 12, v18
	v_cndmask_b32_e64 v3, v224, 64, vcc
	v_lshlrev_b32_e32 v0, 3, v5
	v_bitop3_b32 v5, v15, 64, v16 bitop3:0x36
	s_lshl_b32 s80, s6, 1
	v_readlane_b32 s6, v254, 31
	v_or_b32_e32 v140, v19, v16
	s_mov_b32 s57, 0
	v_or_b32_e32 v143, s11, v6
	v_bitop3_b32 v144, v19, 64, v16 bitop3:0x36
	v_add_u32_e32 v136, v4, v1
	v_mov_b32_e32 v137, v161
	v_add_u32_e32 v138, v2, v1
	v_mov_b32_e32 v139, v161
	v_add_u32_e32 v145, 0, v17
	v_add_u32_e32 v146, 0, v5
	v_lshlrev_b32_e32 v160, 1, v0
	v_add_u32_e32 v147, v141, v7
	v_add_u32_e32 v148, v142, v3
	v_readlane_b32 s58, v254, 48
	s_mov_b32 s59, s6
	s_barrier
	v_readlane_b32 s7, v254, 32
	s_branch .LBB0_904

.LBB0_907:
	s_add_u32 s20, s18, 0xfff00080
	s_addc_u32 s21, s19, -1
	s_add_i32 s65, 0, 0x10000
	s_cmp_eq_u32 s73, 60
	v_add_u32_e32 v149, s65, v140
	v_add_u32_e32 v154, s65, v144
	s_cselect_b32 s31, s13, s21
	s_cselect_b32 s30, s69, s20
	ds_read_b128 v[150:153], v149
	ds_read_b128 v[154:157], v154
	v_add_u32_e32 v149, s1, v140
	s_cselect_b32 s21, s11, s72
	s_cselect_b32 s20, s70, s71
	s_add_i32 s84, 0, 0x14000
	v_add_u32_e32 v158, s1, v144
	ds_read_b128 v[166:169], v149
	ds_read_b128 v[170:173], v158
	v_add_u32_e32 v149, s84, v140
	v_add_u32_e32 v158, s84, v144
	ds_read_b128 v[174:177], v149
	ds_read_b128 v[178:181], v158
	v_add_u32_e32 v149, s86, v140
	v_add_u32_e32 v158, s86, v144
	ds_read_b128 v[182:185], v149
	ds_read_b128 v[186:189], v158
	v_lshl_add_u64 v[158:159], s[18:19], 0, v[136:137]
	s_add_i32 m0, s37, 0xc000
	ds_read_b128 v[190:193], v145
	ds_read_b128 v[194:197], v145 offset:2048
	ds_read_b128 v[198:201], v146
	ds_read_b128 v[202:205], v146 offset:2048
	ds_read_b128 v[206:209], v145 offset:4096
	ds_read_b128 v[210:213], v145 offset:6144
	ds_read_b128 v[214:217], v146 offset:4096
	ds_read_b128 v[226:229], v146 offset:6144
	global_load_lds_dwordx4 v[158:159], off
	v_lshl_add_u64 v[158:159], s[18:19], 0, v[138:139]
	s_add_i32 m0, s37, 0xe000
	s_nop 0
	global_load_lds_dwordx4 v[158:159], off
	s_waitcnt vmcnt(24)
	s_cmp_lg_u32 s100, 0
	s_cbranch_scc1 .Lgrx_11
	s_waitcnt vmcnt(8)
.Lgrx_11:
	s_waitcnt lgkmcnt(0)
	s_barrier
	s_setprio 1
	s_waitcnt lgkmcnt(0)
	v_mfma_f32_16x16x32_bf16 v[124:127], v[150:153], v[190:193], v[124:127]
	v_mfma_f32_16x16x32_bf16 v[120:123], v[166:169], v[190:193], v[120:123]
	v_mfma_f32_16x16x32_bf16 v[116:119], v[150:153], v[194:197], v[116:119]
	v_mfma_f32_16x16x32_bf16 v[112:115], v[166:169], v[194:197], v[112:115]
	v_mfma_f32_16x16x32_bf16 v[100:103], v[150:153], v[206:209], v[100:103]
	v_mfma_f32_16x16x32_bf16 v[96:99], v[166:169], v[206:209], v[96:99]
	v_mfma_f32_16x16x32_bf16 v[84:87], v[150:153], v[210:213], v[84:87]
	v_mfma_f32_16x16x32_bf16 v[76:79], v[166:169], v[210:213], v[76:79]
	v_mfma_f32_16x16x32_bf16 v[124:127], v[154:157], v[198:201], v[124:127]
	v_mfma_f32_16x16x32_bf16 v[120:123], v[170:173], v[198:201], v[120:123]
	v_mfma_f32_16x16x32_bf16 v[116:119], v[154:157], v[202:205], v[116:119]
	v_mfma_f32_16x16x32_bf16 v[112:115], v[170:173], v[202:205], v[112:115]
	v_mfma_f32_16x16x32_bf16 v[100:103], v[154:157], v[214:217], v[100:103]
	v_mfma_f32_16x16x32_bf16 v[96:99], v[170:173], v[214:217], v[96:99]
	v_mfma_f32_16x16x32_bf16 v[84:87], v[154:157], v[226:229], v[84:87]
	v_mfma_f32_16x16x32_bf16 v[76:79], v[170:173], v[226:229], v[76:79]
	s_setprio 0
	s_setprio 1
	v_mfma_f32_16x16x32_bf16 v[108:111], v[174:177], v[190:193], v[108:111]
	v_mfma_f32_16x16x32_bf16 v[104:107], v[182:185], v[190:193], v[104:107]
	v_mfma_f32_16x16x32_bf16 v[92:95], v[174:177], v[194:197], v[92:95]
	v_mfma_f32_16x16x32_bf16 v[88:91], v[182:185], v[194:197], v[88:91]
	v_mfma_f32_16x16x32_bf16 v[80:83], v[174:177], v[206:209], v[80:83]
	v_mfma_f32_16x16x32_bf16 v[72:75], v[182:185], v[206:209], v[72:75]
	v_mfma_f32_16x16x32_bf16 v[68:71], v[174:177], v[210:213], v[68:71]
	v_mfma_f32_16x16x32_bf16 v[64:67], v[182:185], v[210:213], v[64:67]
	v_mfma_f32_16x16x32_bf16 v[108:111], v[178:181], v[198:201], v[108:111]
	v_mfma_f32_16x16x32_bf16 v[104:107], v[186:189], v[198:201], v[104:107]
	v_mfma_f32_16x16x32_bf16 v[92:95], v[178:181], v[202:205], v[92:95]
	v_mfma_f32_16x16x32_bf16 v[88:91], v[186:189], v[202:205], v[88:91]
	v_mfma_f32_16x16x32_bf16 v[80:83], v[178:181], v[214:217], v[80:83]
	v_mfma_f32_16x16x32_bf16 v[72:75], v[186:189], v[214:217], v[72:75]
	v_mfma_f32_16x16x32_bf16 v[68:71], v[178:181], v[226:229], v[68:71]
	v_mfma_f32_16x16x32_bf16 v[64:67], v[186:189], v[226:229], v[64:67]
	s_setprio 0
	s_barrier
	s_add_i32 s65, s65, s36
	v_lshl_add_u64 v[158:159], s[20:21], 0, v[132:133]
	s_mov_b32 m0, s65
	ds_read_b128 v[190:193], v145 offset:16384
	ds_read_b128 v[194:197], v145 offset:18432
	ds_read_b128 v[198:201], v146 offset:16384
	ds_read_b128 v[202:205], v146 offset:18432
	ds_read_b128 v[206:209], v145 offset:20480
	ds_read_b128 v[210:213], v145 offset:22528
	ds_read_b128 v[214:217], v146 offset:20480
	ds_read_b128 v[226:229], v146 offset:22528
	global_load_lds_dwordx4 v[158:159], off
	s_add_i32 m0, s65, 0x2000
	s_add_u32 s76, s20, 0x40000
	v_lshl_add_u64 v[218:219], s[20:21], 0, v[128:129]
	s_addc_u32 s77, s21, 0
	s_add_i32 s65, s84, s36
	global_load_lds_dwordx4 v[218:219], off
	v_lshl_add_u64 v[230:231], s[76:77], 0, v[132:133]
	s_mov_b32 m0, s65
	v_lshl_add_u64 v[232:233], s[30:31], 0, v[130:131]
	global_load_lds_dwordx4 v[230:231], off
	v_lshl_add_u64 v[230:231], s[76:77], 0, v[128:129]
	s_add_i32 m0, s65, 0x2000
	s_nop 0
	global_load_lds_dwordx4 v[230:231], off
	v_lshl_add_u64 v[230:231], s[30:31], 0, v[134:135]
	s_mov_b32 m0, s37
	s_nop 0
	global_load_lds_dwordx4 v[230:231], off
	s_mov_b32 m0, s41
	s_nop 0
	global_load_lds_dwordx4 v[232:233], off
	s_waitcnt vmcnt(24)
	s_cmp_lg_u32 s100, 0
	s_cbranch_scc1 .Lgrx_12
	s_waitcnt vmcnt(8)
.Lgrx_12:
	s_mov_b32 s100, 0
	s_waitcnt lgkmcnt(0)
	s_barrier
	s_setprio 1
	s_waitcnt lgkmcnt(0)
	v_mfma_f32_16x16x32_bf16 v[60:63], v[150:153], v[190:193], v[60:63]
	v_mfma_f32_16x16x32_bf16 v[56:59], v[166:169], v[190:193], v[56:59]
	v_mfma_f32_16x16x32_bf16 v[52:55], v[150:153], v[194:197], v[52:55]
	v_mfma_f32_16x16x32_bf16 v[44:47], v[166:169], v[194:197], v[44:47]
	v_mfma_f32_16x16x32_bf16 v[36:39], v[150:153], v[206:209], v[36:39]
	v_mfma_f32_16x16x32_bf16 v[28:31], v[166:169], v[206:209], v[28:31]
	v_mfma_f32_16x16x32_bf16 v[20:23], v[150:153], v[210:213], v[20:23]
	v_mfma_f32_16x16x32_bf16 v[12:15], v[166:169], v[210:213], v[12:15]
	v_mfma_f32_16x16x32_bf16 v[60:63], v[154:157], v[198:201], v[60:63]
	v_mfma_f32_16x16x32_bf16 v[56:59], v[170:173], v[198:201], v[56:59]
	v_mfma_f32_16x16x32_bf16 v[52:55], v[154:157], v[202:205], v[52:55]
	v_mfma_f32_16x16x32_bf16 v[44:47], v[170:173], v[202:205], v[44:47]
	v_mfma_f32_16x16x32_bf16 v[36:39], v[154:157], v[214:217], v[36:39]
	v_mfma_f32_16x16x32_bf16 v[28:31], v[170:173], v[214:217], v[28:31]
	v_mfma_f32_16x16x32_bf16 v[20:23], v[154:157], v[226:229], v[20:23]
	v_mfma_f32_16x16x32_bf16 v[12:15], v[170:173], v[226:229], v[12:15]
	s_setprio 0
	s_setprio 1
	v_mfma_f32_16x16x32_bf16 v[48:51], v[174:177], v[190:193], v[48:51]
	v_mfma_f32_16x16x32_bf16 v[40:43], v[182:185], v[190:193], v[40:43]
	v_mfma_f32_16x16x32_bf16 v[32:35], v[174:177], v[194:197], v[32:35]
	v_mfma_f32_16x16x32_bf16 v[24:27], v[182:185], v[194:197], v[24:27]
	v_mfma_f32_16x16x32_bf16 v[16:19], v[174:177], v[206:209], v[16:19]
	v_mfma_f32_16x16x32_bf16 v[8:11], v[182:185], v[206:209], v[8:11]
	v_mfma_f32_16x16x32_bf16 v[4:7], v[174:177], v[210:213], v[4:7]
	v_mfma_f32_16x16x32_bf16 v[0:3], v[182:185], v[210:213], v[0:3]
	v_mfma_f32_16x16x32_bf16 v[48:51], v[178:181], v[198:201], v[48:51]
	v_mfma_f32_16x16x32_bf16 v[40:43], v[186:189], v[198:201], v[40:43]
	v_mfma_f32_16x16x32_bf16 v[32:35], v[178:181], v[202:205], v[32:35]
	v_mfma_f32_16x16x32_bf16 v[24:27], v[186:189], v[202:205], v[24:27]
	v_mfma_f32_16x16x32_bf16 v[16:19], v[178:181], v[214:217], v[16:19]
	v_mfma_f32_16x16x32_bf16 v[8:11], v[186:189], v[214:217], v[8:11]
	v_mfma_f32_16x16x32_bf16 v[4:7], v[178:181], v[226:229], v[4:7]
	v_mfma_f32_16x16x32_bf16 v[0:3], v[186:189], v[226:229], v[0:3]
	s_setprio 0
	s_barrier
	s_add_i32 s65, 0, 0x18000
	v_add_u32_e32 v149, s65, v140
	v_add_u32_e32 v154, s65, v144
	ds_read_b128 v[150:153], v149
	ds_read_b128 v[154:157], v154
	v_add_u32_e32 v149, s87, v140
	s_add_i32 s76, 0, 0x1c000
	v_add_u32_e32 v162, s87, v144
	ds_read_b128 v[166:169], v149
	ds_read_b128 v[170:173], v162
	v_add_u32_e32 v149, s76, v140
	v_add_u32_e32 v162, s76, v144
	ds_read_b128 v[174:177], v149
	ds_read_b128 v[178:181], v162
	v_add_u32_e32 v149, s2, v140
	v_add_u32_e32 v162, s2, v144
	ds_read_b128 v[182:185], v149
	ds_read_b128 v[186:189], v162
	s_add_u32 s30, s30, 0x100000
	s_addc_u32 s31, s31, 0
	s_mov_b32 m0, s43
	v_lshl_add_u64 v[234:235], s[30:31], 0, v[134:135]
	ds_read_b128 v[190:193], v145 offset:32768
	ds_read_b128 v[194:197], v145 offset:34816
	ds_read_b128 v[198:201], v146 offset:32768
	ds_read_b128 v[202:205], v146 offset:34816
	ds_read_b128 v[206:209], v145 offset:36864
	ds_read_b128 v[210:213], v145 offset:38912
	ds_read_b128 v[214:217], v146 offset:36864
	ds_read_b128 v[226:229], v146 offset:38912
	global_load_lds_dwordx4 v[234:235], off
	v_lshl_add_u64 v[234:235], s[30:31], 0, v[130:131]
	s_mov_b32 m0, s46
	s_nop 0
	global_load_lds_dwordx4 v[234:235], off
	s_waitcnt vmcnt(8)
	s_waitcnt lgkmcnt(0)
	s_barrier
	s_setprio 1
	s_waitcnt lgkmcnt(0)
	v_mfma_f32_16x16x32_bf16 v[124:127], v[150:153], v[190:193], v[124:127]
	v_mfma_f32_16x16x32_bf16 v[120:123], v[166:169], v[190:193], v[120:123]
	v_mfma_f32_16x16x32_bf16 v[116:119], v[150:153], v[194:197], v[116:119]
	v_mfma_f32_16x16x32_bf16 v[112:115], v[166:169], v[194:197], v[112:115]
	v_mfma_f32_16x16x32_bf16 v[100:103], v[150:153], v[206:209], v[100:103]
	v_mfma_f32_16x16x32_bf16 v[96:99], v[166:169], v[206:209], v[96:99]
	v_mfma_f32_16x16x32_bf16 v[84:87], v[150:153], v[210:213], v[84:87]
	v_mfma_f32_16x16x32_bf16 v[76:79], v[166:169], v[210:213], v[76:79]
	v_mfma_f32_16x16x32_bf16 v[124:127], v[154:157], v[198:201], v[124:127]
	v_mfma_f32_16x16x32_bf16 v[120:123], v[170:173], v[198:201], v[120:123]
	v_mfma_f32_16x16x32_bf16 v[116:119], v[154:157], v[202:205], v[116:119]
	v_mfma_f32_16x16x32_bf16 v[112:115], v[170:173], v[202:205], v[112:115]
	v_mfma_f32_16x16x32_bf16 v[100:103], v[154:157], v[214:217], v[100:103]
	v_mfma_f32_16x16x32_bf16 v[96:99], v[170:173], v[214:217], v[96:99]
	v_mfma_f32_16x16x32_bf16 v[84:87], v[154:157], v[226:229], v[84:87]
	v_mfma_f32_16x16x32_bf16 v[76:79], v[170:173], v[226:229], v[76:79]
	s_setprio 0
	s_setprio 1
	v_mfma_f32_16x16x32_bf16 v[108:111], v[174:177], v[190:193], v[108:111]
	v_mfma_f32_16x16x32_bf16 v[104:107], v[182:185], v[190:193], v[104:107]
	v_mfma_f32_16x16x32_bf16 v[92:95], v[174:177], v[194:197], v[92:95]
	v_mfma_f32_16x16x32_bf16 v[88:91], v[182:185], v[194:197], v[88:91]
	v_mfma_f32_16x16x32_bf16 v[80:83], v[174:177], v[206:209], v[80:83]
	v_mfma_f32_16x16x32_bf16 v[72:75], v[182:185], v[206:209], v[72:75]
	v_mfma_f32_16x16x32_bf16 v[68:71], v[174:177], v[210:213], v[68:71]
	v_mfma_f32_16x16x32_bf16 v[64:67], v[182:185], v[210:213], v[64:67]
	v_mfma_f32_16x16x32_bf16 v[108:111], v[178:181], v[198:201], v[108:111]
	v_mfma_f32_16x16x32_bf16 v[104:107], v[186:189], v[198:201], v[104:107]
	v_mfma_f32_16x16x32_bf16 v[92:95], v[178:181], v[202:205], v[92:95]
	v_mfma_f32_16x16x32_bf16 v[88:91], v[186:189], v[202:205], v[88:91]
	v_mfma_f32_16x16x32_bf16 v[80:83], v[178:181], v[214:217], v[80:83]
	v_mfma_f32_16x16x32_bf16 v[72:75], v[186:189], v[214:217], v[72:75]
	v_mfma_f32_16x16x32_bf16 v[68:71], v[178:181], v[226:229], v[68:71]
	v_mfma_f32_16x16x32_bf16 v[64:67], v[186:189], v[226:229], v[64:67]
	s_setprio 0
	s_barrier
	s_add_i32 s30, s65, s36
	v_lshl_add_u64 v[158:159], v[158:159], 0, s[54:55]
	s_mov_b32 m0, s30
	ds_read_b128 v[190:193], v145 offset:49152
	ds_read_b128 v[194:197], v145 offset:51200
	ds_read_b128 v[198:201], v146 offset:49152
	ds_read_b128 v[202:205], v146 offset:51200
	ds_read_b128 v[206:209], v145 offset:53248
	ds_read_b128 v[210:213], v145 offset:55296
	ds_read_b128 v[214:217], v146 offset:53248
	ds_read_b128 v[226:229], v146 offset:55296
	global_load_lds_dwordx4 v[158:159], off
	s_add_i32 m0, s30, 0x2000
	s_add_u32 s20, s20, 0x40080
	v_lshl_add_u64 v[158:159], v[218:219], 0, s[54:55]
	s_addc_u32 s21, s21, 0
	s_add_i32 s30, s76, s36
	global_load_lds_dwordx4 v[158:159], off
	v_lshl_add_u64 v[158:159], s[20:21], 0, v[132:133]
	s_mov_b32 m0, s30
	s_nop 0
	global_load_lds_dwordx4 v[158:159], off
	v_lshl_add_u64 v[158:159], s[20:21], 0, v[128:129]
	s_add_i32 m0, s30, 0x2000
	s_nop 0
	global_load_lds_dwordx4 v[158:159], off
	v_lshl_add_u64 v[158:159], v[230:231], 0, s[54:55]
	s_mov_b32 m0, s47
	s_nop 0
	global_load_lds_dwordx4 v[158:159], off
	v_lshl_add_u64 v[158:159], v[232:233], 0, s[54:55]
	s_mov_b32 m0, s56
	s_nop 0
	global_load_lds_dwordx4 v[158:159], off
	s_waitcnt vmcnt(8)
	s_waitcnt lgkmcnt(0)
	s_barrier
	s_setprio 1
	s_waitcnt lgkmcnt(0)
	v_mfma_f32_16x16x32_bf16 v[60:63], v[150:153], v[190:193], v[60:63]
	v_mfma_f32_16x16x32_bf16 v[56:59], v[166:169], v[190:193], v[56:59]
	v_mfma_f32_16x16x32_bf16 v[52:55], v[150:153], v[194:197], v[52:55]
	v_mfma_f32_16x16x32_bf16 v[44:47], v[166:169], v[194:197], v[44:47]
	v_mfma_f32_16x16x32_bf16 v[36:39], v[150:153], v[206:209], v[36:39]
	v_mfma_f32_16x16x32_bf16 v[28:31], v[166:169], v[206:209], v[28:31]
	v_mfma_f32_16x16x32_bf16 v[20:23], v[150:153], v[210:213], v[20:23]
	v_mfma_f32_16x16x32_bf16 v[12:15], v[166:169], v[210:213], v[12:15]
	v_mfma_f32_16x16x32_bf16 v[60:63], v[154:157], v[198:201], v[60:63]
	v_mfma_f32_16x16x32_bf16 v[56:59], v[170:173], v[198:201], v[56:59]
	v_mfma_f32_16x16x32_bf16 v[52:55], v[154:157], v[202:205], v[52:55]
	v_mfma_f32_16x16x32_bf16 v[44:47], v[170:173], v[202:205], v[44:47]
	v_mfma_f32_16x16x32_bf16 v[36:39], v[154:157], v[214:217], v[36:39]
	v_mfma_f32_16x16x32_bf16 v[28:31], v[170:173], v[214:217], v[28:31]
	v_mfma_f32_16x16x32_bf16 v[20:23], v[154:157], v[226:229], v[20:23]
	v_mfma_f32_16x16x32_bf16 v[12:15], v[170:173], v[226:229], v[12:15]
	s_setprio 0
	s_setprio 1
	v_mfma_f32_16x16x32_bf16 v[48:51], v[174:177], v[190:193], v[48:51]
	v_mfma_f32_16x16x32_bf16 v[40:43], v[182:185], v[190:193], v[40:43]
	v_mfma_f32_16x16x32_bf16 v[32:35], v[174:177], v[194:197], v[32:35]
	v_mfma_f32_16x16x32_bf16 v[24:27], v[182:185], v[194:197], v[24:27]
	v_mfma_f32_16x16x32_bf16 v[16:19], v[174:177], v[206:209], v[16:19]
	v_mfma_f32_16x16x32_bf16 v[8:11], v[182:185], v[206:209], v[8:11]
	v_mfma_f32_16x16x32_bf16 v[4:7], v[174:177], v[210:213], v[4:7]
	v_mfma_f32_16x16x32_bf16 v[0:3], v[182:185], v[210:213], v[0:3]
	v_mfma_f32_16x16x32_bf16 v[48:51], v[178:181], v[198:201], v[48:51]
	v_mfma_f32_16x16x32_bf16 v[40:43], v[186:189], v[198:201], v[40:43]
	v_mfma_f32_16x16x32_bf16 v[32:35], v[178:181], v[202:205], v[32:35]
	v_mfma_f32_16x16x32_bf16 v[24:27], v[186:189], v[202:205], v[24:27]
	v_mfma_f32_16x16x32_bf16 v[16:19], v[178:181], v[214:217], v[16:19]
	v_mfma_f32_16x16x32_bf16 v[8:11], v[186:189], v[214:217], v[8:11]
	v_mfma_f32_16x16x32_bf16 v[4:7], v[178:181], v[226:229], v[4:7]
	v_mfma_f32_16x16x32_bf16 v[0:3], v[186:189], v[226:229], v[0:3]
	s_setprio 0
	s_barrier
	s_add_i32 s73, s73, 2
	s_add_u32 s18, s18, 0x100
	s_addc_u32 s19, s19, 0
	s_add_u32 s71, s71, 0x100
	s_addc_u32 s72, s72, 0
	s_cmp_gt_u32 s73, 61
	s_cbranch_scc0 .LBB0_907
	s_mov_b32 s100, 1
	s_and_b64 vcc, exec, s[8:9]
	s_cbranch_vccz .LBB0_910
	s_barrier

.LBB0_1030:
	v_mov_b32_e32 v133, v161
	v_lshl_add_u64 v[6:7], s[34:35], 0, v[132:133]
	v_mov_b32_e32 v129, v161
	v_readlane_b32 s30, v253, 51
	v_lshl_add_u64 v[8:9], s[34:35], 0, v[128:129]
	v_mov_b32_e32 v135, v161
	v_readlane_b32 s31, v253, 52
	s_add_i32 m0, s47, 0x18000
	v_lshl_add_u64 v[6:7], v[6:7], 0, s[54:55]
	v_lshl_add_u64 v[10:11], s[30:31], 0, v[134:135]
	v_mov_b32_e32 v131, v161
	s_and_b32 s10, s8, 3
	s_lshl_b32 s11, s7, 6
	s_mov_b32 s100, 0
	s_waitcnt vmcnt(2)
	s_barrier
	global_load_lds_dwordx4 v[6:7], off
	v_lshl_add_u64 v[6:7], v[8:9], 0, s[54:55]
	s_add_i32 m0, s47, 0x1a000
	s_add_i32 s59, s47, 0x8000
	s_add_i32 s70, s47, 0xa000
	v_lshl_add_u64 v[12:13], s[30:31], 0, v[130:131]
	global_load_lds_dwordx4 v[6:7], off
	v_lshl_add_u64 v[6:7], v[10:11], 0, s[54:55]
	s_mov_b32 m0, s59
	s_add_u32 s8, s34, 0x20080
	global_load_lds_dwordx4 v[6:7], off
	v_lshl_add_u64 v[6:7], v[12:13], 0, s[54:55]
	s_mov_b32 m0, s70
	s_addc_u32 s9, s35, 0
	global_load_lds_dwordx4 v[6:7], off
	s_add_i32 m0, s47, 0x1c000
	v_lshl_add_u64 v[6:7], s[8:9], 0, v[132:133]
	global_load_lds_dwordx4 v[6:7], off
	v_lshl_add_u64 v[6:7], s[8:9], 0, v[128:129]
	s_add_i32 m0, s47, 0x1e000
	s_cmpk_lt_u32 s6, 0x100
	global_load_lds_dwordx4 v[6:7], off
	s_cselect_b64 s[8:9], -1, 0
	s_lshl_b32 s6, s7, 13
	v_and_b32_e32 v5, 7, v0
	v_bfe_u32 v16, v0, 1, 3
	s_lshl_b32 s7, s10, 11
	s_add_i32 s6, s6, 0
	v_and_b32_e32 v14, 15, v0
	v_bitop3_b32 v16, v3, v16, 3 bitop3:0x6c
	s_add_i32 s6, s6, s7
	v_bfe_u32 v6, v0, 3, 3
	v_bitop3_b32 v3, v3, v5, 3 bitop3:0x6c
	v_or_b32_e32 v15, s11, v14
	v_lshlrev_b32_e32 v16, 4, v16
	v_lshlrev_b32_e32 v18, 7, v14
	s_add_i32 s6, s6, 0x20000
	v_cmp_gt_u32_e32 vcc, 8, v14
	v_lshlrev_b32_e32 v8, 7, v6
	v_lshlrev_b32_e32 v3, 4, v3
	v_and_b32_e32 v0, 4, v0
	v_lshlrev_b32_e32 v15, 7, v15
	s_waitcnt vmcnt(6)
	v_add3_u32 v143, s6, v18, v16
	v_cndmask_b32_e64 v7, v224, 64, vcc
	v_add3_u32 v144, s6, v8, v3
	v_cmp_eq_u32_e32 vcc, 0, v0
	s_lshl_b32 s6, s10, 6
	v_or_b32_e32 v17, v15, v16
	v_lshl_or_b32 v19, s10, 12, v18
	v_cndmask_b32_e64 v3, v224, 64, vcc
	v_lshlrev_b32_e32 v0, 3, v5
	v_bitop3_b32 v5, v15, 64, v16 bitop3:0x36
	s_lshl_b32 s80, s6, 1
	v_readlane_b32 s6, v253, 49
	v_or_b32_e32 v142, v19, v16
	s_mov_b32 s71, 0
	v_or_b32_e32 v145, s11, v6
	v_bitop3_b32 v146, v19, 64, v16 bitop3:0x36
	v_add_u32_e32 v136, v4, v1
	v_mov_b32_e32 v137, v161
	v_add_u32_e32 v138, v2, v1
	v_mov_b32_e32 v139, v161
	v_add_u32_e32 v147, 0, v17
	v_add_u32_e32 v148, 0, v5
	v_lshlrev_b32_e32 v160, 1, v0
	v_add_u32_e32 v149, v143, v7
	v_add_u32_e32 v150, v144, v3
	v_readlane_b32 s72, v253, 46
	s_mov_b32 s73, s6
	s_barrier
	v_readlane_b32 s7, v253, 50
	s_branch .LBB0_1033

.LBB0_1040:
	s_add_u32 s34, s30, 0xfff80080
	s_addc_u32 s35, s31, -1
	s_add_i32 s65, 0, 0x10000
	s_cmp_eq_u32 s89, 28
	v_add_u32_e32 v140, s65, v142
	s_cselect_b32 s37, s17, s35
	s_cselect_b32 s36, s76, s34
	v_add_u32_e32 v141, s65, v146
	ds_read_b128 v[152:155], v140
	ds_read_b128 v[156:159], v141
	v_add_u32_e32 v140, s1, v142
	s_cselect_b32 s35, s11, s88
	s_cselect_b32 s34, s77, s84
	s_add_i32 s94, 0, 0x14000
	v_add_u32_e32 v141, s1, v146
	ds_read_b128 v[166:169], v140
	ds_read_b128 v[170:173], v141
	v_add_u32_e32 v140, s94, v142
	v_add_u32_e32 v141, s94, v146
	ds_read_b128 v[174:177], v140
	ds_read_b128 v[178:181], v141
	v_add_u32_e32 v140, s86, v142
	v_add_u32_e32 v141, s86, v146
	ds_read_b128 v[182:185], v140
	ds_read_b128 v[186:189], v141
	v_lshl_add_u64 v[140:141], s[30:31], 0, v[136:137]
	s_add_i32 m0, s47, 0xc000
	ds_read_b128 v[190:193], v147
	ds_read_b128 v[194:197], v147 offset:2048
	ds_read_b128 v[198:201], v148
	ds_read_b128 v[202:205], v148 offset:2048
	ds_read_b128 v[206:209], v147 offset:4096
	ds_read_b128 v[210:213], v147 offset:6144
	ds_read_b128 v[214:217], v148 offset:4096
	ds_read_b128 v[226:229], v148 offset:6144
	global_load_lds_dwordx4 v[140:141], off
	v_lshl_add_u64 v[140:141], s[30:31], 0, v[138:139]
	s_add_i32 m0, s47, 0xe000
	s_nop 0
	global_load_lds_dwordx4 v[140:141], off
	s_waitcnt vmcnt(24)
	s_cmp_lg_u32 s100, 0
	s_cbranch_scc1 .Lgrx_13
	s_waitcnt vmcnt(8)
.Lgrx_13:
	s_waitcnt lgkmcnt(0)
	s_barrier
	s_setprio 1
	s_waitcnt lgkmcnt(0)
	v_mfma_f32_16x16x32_bf16 v[124:127], v[152:155], v[190:193], v[124:127]
	v_mfma_f32_16x16x32_bf16 v[120:123], v[166:169], v[190:193], v[120:123]
	v_mfma_f32_16x16x32_bf16 v[112:115], v[152:155], v[194:197], v[112:115]
	v_mfma_f32_16x16x32_bf16 v[104:107], v[166:169], v[194:197], v[104:107]
	v_mfma_f32_16x16x32_bf16 v[92:95], v[152:155], v[206:209], v[92:95]
	v_mfma_f32_16x16x32_bf16 v[88:91], v[166:169], v[206:209], v[88:91]
	v_mfma_f32_16x16x32_bf16 v[76:79], v[152:155], v[210:213], v[76:79]
	v_mfma_f32_16x16x32_bf16 v[72:75], v[166:169], v[210:213], v[72:75]
	v_mfma_f32_16x16x32_bf16 v[124:127], v[156:159], v[198:201], v[124:127]
	v_mfma_f32_16x16x32_bf16 v[120:123], v[170:173], v[198:201], v[120:123]
	v_mfma_f32_16x16x32_bf16 v[112:115], v[156:159], v[202:205], v[112:115]
	v_mfma_f32_16x16x32_bf16 v[104:107], v[170:173], v[202:205], v[104:107]
	v_mfma_f32_16x16x32_bf16 v[92:95], v[156:159], v[214:217], v[92:95]
	v_mfma_f32_16x16x32_bf16 v[88:91], v[170:173], v[214:217], v[88:91]
	v_mfma_f32_16x16x32_bf16 v[76:79], v[156:159], v[226:229], v[76:79]
	v_mfma_f32_16x16x32_bf16 v[72:75], v[170:173], v[226:229], v[72:75]
	s_setprio 0
	s_setprio 1
	v_mfma_f32_16x16x32_bf16 v[116:119], v[174:177], v[190:193], v[116:119]
	v_mfma_f32_16x16x32_bf16 v[108:111], v[182:185], v[190:193], v[108:111]
	v_mfma_f32_16x16x32_bf16 v[100:103], v[174:177], v[194:197], v[100:103]
	v_mfma_f32_16x16x32_bf16 v[96:99], v[182:185], v[194:197], v[96:99]
	v_mfma_f32_16x16x32_bf16 v[84:87], v[174:177], v[206:209], v[84:87]
	v_mfma_f32_16x16x32_bf16 v[80:83], v[182:185], v[206:209], v[80:83]
	v_mfma_f32_16x16x32_bf16 v[68:71], v[174:177], v[210:213], v[68:71]
	v_mfma_f32_16x16x32_bf16 v[64:67], v[182:185], v[210:213], v[64:67]
	v_mfma_f32_16x16x32_bf16 v[116:119], v[178:181], v[198:201], v[116:119]
	v_mfma_f32_16x16x32_bf16 v[108:111], v[186:189], v[198:201], v[108:111]
	v_mfma_f32_16x16x32_bf16 v[100:103], v[178:181], v[202:205], v[100:103]
	v_mfma_f32_16x16x32_bf16 v[96:99], v[186:189], v[202:205], v[96:99]
	v_mfma_f32_16x16x32_bf16 v[84:87], v[178:181], v[214:217], v[84:87]
	v_mfma_f32_16x16x32_bf16 v[80:83], v[186:189], v[214:217], v[80:83]
	v_mfma_f32_16x16x32_bf16 v[68:71], v[178:181], v[226:229], v[68:71]
	v_mfma_f32_16x16x32_bf16 v[64:67], v[186:189], v[226:229], v[64:67]
	s_setprio 0
	s_barrier
	s_add_i32 s65, s65, s46
	v_lshl_add_u64 v[140:141], s[34:35], 0, v[132:133]
	s_mov_b32 m0, s65
	ds_read_b128 v[190:193], v147 offset:16384
	ds_read_b128 v[194:197], v147 offset:18432
	ds_read_b128 v[198:201], v148 offset:16384
	ds_read_b128 v[202:205], v148 offset:18432
	ds_read_b128 v[206:209], v147 offset:20480
	ds_read_b128 v[210:213], v147 offset:22528
	ds_read_b128 v[214:217], v148 offset:20480
	ds_read_b128 v[226:229], v148 offset:22528
	global_load_lds_dwordx4 v[140:141], off
	s_add_i32 m0, s65, 0x2000
	s_add_u32 s90, s34, 0x20000
	v_lshl_add_u64 v[162:163], s[34:35], 0, v[128:129]
	s_addc_u32 s91, s35, 0
	s_add_i32 s65, s94, s46
	global_load_lds_dwordx4 v[162:163], off
	v_lshl_add_u64 v[218:219], s[90:91], 0, v[132:133]
	s_mov_b32 m0, s65
	v_lshl_add_u64 v[230:231], s[36:37], 0, v[130:131]
	global_load_lds_dwordx4 v[218:219], off
	v_lshl_add_u64 v[218:219], s[90:91], 0, v[128:129]
	s_add_i32 m0, s65, 0x2000
	s_nop 0
	global_load_lds_dwordx4 v[218:219], off
	v_lshl_add_u64 v[218:219], s[36:37], 0, v[134:135]
	s_mov_b32 m0, s47
	s_nop 0
	global_load_lds_dwordx4 v[218:219], off
	s_mov_b32 m0, s56
	s_nop 0
	global_load_lds_dwordx4 v[230:231], off
	s_waitcnt vmcnt(24)
	s_cmp_lg_u32 s100, 0
	s_cbranch_scc1 .Lgrx_14
	s_waitcnt vmcnt(8)
.Lgrx_14:
	s_mov_b32 s100, 0
	s_waitcnt lgkmcnt(0)
	s_barrier
	s_setprio 1
	s_waitcnt lgkmcnt(0)
	v_mfma_f32_16x16x32_bf16 v[60:63], v[152:155], v[190:193], v[60:63]
	v_mfma_f32_16x16x32_bf16 v[56:59], v[166:169], v[190:193], v[56:59]
	v_mfma_f32_16x16x32_bf16 v[44:47], v[152:155], v[194:197], v[44:47]
	v_mfma_f32_16x16x32_bf16 v[40:43], v[166:169], v[194:197], v[40:43]
	v_mfma_f32_16x16x32_bf16 v[28:31], v[152:155], v[206:209], v[28:31]
	v_mfma_f32_16x16x32_bf16 v[24:27], v[166:169], v[206:209], v[24:27]
	v_mfma_f32_16x16x32_bf16 v[12:15], v[152:155], v[210:213], v[12:15]
	v_mfma_f32_16x16x32_bf16 v[8:11], v[166:169], v[210:213], v[8:11]
	v_mfma_f32_16x16x32_bf16 v[60:63], v[156:159], v[198:201], v[60:63]
	v_mfma_f32_16x16x32_bf16 v[56:59], v[170:173], v[198:201], v[56:59]
	v_mfma_f32_16x16x32_bf16 v[44:47], v[156:159], v[202:205], v[44:47]
	v_mfma_f32_16x16x32_bf16 v[40:43], v[170:173], v[202:205], v[40:43]
	v_mfma_f32_16x16x32_bf16 v[28:31], v[156:159], v[214:217], v[28:31]
	v_mfma_f32_16x16x32_bf16 v[24:27], v[170:173], v[214:217], v[24:27]
	v_mfma_f32_16x16x32_bf16 v[12:15], v[156:159], v[226:229], v[12:15]
	v_mfma_f32_16x16x32_bf16 v[8:11], v[170:173], v[226:229], v[8:11]
	s_setprio 0
	s_setprio 1
	v_mfma_f32_16x16x32_bf16 v[52:55], v[174:177], v[190:193], v[52:55]
	v_mfma_f32_16x16x32_bf16 v[48:51], v[182:185], v[190:193], v[48:51]
	v_mfma_f32_16x16x32_bf16 v[36:39], v[174:177], v[194:197], v[36:39]
	v_mfma_f32_16x16x32_bf16 v[32:35], v[182:185], v[194:197], v[32:35]
	v_mfma_f32_16x16x32_bf16 v[20:23], v[174:177], v[206:209], v[20:23]
	v_mfma_f32_16x16x32_bf16 v[16:19], v[182:185], v[206:209], v[16:19]
	v_mfma_f32_16x16x32_bf16 v[4:7], v[174:177], v[210:213], v[4:7]
	v_mfma_f32_16x16x32_bf16 v[0:3], v[182:185], v[210:213], v[0:3]
	v_mfma_f32_16x16x32_bf16 v[52:55], v[178:181], v[198:201], v[52:55]
	v_mfma_f32_16x16x32_bf16 v[48:51], v[186:189], v[198:201], v[48:51]
	v_mfma_f32_16x16x32_bf16 v[36:39], v[178:181], v[202:205], v[36:39]
	v_mfma_f32_16x16x32_bf16 v[32:35], v[186:189], v[202:205], v[32:35]
	v_mfma_f32_16x16x32_bf16 v[20:23], v[178:181], v[214:217], v[20:23]
	v_mfma_f32_16x16x32_bf16 v[16:19], v[186:189], v[214:217], v[16:19]
	v_mfma_f32_16x16x32_bf16 v[4:7], v[178:181], v[226:229], v[4:7]
	v_mfma_f32_16x16x32_bf16 v[0:3], v[186:189], v[226:229], v[0:3]
	s_setprio 0
	s_barrier
	s_add_i32 s65, 0, 0x18000
	v_add_u32_e32 v151, s65, v142
	v_add_u32_e32 v156, s65, v146
	ds_read_b128 v[152:155], v151
	ds_read_b128 v[156:159], v156
	v_add_u32_e32 v151, s87, v142
	v_add_u32_e32 v170, s87, v146
	s_add_i32 s90, 0, 0x1c000
	ds_read_b128 v[166:169], v151
	ds_read_b128 v[170:173], v170
	v_add_u32_e32 v151, s90, v142
	v_add_u32_e32 v178, s90, v146
	ds_read_b128 v[174:177], v151
	ds_read_b128 v[178:181], v178
	v_add_u32_e32 v151, s2, v142
	v_add_u32_e32 v186, s2, v146
	ds_read_b128 v[182:185], v151
	ds_read_b128 v[186:189], v186
	s_add_u32 s36, s36, 0x80000
	s_addc_u32 s37, s37, 0
	s_mov_b32 m0, s57
	v_lshl_add_u64 v[232:233], s[36:37], 0, v[134:135]
	ds_read_b128 v[190:193], v147 offset:32768
	ds_read_b128 v[194:197], v147 offset:34816
	ds_read_b128 v[198:201], v148 offset:32768
	ds_read_b128 v[202:205], v148 offset:34816
	ds_read_b128 v[206:209], v147 offset:36864
	ds_read_b128 v[210:213], v147 offset:38912
	ds_read_b128 v[214:217], v148 offset:36864
	ds_read_b128 v[226:229], v148 offset:38912
	global_load_lds_dwordx4 v[232:233], off
	v_lshl_add_u64 v[232:233], s[36:37], 0, v[130:131]
	s_mov_b32 m0, s58
	s_nop 0
	global_load_lds_dwordx4 v[232:233], off
	s_waitcnt vmcnt(8)
	s_waitcnt lgkmcnt(0)
	s_barrier
	s_setprio 1
	s_waitcnt lgkmcnt(0)
	v_mfma_f32_16x16x32_bf16 v[124:127], v[152:155], v[190:193], v[124:127]
	v_mfma_f32_16x16x32_bf16 v[120:123], v[166:169], v[190:193], v[120:123]
	v_mfma_f32_16x16x32_bf16 v[112:115], v[152:155], v[194:197], v[112:115]
	v_mfma_f32_16x16x32_bf16 v[104:107], v[166:169], v[194:197], v[104:107]
	v_mfma_f32_16x16x32_bf16 v[92:95], v[152:155], v[206:209], v[92:95]
	v_mfma_f32_16x16x32_bf16 v[88:91], v[166:169], v[206:209], v[88:91]
	v_mfma_f32_16x16x32_bf16 v[76:79], v[152:155], v[210:213], v[76:79]
	v_mfma_f32_16x16x32_bf16 v[72:75], v[166:169], v[210:213], v[72:75]
	v_mfma_f32_16x16x32_bf16 v[124:127], v[156:159], v[198:201], v[124:127]
	v_mfma_f32_16x16x32_bf16 v[120:123], v[170:173], v[198:201], v[120:123]
	v_mfma_f32_16x16x32_bf16 v[112:115], v[156:159], v[202:205], v[112:115]
	v_mfma_f32_16x16x32_bf16 v[104:107], v[170:173], v[202:205], v[104:107]
	v_mfma_f32_16x16x32_bf16 v[92:95], v[156:159], v[214:217], v[92:95]
	v_mfma_f32_16x16x32_bf16 v[88:91], v[170:173], v[214:217], v[88:91]
	v_mfma_f32_16x16x32_bf16 v[76:79], v[156:159], v[226:229], v[76:79]
	v_mfma_f32_16x16x32_bf16 v[72:75], v[170:173], v[226:229], v[72:75]
	s_setprio 0
	s_setprio 1
	v_mfma_f32_16x16x32_bf16 v[116:119], v[174:177], v[190:193], v[116:119]
	v_mfma_f32_16x16x32_bf16 v[108:111], v[182:185], v[190:193], v[108:111]
	v_mfma_f32_16x16x32_bf16 v[100:103], v[174:177], v[194:197], v[100:103]
	v_mfma_f32_16x16x32_bf16 v[96:99], v[182:185], v[194:197], v[96:99]
	v_mfma_f32_16x16x32_bf16 v[84:87], v[174:177], v[206:209], v[84:87]
	v_mfma_f32_16x16x32_bf16 v[80:83], v[182:185], v[206:209], v[80:83]
	v_mfma_f32_16x16x32_bf16 v[68:71], v[174:177], v[210:213], v[68:71]
	v_mfma_f32_16x16x32_bf16 v[64:67], v[182:185], v[210:213], v[64:67]
	v_mfma_f32_16x16x32_bf16 v[116:119], v[178:181], v[198:201], v[116:119]
	v_mfma_f32_16x16x32_bf16 v[108:111], v[186:189], v[198:201], v[108:111]
	v_mfma_f32_16x16x32_bf16 v[100:103], v[178:181], v[202:205], v[100:103]
	v_mfma_f32_16x16x32_bf16 v[96:99], v[186:189], v[202:205], v[96:99]
	v_mfma_f32_16x16x32_bf16 v[84:87], v[178:181], v[214:217], v[84:87]
	v_mfma_f32_16x16x32_bf16 v[80:83], v[186:189], v[214:217], v[80:83]
	v_mfma_f32_16x16x32_bf16 v[68:71], v[178:181], v[226:229], v[68:71]
	v_mfma_f32_16x16x32_bf16 v[64:67], v[186:189], v[226:229], v[64:67]
	s_setprio 0
	s_barrier
	s_add_i32 s36, s65, s46
	v_lshl_add_u64 v[140:141], v[140:141], 0, s[54:55]
	s_mov_b32 m0, s36
	ds_read_b128 v[190:193], v147 offset:49152
	ds_read_b128 v[194:197], v147 offset:51200
	ds_read_b128 v[198:201], v148 offset:49152
	ds_read_b128 v[202:205], v148 offset:51200
	ds_read_b128 v[206:209], v147 offset:53248
	ds_read_b128 v[210:213], v147 offset:55296
	ds_read_b128 v[214:217], v148 offset:53248
	ds_read_b128 v[226:229], v148 offset:55296
	global_load_lds_dwordx4 v[140:141], off
	s_add_i32 m0, s36, 0x2000
	s_add_u32 s34, s34, 0x20080
	v_lshl_add_u64 v[140:141], v[162:163], 0, s[54:55]
	s_addc_u32 s35, s35, 0
	s_add_i32 s36, s90, s46
	global_load_lds_dwordx4 v[140:141], off
	v_lshl_add_u64 v[140:141], s[34:35], 0, v[132:133]
	s_mov_b32 m0, s36
	s_nop 0
	global_load_lds_dwordx4 v[140:141], off
	v_lshl_add_u64 v[140:141], s[34:35], 0, v[128:129]
	s_add_i32 m0, s36, 0x2000
	s_nop 0
	global_load_lds_dwordx4 v[140:141], off
	v_lshl_add_u64 v[140:141], v[218:219], 0, s[54:55]
	s_mov_b32 m0, s59
	s_nop 0
	global_load_lds_dwordx4 v[140:141], off
	v_lshl_add_u64 v[140:141], v[230:231], 0, s[54:55]
	s_mov_b32 m0, s70
	s_nop 0
	global_load_lds_dwordx4 v[140:141], off
	s_waitcnt vmcnt(8)
	s_waitcnt lgkmcnt(0)
	s_barrier
	s_setprio 1
	s_waitcnt lgkmcnt(0)
	v_mfma_f32_16x16x32_bf16 v[60:63], v[152:155], v[190:193], v[60:63]
	v_mfma_f32_16x16x32_bf16 v[56:59], v[166:169], v[190:193], v[56:59]
	v_mfma_f32_16x16x32_bf16 v[44:47], v[152:155], v[194:197], v[44:47]
	v_mfma_f32_16x16x32_bf16 v[40:43], v[166:169], v[194:197], v[40:43]
	v_mfma_f32_16x16x32_bf16 v[28:31], v[152:155], v[206:209], v[28:31]
	v_mfma_f32_16x16x32_bf16 v[24:27], v[166:169], v[206:209], v[24:27]
	v_mfma_f32_16x16x32_bf16 v[12:15], v[152:155], v[210:213], v[12:15]
	v_mfma_f32_16x16x32_bf16 v[8:11], v[166:169], v[210:213], v[8:11]
	v_mfma_f32_16x16x32_bf16 v[60:63], v[156:159], v[198:201], v[60:63]
	v_mfma_f32_16x16x32_bf16 v[56:59], v[170:173], v[198:201], v[56:59]
	v_mfma_f32_16x16x32_bf16 v[44:47], v[156:159], v[202:205], v[44:47]
	v_mfma_f32_16x16x32_bf16 v[40:43], v[170:173], v[202:205], v[40:43]
	v_mfma_f32_16x16x32_bf16 v[28:31], v[156:159], v[214:217], v[28:31]
	v_mfma_f32_16x16x32_bf16 v[24:27], v[170:173], v[214:217], v[24:27]
	v_mfma_f32_16x16x32_bf16 v[12:15], v[156:159], v[226:229], v[12:15]
	v_mfma_f32_16x16x32_bf16 v[8:11], v[170:173], v[226:229], v[8:11]
	s_setprio 0
	s_setprio 1
	v_mfma_f32_16x16x32_bf16 v[52:55], v[174:177], v[190:193], v[52:55]
	v_mfma_f32_16x16x32_bf16 v[48:51], v[182:185], v[190:193], v[48:51]
	v_mfma_f32_16x16x32_bf16 v[36:39], v[174:177], v[194:197], v[36:39]
	v_mfma_f32_16x16x32_bf16 v[32:35], v[182:185], v[194:197], v[32:35]
	v_mfma_f32_16x16x32_bf16 v[20:23], v[174:177], v[206:209], v[20:23]
	v_mfma_f32_16x16x32_bf16 v[16:19], v[182:185], v[206:209], v[16:19]
	v_mfma_f32_16x16x32_bf16 v[4:7], v[174:177], v[210:213], v[4:7]
	v_mfma_f32_16x16x32_bf16 v[0:3], v[182:185], v[210:213], v[0:3]
	v_mfma_f32_16x16x32_bf16 v[52:55], v[178:181], v[198:201], v[52:55]
	v_mfma_f32_16x16x32_bf16 v[48:51], v[186:189], v[198:201], v[48:51]
	v_mfma_f32_16x16x32_bf16 v[36:39], v[178:181], v[202:205], v[36:39]
	v_mfma_f32_16x16x32_bf16 v[32:35], v[186:189], v[202:205], v[32:35]
	v_mfma_f32_16x16x32_bf16 v[20:23], v[178:181], v[214:217], v[20:23]
	v_mfma_f32_16x16x32_bf16 v[16:19], v[186:189], v[214:217], v[16:19]
	v_mfma_f32_16x16x32_bf16 v[4:7], v[178:181], v[226:229], v[4:7]
	v_mfma_f32_16x16x32_bf16 v[0:3], v[186:189], v[226:229], v[0:3]
	s_setprio 0
	s_barrier
	s_add_i32 s89, s89, 2
	s_add_u32 s30, s30, 0x100
	s_addc_u32 s31, s31, 0
	s_add_u32 s84, s84, 0x100
	s_addc_u32 s88, s88, 0
	s_cmp_gt_u32 s89, 29
	s_cbranch_scc0 .LBB0_1040
	s_mov_b32 s100, 1
	s_and_b64 vcc, exec, s[8:9]
	s_cbranch_vccz .LBB0_1043
	s_barrier

.LBB0_1085:
	v_mov_b32_e32 v133, v161
	v_lshl_add_u64 v[6:7], s[34:35], 0, v[132:133]
	v_mov_b32_e32 v129, v161
	v_readlane_b32 s30, v254, 33
	v_lshl_add_u64 v[8:9], s[34:35], 0, v[128:129]
	v_mov_b32_e32 v135, v161
	v_readlane_b32 s31, v254, 34
	s_add_i32 m0, s47, 0x18000
	v_lshl_add_u64 v[6:7], v[6:7], 0, s[54:55]
	v_lshl_add_u64 v[10:11], s[30:31], 0, v[134:135]
	v_mov_b32_e32 v131, v161
	s_and_b32 s10, s8, 3
	s_lshl_b32 s11, s7, 6
	s_mov_b32 s100, 0
	s_waitcnt vmcnt(2)
	s_barrier
	global_load_lds_dwordx4 v[6:7], off
	v_lshl_add_u64 v[6:7], v[8:9], 0, s[54:55]
	s_add_i32 m0, s47, 0x1a000
	s_add_i32 s59, s47, 0x8000
	s_add_i32 s69, s47, 0xa000
	v_lshl_add_u64 v[12:13], s[30:31], 0, v[130:131]
	global_load_lds_dwordx4 v[6:7], off
	v_lshl_add_u64 v[6:7], v[10:11], 0, s[54:55]
	s_mov_b32 m0, s59
	s_add_u32 s8, s34, 0x80080
	global_load_lds_dwordx4 v[6:7], off
	v_lshl_add_u64 v[6:7], v[12:13], 0, s[54:55]
	s_mov_b32 m0, s69
	s_addc_u32 s9, s35, 0
	global_load_lds_dwordx4 v[6:7], off
	s_add_i32 m0, s47, 0x1c000
	v_lshl_add_u64 v[6:7], s[8:9], 0, v[132:133]
	global_load_lds_dwordx4 v[6:7], off
	v_lshl_add_u64 v[6:7], s[8:9], 0, v[128:129]
	s_add_i32 m0, s47, 0x1e000
	s_cmpk_lt_u32 s6, 0x100
	global_load_lds_dwordx4 v[6:7], off
	s_cselect_b64 s[8:9], -1, 0
	s_lshl_b32 s6, s7, 13
	v_and_b32_e32 v5, 7, v0
	v_bfe_u32 v16, v0, 1, 3
	s_lshl_b32 s7, s10, 11
	s_add_i32 s6, s6, 0
	v_and_b32_e32 v14, 15, v0
	v_bitop3_b32 v16, v3, v16, 3 bitop3:0x6c
	s_add_i32 s6, s6, s7
	v_bfe_u32 v6, v0, 3, 3
	v_bitop3_b32 v3, v3, v5, 3 bitop3:0x6c
	v_or_b32_e32 v15, s11, v14
	v_lshlrev_b32_e32 v16, 4, v16
	v_lshlrev_b32_e32 v18, 7, v14
	s_add_i32 s6, s6, 0x20000
	v_cmp_gt_u32_e32 vcc, 8, v14
	v_lshlrev_b32_e32 v8, 7, v6
	v_lshlrev_b32_e32 v3, 4, v3
	v_and_b32_e32 v0, 4, v0
	v_lshlrev_b32_e32 v15, 7, v15
	s_waitcnt vmcnt(6)
	v_add3_u32 v141, s6, v18, v16
	v_cndmask_b32_e64 v7, v224, 64, vcc
	v_add3_u32 v142, s6, v8, v3
	v_cmp_eq_u32_e32 vcc, 0, v0
	s_lshl_b32 s6, s10, 6
	v_or_b32_e32 v17, v15, v16
	v_lshl_or_b32 v19, s10, 12, v18
	v_cndmask_b32_e64 v3, v224, 64, vcc
	v_lshlrev_b32_e32 v0, 3, v5
	v_bitop3_b32 v5, v15, 64, v16 bitop3:0x36
	s_lshl_b32 s80, s6, 1
	v_readlane_b32 s6, v254, 31
	v_or_b32_e32 v140, v19, v16
	s_mov_b32 s70, 0
	v_or_b32_e32 v143, s11, v6
	v_bitop3_b32 v144, v19, 64, v16 bitop3:0x36
	v_add_u32_e32 v136, v4, v1
	v_mov_b32_e32 v137, v161
	v_add_u32_e32 v138, v2, v1
	v_mov_b32_e32 v139, v161
	v_add_u32_e32 v145, 0, v17
	v_add_u32_e32 v146, 0, v5
	v_lshlrev_b32_e32 v160, 1, v0
	v_add_u32_e32 v147, v141, v7
	v_add_u32_e32 v148, v142, v3
	v_readlane_b32 s71, v254, 48
	s_mov_b32 s72, s6
	s_barrier
	v_readlane_b32 s7, v254, 32
	s_branch .LBB0_1088

.LBB0_1091:
	s_add_u32 s34, s30, 0xffe00080
	s_addc_u32 s35, s31, -1
	s_add_i32 s65, 0, 0x10000
	s_cmpk_eq_i32 s88, 0x7c
	v_add_u32_e32 v149, s65, v140
	v_add_u32_e32 v154, s65, v144
	s_cselect_b32 s37, s17, s35
	s_cselect_b32 s36, s73, s34
	ds_read_b128 v[150:153], v149
	ds_read_b128 v[154:157], v154
	v_add_u32_e32 v149, s1, v140
	s_cselect_b32 s35, s11, s84
	s_cselect_b32 s34, s76, s77
	s_add_i32 s89, 0, 0x14000
	v_add_u32_e32 v158, s1, v144
	ds_read_b128 v[166:169], v149
	ds_read_b128 v[170:173], v158
	v_add_u32_e32 v149, s89, v140
	v_add_u32_e32 v158, s89, v144
	ds_read_b128 v[174:177], v149
	ds_read_b128 v[178:181], v158
	v_add_u32_e32 v149, s86, v140
	v_add_u32_e32 v158, s86, v144
	ds_read_b128 v[182:185], v149
	ds_read_b128 v[186:189], v158
	v_lshl_add_u64 v[158:159], s[30:31], 0, v[136:137]
	s_add_i32 m0, s47, 0xc000
	ds_read_b128 v[190:193], v145
	ds_read_b128 v[194:197], v145 offset:2048
	ds_read_b128 v[198:201], v146
	ds_read_b128 v[202:205], v146 offset:2048
	ds_read_b128 v[206:209], v145 offset:4096
	ds_read_b128 v[210:213], v145 offset:6144
	ds_read_b128 v[214:217], v146 offset:4096
	ds_read_b128 v[226:229], v146 offset:6144
	global_load_lds_dwordx4 v[158:159], off
	v_lshl_add_u64 v[158:159], s[30:31], 0, v[138:139]
	s_add_i32 m0, s47, 0xe000
	s_nop 0
	global_load_lds_dwordx4 v[158:159], off
	s_waitcnt vmcnt(24)
	s_cmp_lg_u32 s100, 0
	s_cbranch_scc1 .Lgrx_15
	s_waitcnt vmcnt(8)
.Lgrx_15:
	s_waitcnt lgkmcnt(0)
	s_barrier
	s_setprio 1
	s_waitcnt lgkmcnt(0)
	v_mfma_f32_16x16x32_bf16 v[124:127], v[150:153], v[190:193], v[124:127]
	v_mfma_f32_16x16x32_bf16 v[120:123], v[166:169], v[190:193], v[120:123]
	v_mfma_f32_16x16x32_bf16 v[116:119], v[150:153], v[194:197], v[116:119]
	v_mfma_f32_16x16x32_bf16 v[112:115], v[166:169], v[194:197], v[112:115]
	v_mfma_f32_16x16x32_bf16 v[100:103], v[150:153], v[206:209], v[100:103]
	v_mfma_f32_16x16x32_bf16 v[96:99], v[166:169], v[206:209], v[96:99]
	v_mfma_f32_16x16x32_bf16 v[84:87], v[150:153], v[210:213], v[84:87]
	v_mfma_f32_16x16x32_bf16 v[76:79], v[166:169], v[210:213], v[76:79]
	v_mfma_f32_16x16x32_bf16 v[124:127], v[154:157], v[198:201], v[124:127]
	v_mfma_f32_16x16x32_bf16 v[120:123], v[170:173], v[198:201], v[120:123]
	v_mfma_f32_16x16x32_bf16 v[116:119], v[154:157], v[202:205], v[116:119]
	v_mfma_f32_16x16x32_bf16 v[112:115], v[170:173], v[202:205], v[112:115]
	v_mfma_f32_16x16x32_bf16 v[100:103], v[154:157], v[214:217], v[100:103]
	v_mfma_f32_16x16x32_bf16 v[96:99], v[170:173], v[214:217], v[96:99]
	v_mfma_f32_16x16x32_bf16 v[84:87], v[154:157], v[226:229], v[84:87]
	v_mfma_f32_16x16x32_bf16 v[76:79], v[170:173], v[226:229], v[76:79]
	s_setprio 0
	s_setprio 1
	v_mfma_f32_16x16x32_bf16 v[108:111], v[174:177], v[190:193], v[108:111]
	v_mfma_f32_16x16x32_bf16 v[104:107], v[182:185], v[190:193], v[104:107]
	v_mfma_f32_16x16x32_bf16 v[92:95], v[174:177], v[194:197], v[92:95]
	v_mfma_f32_16x16x32_bf16 v[88:91], v[182:185], v[194:197], v[88:91]
	v_mfma_f32_16x16x32_bf16 v[80:83], v[174:177], v[206:209], v[80:83]
	v_mfma_f32_16x16x32_bf16 v[72:75], v[182:185], v[206:209], v[72:75]
	v_mfma_f32_16x16x32_bf16 v[68:71], v[174:177], v[210:213], v[68:71]
	v_mfma_f32_16x16x32_bf16 v[64:67], v[182:185], v[210:213], v[64:67]
	v_mfma_f32_16x16x32_bf16 v[108:111], v[178:181], v[198:201], v[108:111]
	v_mfma_f32_16x16x32_bf16 v[104:107], v[186:189], v[198:201], v[104:107]
	v_mfma_f32_16x16x32_bf16 v[92:95], v[178:181], v[202:205], v[92:95]
	v_mfma_f32_16x16x32_bf16 v[88:91], v[186:189], v[202:205], v[88:91]
	v_mfma_f32_16x16x32_bf16 v[80:83], v[178:181], v[214:217], v[80:83]
	v_mfma_f32_16x16x32_bf16 v[72:75], v[186:189], v[214:217], v[72:75]
	v_mfma_f32_16x16x32_bf16 v[68:71], v[178:181], v[226:229], v[68:71]
	v_mfma_f32_16x16x32_bf16 v[64:67], v[186:189], v[226:229], v[64:67]
	s_setprio 0
	s_barrier
	s_add_i32 s65, s65, s46
	v_lshl_add_u64 v[158:159], s[34:35], 0, v[132:133]
	s_mov_b32 m0, s65
	ds_read_b128 v[190:193], v145 offset:16384
	ds_read_b128 v[194:197], v145 offset:18432
	ds_read_b128 v[198:201], v146 offset:16384
	ds_read_b128 v[202:205], v146 offset:18432
	ds_read_b128 v[206:209], v145 offset:20480
	ds_read_b128 v[210:213], v145 offset:22528
	ds_read_b128 v[214:217], v146 offset:20480
	ds_read_b128 v[226:229], v146 offset:22528
	global_load_lds_dwordx4 v[158:159], off
	s_add_i32 m0, s65, 0x2000
	s_add_u32 s90, s34, 0x80000
	v_lshl_add_u64 v[162:163], s[34:35], 0, v[128:129]
	s_addc_u32 s91, s35, 0
	s_add_i32 s65, s89, s46
	global_load_lds_dwordx4 v[162:163], off
	v_lshl_add_u64 v[218:219], s[90:91], 0, v[132:133]
	s_mov_b32 m0, s65
	v_lshl_add_u64 v[230:231], s[36:37], 0, v[130:131]
	global_load_lds_dwordx4 v[218:219], off
	v_lshl_add_u64 v[218:219], s[90:91], 0, v[128:129]
	s_add_i32 m0, s65, 0x2000
	s_nop 0
	global_load_lds_dwordx4 v[218:219], off
	v_lshl_add_u64 v[218:219], s[36:37], 0, v[134:135]
	s_mov_b32 m0, s47
	s_nop 0
	global_load_lds_dwordx4 v[218:219], off
	s_mov_b32 m0, s56
	s_nop 0
	global_load_lds_dwordx4 v[230:231], off
	s_waitcnt vmcnt(24)
	s_cmp_lg_u32 s100, 0
	s_cbranch_scc1 .Lgrx_16
	s_waitcnt vmcnt(8)
.Lgrx_16:
	s_mov_b32 s100, 0
	s_waitcnt lgkmcnt(0)
	s_barrier
	s_setprio 1
	s_waitcnt lgkmcnt(0)
	v_mfma_f32_16x16x32_bf16 v[60:63], v[150:153], v[190:193], v[60:63]
	v_mfma_f32_16x16x32_bf16 v[56:59], v[166:169], v[190:193], v[56:59]
	v_mfma_f32_16x16x32_bf16 v[52:55], v[150:153], v[194:197], v[52:55]
	v_mfma_f32_16x16x32_bf16 v[44:47], v[166:169], v[194:197], v[44:47]
	v_mfma_f32_16x16x32_bf16 v[36:39], v[150:153], v[206:209], v[36:39]
	v_mfma_f32_16x16x32_bf16 v[28:31], v[166:169], v[206:209], v[28:31]
	v_mfma_f32_16x16x32_bf16 v[20:23], v[150:153], v[210:213], v[20:23]
	v_mfma_f32_16x16x32_bf16 v[12:15], v[166:169], v[210:213], v[12:15]
	v_mfma_f32_16x16x32_bf16 v[60:63], v[154:157], v[198:201], v[60:63]
	v_mfma_f32_16x16x32_bf16 v[56:59], v[170:173], v[198:201], v[56:59]
	v_mfma_f32_16x16x32_bf16 v[52:55], v[154:157], v[202:205], v[52:55]
	v_mfma_f32_16x16x32_bf16 v[44:47], v[170:173], v[202:205], v[44:47]
	v_mfma_f32_16x16x32_bf16 v[36:39], v[154:157], v[214:217], v[36:39]
	v_mfma_f32_16x16x32_bf16 v[28:31], v[170:173], v[214:217], v[28:31]
	v_mfma_f32_16x16x32_bf16 v[20:23], v[154:157], v[226:229], v[20:23]
	v_mfma_f32_16x16x32_bf16 v[12:15], v[170:173], v[226:229], v[12:15]
	s_setprio 0
	s_setprio 1
	v_mfma_f32_16x16x32_bf16 v[48:51], v[174:177], v[190:193], v[48:51]
	v_mfma_f32_16x16x32_bf16 v[40:43], v[182:185], v[190:193], v[40:43]
	v_mfma_f32_16x16x32_bf16 v[32:35], v[174:177], v[194:197], v[32:35]
	v_mfma_f32_16x16x32_bf16 v[24:27], v[182:185], v[194:197], v[24:27]
	v_mfma_f32_16x16x32_bf16 v[16:19], v[174:177], v[206:209], v[16:19]
	v_mfma_f32_16x16x32_bf16 v[8:11], v[182:185], v[206:209], v[8:11]
	v_mfma_f32_16x16x32_bf16 v[4:7], v[174:177], v[210:213], v[4:7]
	v_mfma_f32_16x16x32_bf16 v[0:3], v[182:185], v[210:213], v[0:3]
	v_mfma_f32_16x16x32_bf16 v[48:51], v[178:181], v[198:201], v[48:51]
	v_mfma_f32_16x16x32_bf16 v[40:43], v[186:189], v[198:201], v[40:43]
	v_mfma_f32_16x16x32_bf16 v[32:35], v[178:181], v[202:205], v[32:35]
	v_mfma_f32_16x16x32_bf16 v[24:27], v[186:189], v[202:205], v[24:27]
	v_mfma_f32_16x16x32_bf16 v[16:19], v[178:181], v[214:217], v[16:19]
	v_mfma_f32_16x16x32_bf16 v[8:11], v[186:189], v[214:217], v[8:11]
	v_mfma_f32_16x16x32_bf16 v[4:7], v[178:181], v[226:229], v[4:7]
	v_mfma_f32_16x16x32_bf16 v[0:3], v[186:189], v[226:229], v[0:3]
	s_setprio 0
	s_barrier
	s_add_i32 s65, 0, 0x18000
	v_add_u32_e32 v149, s65, v140
	v_add_u32_e32 v154, s65, v144
	ds_read_b128 v[150:153], v149
	ds_read_b128 v[154:157], v154
	v_add_u32_e32 v149, s87, v140
	v_add_u32_e32 v170, s87, v144
	s_add_i32 s89, 0, 0x1c000
	ds_read_b128 v[166:169], v149
	ds_read_b128 v[170:173], v170
	v_add_u32_e32 v149, s89, v140
	v_add_u32_e32 v178, s89, v144
	ds_read_b128 v[174:177], v149
	ds_read_b128 v[178:181], v178
	v_add_u32_e32 v149, s2, v140
	v_add_u32_e32 v186, s2, v144
	ds_read_b128 v[182:185], v149
	ds_read_b128 v[186:189], v186
	s_add_u32 s36, s36, 0x200000
	s_addc_u32 s37, s37, 0
	s_mov_b32 m0, s57
	v_lshl_add_u64 v[232:233], s[36:37], 0, v[134:135]
	ds_read_b128 v[190:193], v145 offset:32768
	ds_read_b128 v[194:197], v145 offset:34816
	ds_read_b128 v[198:201], v146 offset:32768
	ds_read_b128 v[202:205], v146 offset:34816
	ds_read_b128 v[206:209], v145 offset:36864
	ds_read_b128 v[210:213], v145 offset:38912
	ds_read_b128 v[214:217], v146 offset:36864
	ds_read_b128 v[226:229], v146 offset:38912
	global_load_lds_dwordx4 v[232:233], off
	v_lshl_add_u64 v[232:233], s[36:37], 0, v[130:131]
	s_mov_b32 m0, s58
	s_nop 0
	global_load_lds_dwordx4 v[232:233], off
	s_waitcnt vmcnt(8)
	s_waitcnt lgkmcnt(0)
	s_barrier
	s_setprio 1
	s_waitcnt lgkmcnt(0)
	v_mfma_f32_16x16x32_bf16 v[124:127], v[150:153], v[190:193], v[124:127]
	v_mfma_f32_16x16x32_bf16 v[120:123], v[166:169], v[190:193], v[120:123]
	v_mfma_f32_16x16x32_bf16 v[116:119], v[150:153], v[194:197], v[116:119]
	v_mfma_f32_16x16x32_bf16 v[112:115], v[166:169], v[194:197], v[112:115]
	v_mfma_f32_16x16x32_bf16 v[100:103], v[150:153], v[206:209], v[100:103]
	v_mfma_f32_16x16x32_bf16 v[96:99], v[166:169], v[206:209], v[96:99]
	v_mfma_f32_16x16x32_bf16 v[84:87], v[150:153], v[210:213], v[84:87]
	v_mfma_f32_16x16x32_bf16 v[76:79], v[166:169], v[210:213], v[76:79]
	v_mfma_f32_16x16x32_bf16 v[124:127], v[154:157], v[198:201], v[124:127]
	v_mfma_f32_16x16x32_bf16 v[120:123], v[170:173], v[198:201], v[120:123]
	v_mfma_f32_16x16x32_bf16 v[116:119], v[154:157], v[202:205], v[116:119]
	v_mfma_f32_16x16x32_bf16 v[112:115], v[170:173], v[202:205], v[112:115]
	v_mfma_f32_16x16x32_bf16 v[100:103], v[154:157], v[214:217], v[100:103]
	v_mfma_f32_16x16x32_bf16 v[96:99], v[170:173], v[214:217], v[96:99]
	v_mfma_f32_16x16x32_bf16 v[84:87], v[154:157], v[226:229], v[84:87]
	v_mfma_f32_16x16x32_bf16 v[76:79], v[170:173], v[226:229], v[76:79]
	s_setprio 0
	s_setprio 1
	v_mfma_f32_16x16x32_bf16 v[108:111], v[174:177], v[190:193], v[108:111]
	v_mfma_f32_16x16x32_bf16 v[104:107], v[182:185], v[190:193], v[104:107]
	v_mfma_f32_16x16x32_bf16 v[92:95], v[174:177], v[194:197], v[92:95]
	v_mfma_f32_16x16x32_bf16 v[88:91], v[182:185], v[194:197], v[88:91]
	v_mfma_f32_16x16x32_bf16 v[80:83], v[174:177], v[206:209], v[80:83]
	v_mfma_f32_16x16x32_bf16 v[72:75], v[182:185], v[206:209], v[72:75]
	v_mfma_f32_16x16x32_bf16 v[68:71], v[174:177], v[210:213], v[68:71]
	v_mfma_f32_16x16x32_bf16 v[64:67], v[182:185], v[210:213], v[64:67]
	v_mfma_f32_16x16x32_bf16 v[108:111], v[178:181], v[198:201], v[108:111]
	v_mfma_f32_16x16x32_bf16 v[104:107], v[186:189], v[198:201], v[104:107]
	v_mfma_f32_16x16x32_bf16 v[92:95], v[178:181], v[202:205], v[92:95]
	v_mfma_f32_16x16x32_bf16 v[88:91], v[186:189], v[202:205], v[88:91]
	v_mfma_f32_16x16x32_bf16 v[80:83], v[178:181], v[214:217], v[80:83]
	v_mfma_f32_16x16x32_bf16 v[72:75], v[186:189], v[214:217], v[72:75]
	v_mfma_f32_16x16x32_bf16 v[68:71], v[178:181], v[226:229], v[68:71]
	v_mfma_f32_16x16x32_bf16 v[64:67], v[186:189], v[226:229], v[64:67]
	s_setprio 0
	s_barrier
	s_add_i32 s36, s65, s46
	v_lshl_add_u64 v[158:159], v[158:159], 0, s[54:55]
	s_mov_b32 m0, s36
	ds_read_b128 v[190:193], v145 offset:49152
	ds_read_b128 v[194:197], v145 offset:51200
	ds_read_b128 v[198:201], v146 offset:49152
	ds_read_b128 v[202:205], v146 offset:51200
	ds_read_b128 v[206:209], v145 offset:53248
	ds_read_b128 v[210:213], v145 offset:55296
	ds_read_b128 v[214:217], v146 offset:53248
	ds_read_b128 v[226:229], v146 offset:55296
	global_load_lds_dwordx4 v[158:159], off
	s_add_i32 m0, s36, 0x2000
	s_add_u32 s34, s34, 0x80080
	v_lshl_add_u64 v[158:159], v[162:163], 0, s[54:55]
	s_addc_u32 s35, s35, 0
	s_add_i32 s36, s89, s46
	global_load_lds_dwordx4 v[158:159], off
	v_lshl_add_u64 v[158:159], s[34:35], 0, v[132:133]
	s_mov_b32 m0, s36
	s_nop 0
	global_load_lds_dwordx4 v[158:159], off
	v_lshl_add_u64 v[158:159], s[34:35], 0, v[128:129]
	s_add_i32 m0, s36, 0x2000
	s_nop 0
	global_load_lds_dwordx4 v[158:159], off
	v_lshl_add_u64 v[158:159], v[218:219], 0, s[54:55]
	s_mov_b32 m0, s59
	s_nop 0
	global_load_lds_dwordx4 v[158:159], off
	v_lshl_add_u64 v[158:159], v[230:231], 0, s[54:55]
	s_mov_b32 m0, s69
	s_nop 0
	global_load_lds_dwordx4 v[158:159], off
	s_waitcnt vmcnt(8)
	s_waitcnt lgkmcnt(0)
	s_barrier
	s_setprio 1
	s_waitcnt lgkmcnt(0)
	v_mfma_f32_16x16x32_bf16 v[60:63], v[150:153], v[190:193], v[60:63]
	v_mfma_f32_16x16x32_bf16 v[56:59], v[166:169], v[190:193], v[56:59]
	v_mfma_f32_16x16x32_bf16 v[52:55], v[150:153], v[194:197], v[52:55]
	v_mfma_f32_16x16x32_bf16 v[44:47], v[166:169], v[194:197], v[44:47]
	v_mfma_f32_16x16x32_bf16 v[36:39], v[150:153], v[206:209], v[36:39]
	v_mfma_f32_16x16x32_bf16 v[28:31], v[166:169], v[206:209], v[28:31]
	v_mfma_f32_16x16x32_bf16 v[20:23], v[150:153], v[210:213], v[20:23]
	v_mfma_f32_16x16x32_bf16 v[12:15], v[166:169], v[210:213], v[12:15]
	v_mfma_f32_16x16x32_bf16 v[60:63], v[154:157], v[198:201], v[60:63]
	v_mfma_f32_16x16x32_bf16 v[56:59], v[170:173], v[198:201], v[56:59]
	v_mfma_f32_16x16x32_bf16 v[52:55], v[154:157], v[202:205], v[52:55]
	v_mfma_f32_16x16x32_bf16 v[44:47], v[170:173], v[202:205], v[44:47]
	v_mfma_f32_16x16x32_bf16 v[36:39], v[154:157], v[214:217], v[36:39]
	v_mfma_f32_16x16x32_bf16 v[28:31], v[170:173], v[214:217], v[28:31]
	v_mfma_f32_16x16x32_bf16 v[20:23], v[154:157], v[226:229], v[20:23]
	v_mfma_f32_16x16x32_bf16 v[12:15], v[170:173], v[226:229], v[12:15]
	s_setprio 0
	s_setprio 1
	v_mfma_f32_16x16x32_bf16 v[48:51], v[174:177], v[190:193], v[48:51]
	v_mfma_f32_16x16x32_bf16 v[40:43], v[182:185], v[190:193], v[40:43]
	v_mfma_f32_16x16x32_bf16 v[32:35], v[174:177], v[194:197], v[32:35]
	v_mfma_f32_16x16x32_bf16 v[24:27], v[182:185], v[194:197], v[24:27]
	v_mfma_f32_16x16x32_bf16 v[16:19], v[174:177], v[206:209], v[16:19]
	v_mfma_f32_16x16x32_bf16 v[8:11], v[182:185], v[206:209], v[8:11]
	v_mfma_f32_16x16x32_bf16 v[4:7], v[174:177], v[210:213], v[4:7]
	v_mfma_f32_16x16x32_bf16 v[0:3], v[182:185], v[210:213], v[0:3]
	v_mfma_f32_16x16x32_bf16 v[48:51], v[178:181], v[198:201], v[48:51]
	v_mfma_f32_16x16x32_bf16 v[40:43], v[186:189], v[198:201], v[40:43]
	v_mfma_f32_16x16x32_bf16 v[32:35], v[178:181], v[202:205], v[32:35]
	v_mfma_f32_16x16x32_bf16 v[24:27], v[186:189], v[202:205], v[24:27]
	v_mfma_f32_16x16x32_bf16 v[16:19], v[178:181], v[214:217], v[16:19]
	v_mfma_f32_16x16x32_bf16 v[8:11], v[186:189], v[214:217], v[8:11]
	v_mfma_f32_16x16x32_bf16 v[4:7], v[178:181], v[226:229], v[4:7]
	v_mfma_f32_16x16x32_bf16 v[0:3], v[186:189], v[226:229], v[0:3]
	s_setprio 0
	s_barrier
	s_add_i32 s88, s88, 2
	s_add_u32 s30, s30, 0x100
	s_addc_u32 s31, s31, 0
	s_add_u32 s77, s77, 0x100
	s_addc_u32 s84, s84, 0
	s_cmpk_gt_u32 s88, 0x7d
	s_cbranch_scc0 .LBB0_1091
	s_mov_b32 s100, 1
	s_and_b64 vcc, exec, s[8:9]
	s_cbranch_vccz .LBB0_1094
	s_barrier
